# stacked: v59 plus all s_setprio flips removed plus LDS-DMA saddr address form (98 64-bit adds removed)
# speedup vs baseline: 1.0083x; 1.0045x over previous
; #define PG8_STAGE(bufoff, gbase, voff) do { _Pragma("unroll") for (int _i = 0; _i < 2; ++_i) \
;         __builtin_amdgcn_global_load_lds((const unsigned*)((const char*)(gbase) + (voff)[_i]), (PG8_LAS unsigned*)(lds + (bufoff) + ldsw + _i * 8192), 16, 0, 0); } while (0)
; #define PG8_LDA(dst, b, h) do { _Pragma("unroll") for (int m = 0; m < 4; ++m) _Pragma("unroll") for (int k = 0; k < 2; ++k) dst[m][k] = *(const PG8_LAS bf16x8*)(lds + PG8_SA(b, h) + aoff + m * 2048 + k * 1024); } while (0)
; #define PG8_LDB(dst, b, h) do { _Pragma("unroll") for (int n = 0; n < 2; ++n) _Pragma("unroll") for (int k = 0; k < 2; ++k) dst[n][k] = *(const PG8_LAS bf16x8*)(lds + PG8_SB(b, h) + boff + n * 2048 + k * 1024); } while (0)
; #define PG8_WAIT_V(n) asm volatile("s_waitcnt vmcnt(" #n ")" ::: "memory")
; #define PG8_WAIT_V8_UNLESS_FIRST(t) asm volatile("s_cmp_eq_u32 %0, 0\n\ts_cbranch_scc1 .Lpg8skip%=\n\ts_waitcnt vmcnt(8)\n.Lpg8skip%=:" :: "s"(t) : "scc", "memory")
; #define PG8_WAIT_L(n) asm volatile("s_waitcnt lgkmcnt(" #n ")" ::: "memory")
; #define PG8_BAR __builtin_amdgcn_s_barrier()
; template <class Epi, class Sched, bool ALIGN_EPI = false, bool SP2 = false, bool FP8 = false, bool ABLK = false>
; __device__ __forceinline__ void gemm_phase(PG8_LAS unsigned char* lds, const Gemm g, const Sched& S, const Epi& E) {
;     ...
;             PG8_LDB(B0, 0, 0); PG8_LDB(B1, 0, 1); PG8_SCHED; PG8_LDA(At, 0, 0); PG8_STAGE(PG8_SA(1, 1), a1 + hstepA, voffA);
;             PG8_WAIT_V8_UNLESS_FIRST(t); PG8_WAIT_L(0); PG8_BAR; PG8_MMA(0, 0, At, B0); PG8_MMA(0, 1, At, B1); PG8_BAR; PG8_SCHED;
;             PG8_LDA(At, 0, 1); PG8_STAGE(PG8_SB(0, 0), b2, voffB); PG8_STAGE(PG8_SB(0, 1), b2 + hstep, voffB); PG8_STAGE(PG8_SA(0, 0), a2, voffA);
;             PG8_WAIT_V8_UNLESS_FIRST(t); PG8_WAIT_L(0); PG8_BAR; PG8_MMA(1, 0, At, B0); PG8_MMA(1, 1, At, B1); PG8_BAR; PG8_SCHED;
;             PG8_LDB(B0, 1, 0); PG8_LDB(B1, 1, 1); PG8_SCHED; PG8_LDA(At, 1, 0); PG8_STAGE(PG8_SA(0, 1), a2 + hstepA, voffA);
;             PG8_WAIT_V(8); PG8_WAIT_L(0); PG8_BAR; PG8_MMA(0, 0, At, B0); PG8_MMA(0, 1, At, B1); PG8_BAR; PG8_SCHED;
;             PG8_LDA(At, 1, 1); PG8_STAGE(PG8_SB(1, 0), b3, voffB); PG8_STAGE(PG8_SB(1, 1), b3 + hstep, voffB); PG8_STAGE(PG8_SA(1, 0), a3, voffA);
;             PG8_WAIT_V(8); PG8_WAIT_L(0); PG8_BAR; PG8_MMA(1, 0, At, B0); PG8_MMA(1, 1, At, B1); PG8_BAR; PG8_SCHED;
.Lpg8skip0:
	s_waitcnt lgkmcnt(0)
	s_barrier
	s_waitcnt lgkmcnt(0)
	v_mfma_f32_16x16x32_bf16 v[128:131], v[132:135], v[180:183], v[128:131]
	v_mfma_f32_16x16x32_bf16 v[124:127], v[140:143], v[180:183], v[124:127]
	v_mfma_f32_16x16x32_bf16 v[112:115], v[132:135], v[188:191], v[112:115]
	v_mfma_f32_16x16x32_bf16 v[108:111], v[140:143], v[188:191], v[108:111]
	v_mfma_f32_16x16x32_bf16 v[96:99], v[132:135], v[208:211], v[96:99]
	v_mfma_f32_16x16x32_bf16 v[92:95], v[140:143], v[208:211], v[92:95]
	v_mfma_f32_16x16x32_bf16 v[80:83], v[132:135], v[216:219], v[80:83]
	v_mfma_f32_16x16x32_bf16 v[76:79], v[140:143], v[216:219], v[76:79]
	v_mfma_f32_16x16x32_bf16 v[128:131], v[136:139], v[184:187], v[128:131]
	v_mfma_f32_16x16x32_bf16 v[124:127], v[144:147], v[184:187], v[124:127]
	v_mfma_f32_16x16x32_bf16 v[112:115], v[136:139], v[192:195], v[112:115]
	v_mfma_f32_16x16x32_bf16 v[108:111], v[144:147], v[192:195], v[108:111]
	v_mfma_f32_16x16x32_bf16 v[96:99], v[136:139], v[212:215], v[96:99]
	v_mfma_f32_16x16x32_bf16 v[92:95], v[144:147], v[212:215], v[92:95]
	v_mfma_f32_16x16x32_bf16 v[80:83], v[136:139], v[220:223], v[80:83]
	v_mfma_f32_16x16x32_bf16 v[76:79], v[144:147], v[220:223], v[76:79]
	v_mfma_f32_16x16x32_bf16 v[120:123], v[148:151], v[180:183], v[120:123]
	v_mfma_f32_16x16x32_bf16 v[116:119], v[172:175], v[180:183], v[116:119]
	v_mfma_f32_16x16x32_bf16 v[104:107], v[148:151], v[188:191], v[104:107]
	v_mfma_f32_16x16x32_bf16 v[100:103], v[172:175], v[188:191], v[100:103]
	v_mfma_f32_16x16x32_bf16 v[88:91], v[148:151], v[208:211], v[88:91]
	v_mfma_f32_16x16x32_bf16 v[84:87], v[172:175], v[208:211], v[84:87]
	v_mfma_f32_16x16x32_bf16 v[72:75], v[148:151], v[216:219], v[72:75]
	v_mfma_f32_16x16x32_bf16 v[68:71], v[172:175], v[216:219], v[68:71]
	v_mfma_f32_16x16x32_bf16 v[120:123], v[168:171], v[184:187], v[120:123]
	v_mfma_f32_16x16x32_bf16 v[116:119], v[176:179], v[184:187], v[116:119]
	v_mfma_f32_16x16x32_bf16 v[104:107], v[168:171], v[192:195], v[104:107]
	v_mfma_f32_16x16x32_bf16 v[100:103], v[176:179], v[192:195], v[100:103]
	v_mfma_f32_16x16x32_bf16 v[88:91], v[168:171], v[212:215], v[88:91]
	v_mfma_f32_16x16x32_bf16 v[84:87], v[176:179], v[212:215], v[84:87]
	v_mfma_f32_16x16x32_bf16 v[72:75], v[168:171], v[220:223], v[72:75]
	v_mfma_f32_16x16x32_bf16 v[68:71], v[176:179], v[220:223], v[68:71]
	s_barrier
	s_add_i32 s75, s75, s17
	v_lshl_add_u64 v[162:163], s[62:63], 0, v[2:3]
	s_mov_b32 m0, s75
	ds_read_b128 v[180:183], v166 offset:16384
	ds_read_b128 v[184:187], v166 offset:17408
	ds_read_b128 v[188:191], v166 offset:18432
	ds_read_b128 v[192:195], v166 offset:19456
	ds_read_b128 v[208:211], v166 offset:20480
	ds_read_b128 v[212:215], v166 offset:21504
	ds_read_b128 v[216:219], v166 offset:22528
	ds_read_b128 v[220:223], v166 offset:23552
	global_load_lds_dwordx4 v2, s[62:63]
	s_add_i32 m0, s75, 0x2000
	s_add_u32 s76, s62, 0x40000
	v_lshl_add_u64 v[224:225], s[62:63], 0, v[152:153]
	s_addc_u32 s77, s63, 0
	s_add_i32 s75, s81, s17
	global_load_lds_dwordx4 v152, s[62:63]
	s_mov_b32 m0, s75
	v_lshl_add_u64 v[230:231], s[64:65], 0, v[154:155]
	global_load_lds_dwordx4 v2, s[76:77]
	s_add_i32 m0, s75, 0x2000
	s_nop 0
	global_load_lds_dwordx4 v152, s[76:77]
	v_lshl_add_u64 v[228:229], s[64:65], 0, v[156:157]
	s_mov_b32 m0, s18
	s_nop 0
	global_load_lds_dwordx4 v156, s[64:65]
	s_mov_b32 m0, s19
	s_nop 0
	global_load_lds_dwordx4 v154, s[64:65]
	s_cmp_eq_u32 s74, 0
	s_cbranch_scc1 .Lpg8skip1
	s_waitcnt vmcnt(8)
.Lpg8skip1:
	s_waitcnt lgkmcnt(0)
	s_barrier
	s_waitcnt lgkmcnt(0)
	v_mfma_f32_16x16x32_bf16 v[64:67], v[132:135], v[180:183], v[64:67]
	v_mfma_f32_16x16x32_bf16 v[60:63], v[140:143], v[180:183], v[60:63]
	v_mfma_f32_16x16x32_bf16 v[48:51], v[132:135], v[188:191], v[48:51]
	v_mfma_f32_16x16x32_bf16 v[44:47], v[140:143], v[188:191], v[44:47]
	v_mfma_f32_16x16x32_bf16 v[32:35], v[132:135], v[208:211], v[32:35]
	v_mfma_f32_16x16x32_bf16 v[28:31], v[140:143], v[208:211], v[28:31]
	v_mfma_f32_16x16x32_bf16 v[16:19], v[132:135], v[216:219], v[16:19]
	v_mfma_f32_16x16x32_bf16 v[12:15], v[140:143], v[216:219], v[12:15]
	v_mfma_f32_16x16x32_bf16 v[64:67], v[136:139], v[184:187], v[64:67]
	v_mfma_f32_16x16x32_bf16 v[60:63], v[144:147], v[184:187], v[60:63]
	v_mfma_f32_16x16x32_bf16 v[48:51], v[136:139], v[192:195], v[48:51]
	v_mfma_f32_16x16x32_bf16 v[44:47], v[144:147], v[192:195], v[44:47]
	v_mfma_f32_16x16x32_bf16 v[32:35], v[136:139], v[212:215], v[32:35]
	v_mfma_f32_16x16x32_bf16 v[28:31], v[144:147], v[212:215], v[28:31]
	v_mfma_f32_16x16x32_bf16 v[16:19], v[136:139], v[220:223], v[16:19]
	v_mfma_f32_16x16x32_bf16 v[12:15], v[144:147], v[220:223], v[12:15]
	v_mfma_f32_16x16x32_bf16 v[56:59], v[148:151], v[180:183], v[56:59]
	v_mfma_f32_16x16x32_bf16 v[52:55], v[172:175], v[180:183], v[52:55]
	v_mfma_f32_16x16x32_bf16 v[40:43], v[148:151], v[188:191], v[40:43]
	v_mfma_f32_16x16x32_bf16 v[36:39], v[172:175], v[188:191], v[36:39]
	v_mfma_f32_16x16x32_bf16 v[24:27], v[148:151], v[208:211], v[24:27]
	v_mfma_f32_16x16x32_bf16 v[20:23], v[172:175], v[208:211], v[20:23]
	v_mfma_f32_16x16x32_bf16 v[8:11], v[148:151], v[216:219], v[8:11]
	v_mfma_f32_16x16x32_bf16 v[4:7], v[172:175], v[216:219], v[4:7]
	v_mfma_f32_16x16x32_bf16 v[56:59], v[168:171], v[184:187], v[56:59]
	v_mfma_f32_16x16x32_bf16 v[52:55], v[176:179], v[184:187], v[52:55]
	v_mfma_f32_16x16x32_bf16 v[40:43], v[168:171], v[192:195], v[40:43]
	v_mfma_f32_16x16x32_bf16 v[36:39], v[176:179], v[192:195], v[36:39]
	v_mfma_f32_16x16x32_bf16 v[24:27], v[168:171], v[212:215], v[24:27]
	v_mfma_f32_16x16x32_bf16 v[20:23], v[176:179], v[212:215], v[20:23]
	v_mfma_f32_16x16x32_bf16 v[8:11], v[168:171], v[220:223], v[8:11]
	v_mfma_f32_16x16x32_bf16 v[4:7], v[176:179], v[220:223], v[4:7]
	s_barrier
; #define PG8_BAR __builtin_amdgcn_s_barrier()
; template <class Epi, class Sched, bool ALIGN_EPI = false, bool SP2 = false, bool FP8 = false, bool ABLK = false>
; __device__ __forceinline__ void gemm_phase(PG8_LAS unsigned char* lds, const Gemm g, const Sched& S, const Epi& E) {
;     ...
;             PG8_LDB(B0, 0, 0); PG8_LDB(B1, 0, 1); PG8_SCHED; PG8_LDA(At, 0, 0); PG8_STAGE(PG8_SA(1, 1), a1 + hstepA, voffA);
;             PG8_WAIT_V8_UNLESS_FIRST(t); PG8_WAIT_L(0); PG8_BAR; PG8_MMA(0, 0, At, B0); PG8_MMA(0, 1, At, B1); PG8_BAR; PG8_SCHED;
;             PG8_LDA(At, 0, 1); PG8_STAGE(PG8_SB(0, 0), b2, voffB); PG8_STAGE(PG8_SB(0, 1), b2 + hstep, voffB); PG8_STAGE(PG8_SA(0, 0), a2, voffA);
;             PG8_WAIT_V8_UNLESS_FIRST(t); PG8_WAIT_L(0); PG8_BAR; PG8_MMA(1, 0, At, B0); PG8_MMA(1, 1, At, B1); PG8_BAR; PG8_SCHED;
;             PG8_LDB(B0, 1, 0); PG8_LDB(B1, 1, 1); PG8_SCHED; PG8_LDA(At, 1, 0); PG8_STAGE(PG8_SA(0, 1), a2 + hstepA, voffA);
;             PG8_WAIT_V(8); PG8_WAIT_L(0); PG8_BAR; PG8_MMA(0, 0, At, B0); PG8_MMA(0, 1, At, B1); PG8_BAR; PG8_SCHED;
;             PG8_LDA(At, 1, 1); PG8_STAGE(PG8_SB(1, 0), b3, voffB); PG8_STAGE(PG8_SB(1, 1), b3 + hstep, voffB); PG8_STAGE(PG8_SA(1, 0), a3, voffA);
;             PG8_WAIT_V(8); PG8_WAIT_L(0); PG8_BAR; PG8_MMA(1, 0, At, B0); PG8_MMA(1, 1, At, B1); PG8_BAR; PG8_SCHED;
;             } else {
;             PG8_LDB(B0, 0, 0); PG8_SCHED; PG8_LDA(At, 0, 0); PG8_STAGE(PG8_SA(1, 1), a1 + hstepA, voffA);
;             PG8_WAIT_L(8); PG8_BAR; PG8_WAIT_L(0); PG8_MMA(0, 0, At, B0); PG8_BAR; PG8_SCHED;
;             PG8_LDB(B1, 0, 1); PG8_STAGE(PG8_SB(0, 0), b2, voffB);
;             PG8_BAR; PG8_WAIT_L(0); PG8_MMA(0, 1, At, B1); PG8_BAR;
;             PG8_LDA(At, 0, 1); PG8_STAGE(PG8_SA(0, 0), a2, voffA);
;             PG8_BAR; PG8_WAIT_L(0); PG8_MMA(1, 0, At, B0); PG8_BAR; PG8_SCHED;
;             PG8_STAGE(PG8_SB(0, 1), b2 + hstep, voffB);
;             PG8_WAIT_V(6); PG8_BAR; PG8_MMA(1, 1, At, B1); PG8_BAR;
;             PG8_LDB(B0, 1, 0); PG8_SCHED; PG8_LDA(At, 1, 0); PG8_STAGE(PG8_SA(0, 1), a2 + hstepA, voffA);
;             PG8_WAIT_L(8); PG8_BAR; PG8_WAIT_L(0); PG8_MMA(0, 0, At, B0); PG8_BAR; PG8_SCHED;
;             PG8_LDB(B1, 1, 1); PG8_STAGE(PG8_SB(1, 0), b3, voffB);
;             PG8_BAR; PG8_WAIT_L(0); PG8_MMA(0, 1, At, B1); PG8_BAR;
;             PG8_LDA(At, 1, 1); PG8_STAGE(PG8_SA(1, 0), a3, voffA);
	s_add_i32 s75, 0, 0x18000
	s_add_i32 s76, 0, 0x1c000
	v_add_u32_e32 v144, s75, v165
	v_add_u32_e32 v167, s76, v165
	ds_read_b128 v[132:135], v144
	ds_read_b128 v[136:139], v144 offset:1024
	ds_read_b128 v[140:143], v144 offset:2048
	ds_read_b128 v[144:147], v144 offset:3072
	ds_read_b128 v[148:151], v167
	ds_read_b128 v[168:171], v167 offset:1024
	ds_read_b128 v[172:175], v167 offset:2048
	ds_read_b128 v[176:179], v167 offset:3072
	s_add_u32 s64, s64, 0x40000
	s_addc_u32 s65, s65, 0
	s_mov_b32 m0, s20
	ds_read_b128 v[180:183], v166 offset:32768
	ds_read_b128 v[184:187], v166 offset:33792
	ds_read_b128 v[188:191], v166 offset:34816
	ds_read_b128 v[192:195], v166 offset:35840
	ds_read_b128 v[208:211], v166 offset:36864
	ds_read_b128 v[212:215], v166 offset:37888
	ds_read_b128 v[216:219], v166 offset:38912
	ds_read_b128 v[220:223], v166 offset:39936
	global_load_lds_dwordx4 v156, s[64:65]
	s_mov_b32 m0, s21
	s_nop 0
	global_load_lds_dwordx4 v154, s[64:65]
	s_waitcnt vmcnt(8)
	s_waitcnt lgkmcnt(0)
	s_barrier
	s_waitcnt lgkmcnt(0)
	v_mfma_f32_16x16x32_bf16 v[128:131], v[132:135], v[180:183], v[128:131]
	v_mfma_f32_16x16x32_bf16 v[124:127], v[140:143], v[180:183], v[124:127]
	v_mfma_f32_16x16x32_bf16 v[112:115], v[132:135], v[188:191], v[112:115]
	v_mfma_f32_16x16x32_bf16 v[108:111], v[140:143], v[188:191], v[108:111]
	v_mfma_f32_16x16x32_bf16 v[96:99], v[132:135], v[208:211], v[96:99]
	v_mfma_f32_16x16x32_bf16 v[92:95], v[140:143], v[208:211], v[92:95]
	v_mfma_f32_16x16x32_bf16 v[80:83], v[132:135], v[216:219], v[80:83]
	v_mfma_f32_16x16x32_bf16 v[76:79], v[140:143], v[216:219], v[76:79]
	v_mfma_f32_16x16x32_bf16 v[128:131], v[136:139], v[184:187], v[128:131]
	v_mfma_f32_16x16x32_bf16 v[124:127], v[144:147], v[184:187], v[124:127]
	v_mfma_f32_16x16x32_bf16 v[112:115], v[136:139], v[192:195], v[112:115]
	v_mfma_f32_16x16x32_bf16 v[108:111], v[144:147], v[192:195], v[108:111]
	v_mfma_f32_16x16x32_bf16 v[96:99], v[136:139], v[212:215], v[96:99]
	v_mfma_f32_16x16x32_bf16 v[92:95], v[144:147], v[212:215], v[92:95]
	v_mfma_f32_16x16x32_bf16 v[80:83], v[136:139], v[220:223], v[80:83]
	v_mfma_f32_16x16x32_bf16 v[76:79], v[144:147], v[220:223], v[76:79]
	v_mfma_f32_16x16x32_bf16 v[120:123], v[148:151], v[180:183], v[120:123]
	v_mfma_f32_16x16x32_bf16 v[116:119], v[172:175], v[180:183], v[116:119]
	v_mfma_f32_16x16x32_bf16 v[104:107], v[148:151], v[188:191], v[104:107]
	v_mfma_f32_16x16x32_bf16 v[100:103], v[172:175], v[188:191], v[100:103]
	v_mfma_f32_16x16x32_bf16 v[88:91], v[148:151], v[208:211], v[88:91]
	v_mfma_f32_16x16x32_bf16 v[84:87], v[172:175], v[208:211], v[84:87]
	v_mfma_f32_16x16x32_bf16 v[72:75], v[148:151], v[216:219], v[72:75]
	v_mfma_f32_16x16x32_bf16 v[68:71], v[172:175], v[216:219], v[68:71]
	v_mfma_f32_16x16x32_bf16 v[120:123], v[168:171], v[184:187], v[120:123]
	v_mfma_f32_16x16x32_bf16 v[116:119], v[176:179], v[184:187], v[116:119]
	v_mfma_f32_16x16x32_bf16 v[104:107], v[168:171], v[192:195], v[104:107]
	v_mfma_f32_16x16x32_bf16 v[100:103], v[176:179], v[192:195], v[100:103]
	v_mfma_f32_16x16x32_bf16 v[88:91], v[168:171], v[212:215], v[88:91]
	v_mfma_f32_16x16x32_bf16 v[84:87], v[176:179], v[212:215], v[84:87]
	v_mfma_f32_16x16x32_bf16 v[72:75], v[168:171], v[220:223], v[72:75]
	v_mfma_f32_16x16x32_bf16 v[68:71], v[176:179], v[220:223], v[68:71]
	s_barrier
	s_add_i32 s64, s75, s17
	v_lshl_add_u64 v[162:163], v[162:163], 0, s[34:35]
	s_mov_b32 m0, s64
	ds_read_b128 v[180:183], v166 offset:49152
	ds_read_b128 v[184:187], v166 offset:50176
	ds_read_b128 v[188:191], v166 offset:51200
	ds_read_b128 v[192:195], v166 offset:52224
	ds_read_b128 v[208:211], v166 offset:53248
	ds_read_b128 v[212:215], v166 offset:54272
	ds_read_b128 v[216:219], v166 offset:55296
	ds_read_b128 v[220:223], v166 offset:56320
	global_load_lds_dwordx4 v[162:163], off
	s_add_i32 m0, s64, 0x2000
	s_add_u32 s62, s62, 0x40080
	v_lshl_add_u64 v[162:163], v[224:225], 0, s[34:35]
	s_addc_u32 s63, s63, 0
	s_add_i32 s64, s76, s17
	global_load_lds_dwordx4 v[162:163], off
	s_mov_b32 m0, s64
	s_nop 0
	global_load_lds_dwordx4 v2, s[62:63]
	s_add_i32 m0, s64, 0x2000
	s_nop 0
	global_load_lds_dwordx4 v152, s[62:63]
	v_lshl_add_u64 v[162:163], v[228:229], 0, s[34:35]
	s_mov_b32 m0, s66
	s_nop 0
	global_load_lds_dwordx4 v[162:163], off
	v_lshl_add_u64 v[162:163], v[230:231], 0, s[34:35]
	s_mov_b32 m0, s67
	s_nop 0
	global_load_lds_dwordx4 v[162:163], off
	s_waitcnt vmcnt(8)
	s_waitcnt lgkmcnt(0)
	s_barrier
	s_waitcnt lgkmcnt(0)
	v_mfma_f32_16x16x32_bf16 v[64:67], v[132:135], v[180:183], v[64:67]
	v_mfma_f32_16x16x32_bf16 v[60:63], v[140:143], v[180:183], v[60:63]
	v_mfma_f32_16x16x32_bf16 v[48:51], v[132:135], v[188:191], v[48:51]
	v_mfma_f32_16x16x32_bf16 v[44:47], v[140:143], v[188:191], v[44:47]
	v_mfma_f32_16x16x32_bf16 v[32:35], v[132:135], v[208:211], v[32:35]
	v_mfma_f32_16x16x32_bf16 v[28:31], v[140:143], v[208:211], v[28:31]
	v_mfma_f32_16x16x32_bf16 v[16:19], v[132:135], v[216:219], v[16:19]
	v_mfma_f32_16x16x32_bf16 v[12:15], v[140:143], v[216:219], v[12:15]
	v_mfma_f32_16x16x32_bf16 v[64:67], v[136:139], v[184:187], v[64:67]
	v_mfma_f32_16x16x32_bf16 v[60:63], v[144:147], v[184:187], v[60:63]
	v_mfma_f32_16x16x32_bf16 v[48:51], v[136:139], v[192:195], v[48:51]
	v_mfma_f32_16x16x32_bf16 v[44:47], v[144:147], v[192:195], v[44:47]
	v_mfma_f32_16x16x32_bf16 v[32:35], v[136:139], v[212:215], v[32:35]
	v_mfma_f32_16x16x32_bf16 v[28:31], v[144:147], v[212:215], v[28:31]
	v_mfma_f32_16x16x32_bf16 v[16:19], v[136:139], v[220:223], v[16:19]
	v_mfma_f32_16x16x32_bf16 v[12:15], v[144:147], v[220:223], v[12:15]
	v_mfma_f32_16x16x32_bf16 v[56:59], v[148:151], v[180:183], v[56:59]
	v_mfma_f32_16x16x32_bf16 v[52:55], v[172:175], v[180:183], v[52:55]
	v_mfma_f32_16x16x32_bf16 v[40:43], v[148:151], v[188:191], v[40:43]
	v_mfma_f32_16x16x32_bf16 v[36:39], v[172:175], v[188:191], v[36:39]
	v_mfma_f32_16x16x32_bf16 v[24:27], v[148:151], v[208:211], v[24:27]
	v_mfma_f32_16x16x32_bf16 v[20:23], v[172:175], v[208:211], v[20:23]
	v_mfma_f32_16x16x32_bf16 v[8:11], v[148:151], v[216:219], v[8:11]
	v_mfma_f32_16x16x32_bf16 v[4:7], v[172:175], v[216:219], v[4:7]
	v_mfma_f32_16x16x32_bf16 v[56:59], v[168:171], v[184:187], v[56:59]
	v_mfma_f32_16x16x32_bf16 v[52:55], v[176:179], v[184:187], v[52:55]
	v_mfma_f32_16x16x32_bf16 v[40:43], v[168:171], v[192:195], v[40:43]
	v_mfma_f32_16x16x32_bf16 v[36:39], v[176:179], v[192:195], v[36:39]
	v_mfma_f32_16x16x32_bf16 v[24:27], v[168:171], v[212:215], v[24:27]
	v_mfma_f32_16x16x32_bf16 v[20:23], v[176:179], v[212:215], v[20:23]
	v_mfma_f32_16x16x32_bf16 v[8:11], v[168:171], v[220:223], v[8:11]
	v_mfma_f32_16x16x32_bf16 v[4:7], v[176:179], v[220:223], v[4:7]
	s_barrier
	s_add_u32 s60, s60, 0x100
	s_addc_u32 s61, s61, 0
	s_add_u32 s72, s72, 0x100
	s_addc_u32 s73, s73, 0
	s_cmp_gt_u32 s74, 13
	s_mov_b32 s62, s74
	s_cbranch_scc0 .LBB0_431
	s_waitcnt vmcnt(0)
	s_and_b64 vcc, exec, s[50:51]
	s_cbranch_vccz .LBB0_434
	s_barrier

; #define PG8_STAGE(bufoff, gbase, voff) do { _Pragma("unroll") for (int _i = 0; _i < 2; ++_i) \
;         __builtin_amdgcn_global_load_lds((const unsigned*)((const char*)(gbase) + (voff)[_i]), (PG8_LAS unsigned*)(lds + (bufoff) + ldsw + _i * 8192), 16, 0, 0); } while (0)
; #define PG8_LDA(dst, b, h) do { _Pragma("unroll") for (int m = 0; m < 4; ++m) _Pragma("unroll") for (int k = 0; k < 2; ++k) dst[m][k] = *(const PG8_LAS bf16x8*)(lds + PG8_SA(b, h) + aoff + m * 2048 + k * 1024); } while (0)
; #define PG8_LDB(dst, b, h) do { _Pragma("unroll") for (int n = 0; n < 2; ++n) _Pragma("unroll") for (int k = 0; k < 2; ++k) dst[n][k] = *(const PG8_LAS bf16x8*)(lds + PG8_SB(b, h) + boff + n * 2048 + k * 1024); } while (0)
; #define PG8_WAIT_V(n) asm volatile("s_waitcnt vmcnt(" #n ")" ::: "memory")
; #define PG8_WAIT_V8_UNLESS_FIRST(t) asm volatile("s_cmp_eq_u32 %0, 0\n\ts_cbranch_scc1 .Lpg8skip%=\n\ts_waitcnt vmcnt(8)\n.Lpg8skip%=:" :: "s"(t) : "scc", "memory")
; #define PG8_WAIT_L(n) asm volatile("s_waitcnt lgkmcnt(" #n ")" ::: "memory")
; #define PG8_BAR __builtin_amdgcn_s_barrier()
; template <class Epi, class Sched, bool ALIGN_EPI = false, bool SP2 = false, bool FP8 = false, bool ABLK = false>
; __device__ __forceinline__ void gemm_phase(PG8_LAS unsigned char* lds, const Gemm g, const Sched& S, const Epi& E) {
;     ...
;             PG8_LDB(B0, 0, 0); PG8_LDB(B1, 0, 1); PG8_SCHED; PG8_LDA(At, 0, 0); PG8_STAGE(PG8_SA(1, 1), a1 + hstepA, voffA);
;             PG8_WAIT_V8_UNLESS_FIRST(t); PG8_WAIT_L(0); PG8_BAR; PG8_MMA(0, 0, At, B0); PG8_MMA(0, 1, At, B1); PG8_BAR; PG8_SCHED;
;             PG8_LDA(At, 0, 1); PG8_STAGE(PG8_SB(0, 0), b2, voffB); PG8_STAGE(PG8_SB(0, 1), b2 + hstep, voffB); PG8_STAGE(PG8_SA(0, 0), a2, voffA);
;             PG8_WAIT_V8_UNLESS_FIRST(t); PG8_WAIT_L(0); PG8_BAR; PG8_MMA(1, 0, At, B0); PG8_MMA(1, 1, At, B1); PG8_BAR; PG8_SCHED;
;             PG8_LDB(B0, 1, 0); PG8_LDB(B1, 1, 1); PG8_SCHED; PG8_LDA(At, 1, 0); PG8_STAGE(PG8_SA(0, 1), a2 + hstepA, voffA);
;             PG8_WAIT_V(8); PG8_WAIT_L(0); PG8_BAR; PG8_MMA(0, 0, At, B0); PG8_MMA(0, 1, At, B1); PG8_BAR; PG8_SCHED;
;             PG8_LDA(At, 1, 1); PG8_STAGE(PG8_SB(1, 0), b3, voffB); PG8_STAGE(PG8_SB(1, 1), b3 + hstep, voffB); PG8_STAGE(PG8_SA(1, 0), a3, voffA);
;             PG8_WAIT_V(8); PG8_WAIT_L(0); PG8_BAR; PG8_MMA(1, 0, At, B0); PG8_MMA(1, 1, At, B1); PG8_BAR; PG8_SCHED;
.Lpg8skip2:
	s_waitcnt lgkmcnt(0)
	s_barrier
	s_waitcnt lgkmcnt(0)
	v_mfma_scale_f32_16x16x128_f8f6f4 v[160:163], v[28:35], v[186:193], v[160:163], v245, v245 op_sel_hi:[0,0,0]
	v_mfma_scale_f32_16x16x128_f8f6f4 v[156:159], v[20:27], v[186:193], v[156:159], v245, v245 op_sel_hi:[0,0,0]
	v_mfma_scale_f32_16x16x128_f8f6f4 v[144:147], v[28:35], v[208:215], v[144:147], v245, v245 op_sel_hi:[0,0,0]
	v_mfma_scale_f32_16x16x128_f8f6f4 v[140:143], v[20:27], v[208:215], v[140:143], v245, v245 op_sel_hi:[0,0,0]
	v_mfma_scale_f32_16x16x128_f8f6f4 v[128:131], v[28:35], v[216:223], v[128:131], v245, v245 op_sel_hi:[0,0,0]
	v_mfma_scale_f32_16x16x128_f8f6f4 v[124:127], v[20:27], v[216:223], v[124:127], v245, v245 op_sel_hi:[0,0,0]
	v_mfma_scale_f32_16x16x128_f8f6f4 v[112:115], v[28:35], v[228:235], v[112:115], v245, v245 op_sel_hi:[0,0,0]
	v_mfma_scale_f32_16x16x128_f8f6f4 v[108:111], v[20:27], v[228:235], v[108:111], v245, v245 op_sel_hi:[0,0,0]
	v_mfma_scale_f32_16x16x128_f8f6f4 v[152:155], v[12:19], v[186:193], v[152:155], v245, v245 op_sel_hi:[0,0,0]
	v_mfma_scale_f32_16x16x128_f8f6f4 v[148:151], v[4:11], v[186:193], v[148:151], v245, v245 op_sel_hi:[0,0,0]
	v_mfma_scale_f32_16x16x128_f8f6f4 v[136:139], v[12:19], v[208:215], v[136:139], v245, v245 op_sel_hi:[0,0,0]
	v_mfma_scale_f32_16x16x128_f8f6f4 v[132:135], v[4:11], v[208:215], v[132:135], v245, v245 op_sel_hi:[0,0,0]
	v_mfma_scale_f32_16x16x128_f8f6f4 v[120:123], v[12:19], v[216:223], v[120:123], v245, v245 op_sel_hi:[0,0,0]
	v_mfma_scale_f32_16x16x128_f8f6f4 v[116:119], v[4:11], v[216:223], v[116:119], v245, v245 op_sel_hi:[0,0,0]
	v_mfma_scale_f32_16x16x128_f8f6f4 v[104:107], v[12:19], v[228:235], v[104:107], v245, v245 op_sel_hi:[0,0,0]
	v_mfma_scale_f32_16x16x128_f8f6f4 v[100:103], v[4:11], v[228:235], v[100:103], v245, v245 op_sel_hi:[0,0,0]
	s_barrier
	s_add_i32 s73, s73, s17
	v_lshl_add_u64 v[178:179], s[60:61], 0, v[2:3]
	s_mov_b32 m0, s73
	ds_read_b128 v[186:189], v184 offset:16384
	ds_read_b128 v[190:193], v184 offset:17408
	ds_read_b128 v[208:211], v184 offset:18432
	ds_read_b128 v[212:215], v184 offset:19456
	ds_read_b128 v[216:219], v184 offset:20480
	ds_read_b128 v[220:223], v184 offset:21504
	ds_read_b128 v[228:231], v184 offset:22528
	ds_read_b128 v[232:235], v184 offset:23552
	global_load_lds_dwordx4 v2, s[60:61]
	s_add_i32 m0, s73, 0x2000
	s_add_u32 s74, s60, 0x58000
	v_lshl_add_u64 v[180:181], s[60:61], 0, v[164:165]
	s_addc_u32 s75, s61, 0
	s_add_i32 s72, s72, s17
	global_load_lds_dwordx4 v164, s[60:61]
	s_mov_b32 m0, s72
	v_lshl_add_u64 v[224:225], s[62:63], 0, v[166:167]
	global_load_lds_dwordx4 v2, s[74:75]
	s_add_i32 m0, s72, 0x2000
	s_nop 0
	global_load_lds_dwordx4 v164, s[74:75]
	v_lshl_add_u64 v[194:195], s[62:63], 0, v[168:169]
	s_mov_b32 m0, s18
	s_nop 0
	global_load_lds_dwordx4 v168, s[62:63]
	s_mov_b32 m0, s19
	s_nop 0
	global_load_lds_dwordx4 v166, s[62:63]
	s_cmp_eq_u32 s71, 0
	s_cbranch_scc1 .Lpg8skip3
	s_waitcnt vmcnt(8)
.Lpg8skip3:
	s_waitcnt lgkmcnt(0)
	s_barrier
	s_waitcnt lgkmcnt(0)
	v_mfma_scale_f32_16x16x128_f8f6f4 v[96:99], v[28:35], v[186:193], v[96:99], v245, v245 op_sel_hi:[0,0,0]
	v_mfma_scale_f32_16x16x128_f8f6f4 v[92:95], v[20:27], v[186:193], v[92:95], v245, v245 op_sel_hi:[0,0,0]
	v_mfma_scale_f32_16x16x128_f8f6f4 v[80:83], v[28:35], v[208:215], v[80:83], v245, v245 op_sel_hi:[0,0,0]
	v_mfma_scale_f32_16x16x128_f8f6f4 v[76:79], v[20:27], v[208:215], v[76:79], v245, v245 op_sel_hi:[0,0,0]
	v_mfma_scale_f32_16x16x128_f8f6f4 v[64:67], v[28:35], v[216:223], v[64:67], v245, v245 op_sel_hi:[0,0,0]
	v_mfma_scale_f32_16x16x128_f8f6f4 v[60:63], v[20:27], v[216:223], v[60:63], v245, v245 op_sel_hi:[0,0,0]
	v_mfma_scale_f32_16x16x128_f8f6f4 v[48:51], v[28:35], v[228:235], v[48:51], v245, v245 op_sel_hi:[0,0,0]
	v_mfma_scale_f32_16x16x128_f8f6f4 v[44:47], v[20:27], v[228:235], v[44:47], v245, v245 op_sel_hi:[0,0,0]
	v_mfma_scale_f32_16x16x128_f8f6f4 v[88:91], v[12:19], v[186:193], v[88:91], v245, v245 op_sel_hi:[0,0,0]
	v_mfma_scale_f32_16x16x128_f8f6f4 v[84:87], v[4:11], v[186:193], v[84:87], v245, v245 op_sel_hi:[0,0,0]
	v_mfma_scale_f32_16x16x128_f8f6f4 v[72:75], v[12:19], v[208:215], v[72:75], v245, v245 op_sel_hi:[0,0,0]
	v_mfma_scale_f32_16x16x128_f8f6f4 v[68:71], v[4:11], v[208:215], v[68:71], v245, v245 op_sel_hi:[0,0,0]
	v_mfma_scale_f32_16x16x128_f8f6f4 v[56:59], v[12:19], v[216:223], v[56:59], v245, v245 op_sel_hi:[0,0,0]
	v_mfma_scale_f32_16x16x128_f8f6f4 v[52:55], v[4:11], v[216:223], v[52:55], v245, v245 op_sel_hi:[0,0,0]
	v_mfma_scale_f32_16x16x128_f8f6f4 v[40:43], v[12:19], v[228:235], v[40:43], v245, v245 op_sel_hi:[0,0,0]
	v_mfma_scale_f32_16x16x128_f8f6f4 v[36:39], v[4:11], v[228:235], v[36:39], v245, v245 op_sel_hi:[0,0,0]
	s_barrier
	s_add_i32 s62, 0, 0x18000
	s_add_i32 s63, 0, 0x1c000
	v_add_u32_e32 v16, s62, v183
	v_add_u32_e32 v32, s63, v183
	ds_read_b128 v[4:7], v16
	ds_read_b128 v[8:11], v16 offset:1024
	ds_read_b128 v[12:15], v16 offset:2048
	ds_read_b128 v[16:19], v16 offset:3072
	ds_read_b128 v[20:23], v32
	ds_read_b128 v[24:27], v32 offset:1024
	ds_read_b128 v[28:31], v32 offset:2048
	ds_read_b128 v[32:35], v32 offset:3072
	s_mov_b32 m0, s20
	v_lshl_add_u64 v[194:195], v[194:195], 0, s[24:25]
	ds_read_b128 v[186:189], v184 offset:32768
	ds_read_b128 v[190:193], v184 offset:33792
	ds_read_b128 v[208:211], v184 offset:34816
	ds_read_b128 v[212:215], v184 offset:35840
	ds_read_b128 v[216:219], v184 offset:36864
	ds_read_b128 v[220:223], v184 offset:37888
	ds_read_b128 v[228:231], v184 offset:38912
	ds_read_b128 v[232:235], v184 offset:39936
	global_load_lds_dwordx4 v[194:195], off
	v_lshl_add_u64 v[194:195], v[224:225], 0, s[24:25]
	s_mov_b32 m0, s21
	s_nop 0
	global_load_lds_dwordx4 v[194:195], off
	s_waitcnt vmcnt(8)
	s_waitcnt lgkmcnt(0)
	s_barrier
; #define PG8_BAR __builtin_amdgcn_s_barrier()
; template <class Epi, class Sched, bool ALIGN_EPI = false, bool SP2 = false, bool FP8 = false, bool ABLK = false>
; __device__ __forceinline__ void gemm_phase(PG8_LAS unsigned char* lds, const Gemm g, const Sched& S, const Epi& E) {
;     ...
;             PG8_LDB(B0, 0, 0); PG8_LDB(B1, 0, 1); PG8_SCHED; PG8_LDA(At, 0, 0); PG8_STAGE(PG8_SA(1, 1), a1 + hstepA, voffA);
;             PG8_WAIT_V8_UNLESS_FIRST(t); PG8_WAIT_L(0); PG8_BAR; PG8_MMA(0, 0, At, B0); PG8_MMA(0, 1, At, B1); PG8_BAR; PG8_SCHED;
;             PG8_LDA(At, 0, 1); PG8_STAGE(PG8_SB(0, 0), b2, voffB); PG8_STAGE(PG8_SB(0, 1), b2 + hstep, voffB); PG8_STAGE(PG8_SA(0, 0), a2, voffA);
;             PG8_WAIT_V8_UNLESS_FIRST(t); PG8_WAIT_L(0); PG8_BAR; PG8_MMA(1, 0, At, B0); PG8_MMA(1, 1, At, B1); PG8_BAR; PG8_SCHED;
;             PG8_LDB(B0, 1, 0); PG8_LDB(B1, 1, 1); PG8_SCHED; PG8_LDA(At, 1, 0); PG8_STAGE(PG8_SA(0, 1), a2 + hstepA, voffA);
;             PG8_WAIT_V(8); PG8_WAIT_L(0); PG8_BAR; PG8_MMA(0, 0, At, B0); PG8_MMA(0, 1, At, B1); PG8_BAR; PG8_SCHED;
;             PG8_LDA(At, 1, 1); PG8_STAGE(PG8_SB(1, 0), b3, voffB); PG8_STAGE(PG8_SB(1, 1), b3 + hstep, voffB); PG8_STAGE(PG8_SA(1, 0), a3, voffA);
;             PG8_WAIT_V(8); PG8_WAIT_L(0); PG8_BAR; PG8_MMA(1, 0, At, B0); PG8_MMA(1, 1, At, B1); PG8_BAR; PG8_SCHED;
;             } else {
;             PG8_LDB(B0, 0, 0); PG8_SCHED; PG8_LDA(At, 0, 0); PG8_STAGE(PG8_SA(1, 1), a1 + hstepA, voffA);
;             PG8_WAIT_L(8); PG8_BAR; PG8_WAIT_L(0); PG8_MMA(0, 0, At, B0); PG8_BAR; PG8_SCHED;
;             PG8_LDB(B1, 0, 1); PG8_STAGE(PG8_SB(0, 0), b2, voffB);
;             PG8_BAR; PG8_WAIT_L(0); PG8_MMA(0, 1, At, B1); PG8_BAR;
;             PG8_LDA(At, 0, 1); PG8_STAGE(PG8_SA(0, 0), a2, voffA);
;             PG8_BAR; PG8_WAIT_L(0); PG8_MMA(1, 0, At, B0); PG8_BAR; PG8_SCHED;
;             PG8_STAGE(PG8_SB(0, 1), b2 + hstep, voffB);
;             PG8_WAIT_V(6); PG8_BAR; PG8_MMA(1, 1, At, B1); PG8_BAR;
;             PG8_LDB(B0, 1, 0); PG8_SCHED; PG8_LDA(At, 1, 0); PG8_STAGE(PG8_SA(0, 1), a2 + hstepA, voffA);
;             PG8_WAIT_L(8); PG8_BAR; PG8_WAIT_L(0); PG8_MMA(0, 0, At, B0); PG8_BAR; PG8_SCHED;
;             PG8_LDB(B1, 1, 1); PG8_STAGE(PG8_SB(1, 0), b3, voffB);
;             PG8_BAR; PG8_WAIT_L(0); PG8_MMA(0, 1, At, B1); PG8_BAR;
;             PG8_LDA(At, 1, 1); PG8_STAGE(PG8_SA(1, 0), a3, voffA);
	s_waitcnt lgkmcnt(0)
	v_mfma_scale_f32_16x16x128_f8f6f4 v[160:163], v[4:11], v[186:193], v[160:163], v245, v245 op_sel_hi:[0,0,0]
	v_mfma_scale_f32_16x16x128_f8f6f4 v[156:159], v[12:19], v[186:193], v[156:159], v245, v245 op_sel_hi:[0,0,0]
	v_mfma_scale_f32_16x16x128_f8f6f4 v[144:147], v[4:11], v[208:215], v[144:147], v245, v245 op_sel_hi:[0,0,0]
	v_mfma_scale_f32_16x16x128_f8f6f4 v[140:143], v[12:19], v[208:215], v[140:143], v245, v245 op_sel_hi:[0,0,0]
	v_mfma_scale_f32_16x16x128_f8f6f4 v[128:131], v[4:11], v[216:223], v[128:131], v245, v245 op_sel_hi:[0,0,0]
	v_mfma_scale_f32_16x16x128_f8f6f4 v[124:127], v[12:19], v[216:223], v[124:127], v245, v245 op_sel_hi:[0,0,0]
	v_mfma_scale_f32_16x16x128_f8f6f4 v[112:115], v[4:11], v[228:235], v[112:115], v245, v245 op_sel_hi:[0,0,0]
	v_mfma_scale_f32_16x16x128_f8f6f4 v[108:111], v[12:19], v[228:235], v[108:111], v245, v245 op_sel_hi:[0,0,0]
	v_mfma_scale_f32_16x16x128_f8f6f4 v[152:155], v[20:27], v[186:193], v[152:155], v245, v245 op_sel_hi:[0,0,0]
	v_mfma_scale_f32_16x16x128_f8f6f4 v[148:151], v[28:35], v[186:193], v[148:151], v245, v245 op_sel_hi:[0,0,0]
	v_mfma_scale_f32_16x16x128_f8f6f4 v[136:139], v[20:27], v[208:215], v[136:139], v245, v245 op_sel_hi:[0,0,0]
	v_mfma_scale_f32_16x16x128_f8f6f4 v[132:135], v[28:35], v[208:215], v[132:135], v245, v245 op_sel_hi:[0,0,0]
	v_mfma_scale_f32_16x16x128_f8f6f4 v[120:123], v[20:27], v[216:223], v[120:123], v245, v245 op_sel_hi:[0,0,0]
	v_mfma_scale_f32_16x16x128_f8f6f4 v[116:119], v[28:35], v[216:223], v[116:119], v245, v245 op_sel_hi:[0,0,0]
	v_mfma_scale_f32_16x16x128_f8f6f4 v[104:107], v[20:27], v[228:235], v[104:107], v245, v245 op_sel_hi:[0,0,0]
	v_mfma_scale_f32_16x16x128_f8f6f4 v[100:103], v[28:35], v[228:235], v[100:103], v245, v245 op_sel_hi:[0,0,0]
	s_barrier
	s_add_i32 s62, s62, s17
	v_lshl_add_u64 v[178:179], v[178:179], 0, s[34:35]
	s_mov_b32 m0, s62
	ds_read_b128 v[186:189], v184 offset:49152
	ds_read_b128 v[190:193], v184 offset:50176
	ds_read_b128 v[208:211], v184 offset:51200
	ds_read_b128 v[212:215], v184 offset:52224
	ds_read_b128 v[216:219], v184 offset:53248
	ds_read_b128 v[220:223], v184 offset:54272
	ds_read_b128 v[228:231], v184 offset:55296
	ds_read_b128 v[232:235], v184 offset:56320
	global_load_lds_dwordx4 v[178:179], off
	s_add_i32 m0, s62, 0x2000
	s_add_u32 s60, s60, 0x58080
	v_lshl_add_u64 v[178:179], v[180:181], 0, s[34:35]
	s_addc_u32 s61, s61, 0
	s_add_i32 s62, s63, s17
	global_load_lds_dwordx4 v[178:179], off
	s_mov_b32 m0, s62
	s_nop 0
	global_load_lds_dwordx4 v2, s[60:61]
	s_add_i32 m0, s62, 0x2000
	s_nop 0
	global_load_lds_dwordx4 v164, s[60:61]
	s_mov_b32 m0, s64
	s_nop 0
	global_load_lds_dwordx4 v168, s[58:59]
	s_mov_b32 m0, s65
	s_nop 0
	global_load_lds_dwordx4 v166, s[58:59]
	s_waitcnt vmcnt(8)
	s_waitcnt lgkmcnt(0)
	s_barrier
	s_waitcnt lgkmcnt(0)
	v_mfma_scale_f32_16x16x128_f8f6f4 v[96:99], v[4:11], v[186:193], v[96:99], v245, v245 op_sel_hi:[0,0,0]
	v_mfma_scale_f32_16x16x128_f8f6f4 v[92:95], v[12:19], v[186:193], v[92:95], v245, v245 op_sel_hi:[0,0,0]
	v_mfma_scale_f32_16x16x128_f8f6f4 v[80:83], v[4:11], v[208:215], v[80:83], v245, v245 op_sel_hi:[0,0,0]
	v_mfma_scale_f32_16x16x128_f8f6f4 v[76:79], v[12:19], v[208:215], v[76:79], v245, v245 op_sel_hi:[0,0,0]
	v_mfma_scale_f32_16x16x128_f8f6f4 v[64:67], v[4:11], v[216:223], v[64:67], v245, v245 op_sel_hi:[0,0,0]
	v_mfma_scale_f32_16x16x128_f8f6f4 v[60:63], v[12:19], v[216:223], v[60:63], v245, v245 op_sel_hi:[0,0,0]
	v_mfma_scale_f32_16x16x128_f8f6f4 v[48:51], v[4:11], v[228:235], v[48:51], v245, v245 op_sel_hi:[0,0,0]
	v_mfma_scale_f32_16x16x128_f8f6f4 v[44:47], v[12:19], v[228:235], v[44:47], v245, v245 op_sel_hi:[0,0,0]
	v_mfma_scale_f32_16x16x128_f8f6f4 v[88:91], v[20:27], v[186:193], v[88:91], v245, v245 op_sel_hi:[0,0,0]
	v_mfma_scale_f32_16x16x128_f8f6f4 v[84:87], v[28:35], v[186:193], v[84:87], v245, v245 op_sel_hi:[0,0,0]
	v_mfma_scale_f32_16x16x128_f8f6f4 v[72:75], v[20:27], v[208:215], v[72:75], v245, v245 op_sel_hi:[0,0,0]
	v_mfma_scale_f32_16x16x128_f8f6f4 v[68:71], v[28:35], v[208:215], v[68:71], v245, v245 op_sel_hi:[0,0,0]
	v_mfma_scale_f32_16x16x128_f8f6f4 v[56:59], v[20:27], v[216:223], v[56:59], v245, v245 op_sel_hi:[0,0,0]
	v_mfma_scale_f32_16x16x128_f8f6f4 v[52:55], v[28:35], v[216:223], v[52:55], v245, v245 op_sel_hi:[0,0,0]
	v_mfma_scale_f32_16x16x128_f8f6f4 v[40:43], v[20:27], v[228:235], v[40:43], v245, v245 op_sel_hi:[0,0,0]
	v_mfma_scale_f32_16x16x128_f8f6f4 v[36:39], v[28:35], v[228:235], v[36:39], v245, v245 op_sel_hi:[0,0,0]
	s_barrier
	s_add_u32 s4, s4, 0x100
	s_addc_u32 s5, s5, 0
	s_add_u32 s56, s56, 0x10000
	s_addc_u32 s57, s57, 0
	s_cmp_gt_u32 s71, 19
	s_cbranch_scc0 .LBB0_508
	s_waitcnt vmcnt(0)
	s_nop 15
	s_nop 15
	s_and_b64 vcc, exec, s[50:51]
	s_cbranch_vccz .LBB0_511
	s_barrier

; #define PG8_STAGE(bufoff, gbase, voff) do { _Pragma("unroll") for (int _i = 0; _i < 2; ++_i) \
;         __builtin_amdgcn_global_load_lds((const unsigned*)((const char*)(gbase) + (voff)[_i]), (PG8_LAS unsigned*)(lds + (bufoff) + ldsw + _i * 8192), 16, 0, 0); } while (0)
; #define PG8_LDA(dst, b, h) do { _Pragma("unroll") for (int m = 0; m < 4; ++m) _Pragma("unroll") for (int k = 0; k < 2; ++k) dst[m][k] = *(const PG8_LAS bf16x8*)(lds + PG8_SA(b, h) + aoff + m * 2048 + k * 1024); } while (0)
; #define PG8_LDB(dst, b, h) do { _Pragma("unroll") for (int n = 0; n < 2; ++n) _Pragma("unroll") for (int k = 0; k < 2; ++k) dst[n][k] = *(const PG8_LAS bf16x8*)(lds + PG8_SB(b, h) + boff + n * 2048 + k * 1024); } while (0)
; #define PG8_WAIT_V(n) asm volatile("s_waitcnt vmcnt(" #n ")" ::: "memory")
; #define PG8_WAIT_V8_UNLESS_FIRST(t) asm volatile("s_cmp_eq_u32 %0, 0\n\ts_cbranch_scc1 .Lpg8skip%=\n\ts_waitcnt vmcnt(8)\n.Lpg8skip%=:" :: "s"(t) : "scc", "memory")
; #define PG8_WAIT_L(n) asm volatile("s_waitcnt lgkmcnt(" #n ")" ::: "memory")
; #define PG8_BAR __builtin_amdgcn_s_barrier()
; template <class Epi, class Sched, bool ALIGN_EPI = false, bool SP2 = false, bool FP8 = false, bool ABLK = false>
; __device__ __forceinline__ void gemm_phase(PG8_LAS unsigned char* lds, const Gemm g, const Sched& S, const Epi& E) {
;     ...
;             PG8_LDB(B0, 0, 0); PG8_LDB(B1, 0, 1); PG8_SCHED; PG8_LDA(At, 0, 0); PG8_STAGE(PG8_SA(1, 1), a1 + hstepA, voffA);
;             PG8_WAIT_V8_UNLESS_FIRST(t); PG8_WAIT_L(0); PG8_BAR; PG8_MMA(0, 0, At, B0); PG8_MMA(0, 1, At, B1); PG8_BAR; PG8_SCHED;
;             PG8_LDA(At, 0, 1); PG8_STAGE(PG8_SB(0, 0), b2, voffB); PG8_STAGE(PG8_SB(0, 1), b2 + hstep, voffB); PG8_STAGE(PG8_SA(0, 0), a2, voffA);
;             PG8_WAIT_V8_UNLESS_FIRST(t); PG8_WAIT_L(0); PG8_BAR; PG8_MMA(1, 0, At, B0); PG8_MMA(1, 1, At, B1); PG8_BAR; PG8_SCHED;
;             PG8_LDB(B0, 1, 0); PG8_LDB(B1, 1, 1); PG8_SCHED; PG8_LDA(At, 1, 0); PG8_STAGE(PG8_SA(0, 1), a2 + hstepA, voffA);
;             PG8_WAIT_V(8); PG8_WAIT_L(0); PG8_BAR; PG8_MMA(0, 0, At, B0); PG8_MMA(0, 1, At, B1); PG8_BAR; PG8_SCHED;
;             PG8_LDA(At, 1, 1); PG8_STAGE(PG8_SB(1, 0), b3, voffB); PG8_STAGE(PG8_SB(1, 1), b3 + hstep, voffB); PG8_STAGE(PG8_SA(1, 0), a3, voffA);
;             PG8_WAIT_V(8); PG8_WAIT_L(0); PG8_BAR; PG8_MMA(1, 0, At, B0); PG8_MMA(1, 1, At, B1); PG8_BAR; PG8_SCHED;
.Lpg8skip4:
	s_waitcnt lgkmcnt(0)
	s_barrier
	s_waitcnt lgkmcnt(0)
	v_mfma_f32_16x16x32_bf16 v[128:131], v[132:135], v[164:167], v[128:131]
	v_mfma_f32_16x16x32_bf16 v[124:127], v[140:143], v[164:167], v[124:127]
	v_mfma_f32_16x16x32_bf16 v[112:115], v[132:135], v[182:185], v[112:115]
	v_mfma_f32_16x16x32_bf16 v[108:111], v[140:143], v[182:185], v[108:111]
	v_mfma_f32_16x16x32_bf16 v[96:99], v[132:135], v[212:215], v[96:99]
	v_mfma_f32_16x16x32_bf16 v[92:95], v[140:143], v[212:215], v[92:95]
	v_mfma_f32_16x16x32_bf16 v[80:83], v[132:135], v[220:223], v[80:83]
	v_mfma_f32_16x16x32_bf16 v[76:79], v[140:143], v[220:223], v[76:79]
	v_mfma_f32_16x16x32_bf16 v[128:131], v[136:139], v[168:171], v[128:131]
	v_mfma_f32_16x16x32_bf16 v[124:127], v[144:147], v[168:171], v[124:127]
	v_mfma_f32_16x16x32_bf16 v[112:115], v[136:139], v[208:211], v[112:115]
	v_mfma_f32_16x16x32_bf16 v[108:111], v[144:147], v[208:211], v[108:111]
	v_mfma_f32_16x16x32_bf16 v[96:99], v[136:139], v[216:219], v[96:99]
	v_mfma_f32_16x16x32_bf16 v[92:95], v[144:147], v[216:219], v[92:95]
	v_mfma_f32_16x16x32_bf16 v[80:83], v[136:139], v[228:231], v[80:83]
	v_mfma_f32_16x16x32_bf16 v[76:79], v[144:147], v[228:231], v[76:79]
	v_mfma_f32_16x16x32_bf16 v[120:123], v[148:151], v[164:167], v[120:123]
	v_mfma_f32_16x16x32_bf16 v[116:119], v[156:159], v[164:167], v[116:119]
	v_mfma_f32_16x16x32_bf16 v[104:107], v[148:151], v[182:185], v[104:107]
	v_mfma_f32_16x16x32_bf16 v[100:103], v[156:159], v[182:185], v[100:103]
	v_mfma_f32_16x16x32_bf16 v[88:91], v[148:151], v[212:215], v[88:91]
	v_mfma_f32_16x16x32_bf16 v[84:87], v[156:159], v[212:215], v[84:87]
	v_mfma_f32_16x16x32_bf16 v[72:75], v[148:151], v[220:223], v[72:75]
	v_mfma_f32_16x16x32_bf16 v[68:71], v[156:159], v[220:223], v[68:71]
	v_mfma_f32_16x16x32_bf16 v[120:123], v[152:155], v[168:171], v[120:123]
	v_mfma_f32_16x16x32_bf16 v[116:119], v[160:163], v[168:171], v[116:119]
	v_mfma_f32_16x16x32_bf16 v[104:107], v[152:155], v[208:211], v[104:107]
	v_mfma_f32_16x16x32_bf16 v[100:103], v[160:163], v[208:211], v[100:103]
	v_mfma_f32_16x16x32_bf16 v[88:91], v[152:155], v[216:219], v[88:91]
	v_mfma_f32_16x16x32_bf16 v[84:87], v[160:163], v[216:219], v[84:87]
	v_mfma_f32_16x16x32_bf16 v[72:75], v[152:155], v[228:231], v[72:75]
	v_mfma_f32_16x16x32_bf16 v[68:71], v[160:163], v[228:231], v[68:71]
	s_barrier
	s_add_i32 s96, s96, s7
	v_lshl_add_u64 v[188:189], s[44:45], 0, v[2:3]
	s_mov_b32 m0, s96
	ds_read_b128 v[164:167], v195 offset:16384
	ds_read_b128 v[168:171], v195 offset:17408
	ds_read_b128 v[182:185], v195 offset:18432
	ds_read_b128 v[208:211], v195 offset:19456
	ds_read_b128 v[212:215], v195 offset:20480
	ds_read_b128 v[216:219], v195 offset:21504
	ds_read_b128 v[220:223], v195 offset:22528
	ds_read_b128 v[228:231], v195 offset:23552
	global_load_lds_dwordx4 v2, s[44:45]
	s_add_i32 m0, s96, 0x2000
	s_add_u32 s96, s44, 0x40000
	v_lshl_add_u64 v[192:193], s[44:45], 0, v[172:173]
	s_addc_u32 s97, s45, 0
	s_add_i32 vcc_lo, vcc_lo, s7
	global_load_lds_dwordx4 v172, s[44:45]
	s_mov_b32 m0, vcc_lo
	v_lshl_add_u64 v[232:233], s[90:91], 0, v[174:175]
	global_load_lds_dwordx4 v2, s[96:97]
	s_add_i32 m0, vcc_lo, 0x2000
	s_nop 0
	global_load_lds_dwordx4 v172, s[96:97]
	v_lshl_add_u64 v[224:225], s[90:91], 0, v[176:177]
	s_mov_b32 m0, s8
	s_nop 0
	global_load_lds_dwordx4 v176, s[90:91]
	s_mov_b32 m0, s9
	s_nop 0
	global_load_lds_dwordx4 v174, s[90:91]
	s_cmp_eq_u32 s95, 0
	s_cbranch_scc1 .Lpg8skip5
	s_waitcnt vmcnt(8)
.Lpg8skip5:
	s_waitcnt lgkmcnt(0)
	s_barrier
	s_waitcnt lgkmcnt(0)
	v_mfma_f32_16x16x32_bf16 v[64:67], v[132:135], v[164:167], v[64:67]
	v_mfma_f32_16x16x32_bf16 v[60:63], v[140:143], v[164:167], v[60:63]
	v_mfma_f32_16x16x32_bf16 v[48:51], v[132:135], v[182:185], v[48:51]
	v_mfma_f32_16x16x32_bf16 v[44:47], v[140:143], v[182:185], v[44:47]
	v_mfma_f32_16x16x32_bf16 v[32:35], v[132:135], v[212:215], v[32:35]
	v_mfma_f32_16x16x32_bf16 v[28:31], v[140:143], v[212:215], v[28:31]
	v_mfma_f32_16x16x32_bf16 v[16:19], v[132:135], v[220:223], v[16:19]
	v_mfma_f32_16x16x32_bf16 v[12:15], v[140:143], v[220:223], v[12:15]
	v_mfma_f32_16x16x32_bf16 v[64:67], v[136:139], v[168:171], v[64:67]
	v_mfma_f32_16x16x32_bf16 v[60:63], v[144:147], v[168:171], v[60:63]
	v_mfma_f32_16x16x32_bf16 v[48:51], v[136:139], v[208:211], v[48:51]
	v_mfma_f32_16x16x32_bf16 v[44:47], v[144:147], v[208:211], v[44:47]
	v_mfma_f32_16x16x32_bf16 v[32:35], v[136:139], v[216:219], v[32:35]
	v_mfma_f32_16x16x32_bf16 v[28:31], v[144:147], v[216:219], v[28:31]
	v_mfma_f32_16x16x32_bf16 v[16:19], v[136:139], v[228:231], v[16:19]
	v_mfma_f32_16x16x32_bf16 v[12:15], v[144:147], v[228:231], v[12:15]
	v_mfma_f32_16x16x32_bf16 v[56:59], v[148:151], v[164:167], v[56:59]
	v_mfma_f32_16x16x32_bf16 v[52:55], v[156:159], v[164:167], v[52:55]
	v_mfma_f32_16x16x32_bf16 v[40:43], v[148:151], v[182:185], v[40:43]
	v_mfma_f32_16x16x32_bf16 v[36:39], v[156:159], v[182:185], v[36:39]
	v_mfma_f32_16x16x32_bf16 v[24:27], v[148:151], v[212:215], v[24:27]
	v_mfma_f32_16x16x32_bf16 v[20:23], v[156:159], v[212:215], v[20:23]
	v_mfma_f32_16x16x32_bf16 v[8:11], v[148:151], v[220:223], v[8:11]
	v_mfma_f32_16x16x32_bf16 v[4:7], v[156:159], v[220:223], v[4:7]
	v_mfma_f32_16x16x32_bf16 v[56:59], v[152:155], v[168:171], v[56:59]
	v_mfma_f32_16x16x32_bf16 v[52:55], v[160:163], v[168:171], v[52:55]
	v_mfma_f32_16x16x32_bf16 v[40:43], v[152:155], v[208:211], v[40:43]
	v_mfma_f32_16x16x32_bf16 v[36:39], v[160:163], v[208:211], v[36:39]
	v_mfma_f32_16x16x32_bf16 v[24:27], v[152:155], v[216:219], v[24:27]
	v_mfma_f32_16x16x32_bf16 v[20:23], v[160:163], v[216:219], v[20:23]
	v_mfma_f32_16x16x32_bf16 v[8:11], v[152:155], v[228:231], v[8:11]
	v_mfma_f32_16x16x32_bf16 v[4:7], v[160:163], v[228:231], v[4:7]
	s_barrier
; #define PG8_BAR __builtin_amdgcn_s_barrier()
; template <class Epi, class Sched, bool ALIGN_EPI = false, bool SP2 = false, bool FP8 = false, bool ABLK = false>
; __device__ __forceinline__ void gemm_phase(PG8_LAS unsigned char* lds, const Gemm g, const Sched& S, const Epi& E) {
;     ...
;             PG8_LDB(B0, 0, 0); PG8_LDB(B1, 0, 1); PG8_SCHED; PG8_LDA(At, 0, 0); PG8_STAGE(PG8_SA(1, 1), a1 + hstepA, voffA);
;             PG8_WAIT_V8_UNLESS_FIRST(t); PG8_WAIT_L(0); PG8_BAR; PG8_MMA(0, 0, At, B0); PG8_MMA(0, 1, At, B1); PG8_BAR; PG8_SCHED;
;             PG8_LDA(At, 0, 1); PG8_STAGE(PG8_SB(0, 0), b2, voffB); PG8_STAGE(PG8_SB(0, 1), b2 + hstep, voffB); PG8_STAGE(PG8_SA(0, 0), a2, voffA);
;             PG8_WAIT_V8_UNLESS_FIRST(t); PG8_WAIT_L(0); PG8_BAR; PG8_MMA(1, 0, At, B0); PG8_MMA(1, 1, At, B1); PG8_BAR; PG8_SCHED;
;             PG8_LDB(B0, 1, 0); PG8_LDB(B1, 1, 1); PG8_SCHED; PG8_LDA(At, 1, 0); PG8_STAGE(PG8_SA(0, 1), a2 + hstepA, voffA);
;             PG8_WAIT_V(8); PG8_WAIT_L(0); PG8_BAR; PG8_MMA(0, 0, At, B0); PG8_MMA(0, 1, At, B1); PG8_BAR; PG8_SCHED;
;             PG8_LDA(At, 1, 1); PG8_STAGE(PG8_SB(1, 0), b3, voffB); PG8_STAGE(PG8_SB(1, 1), b3 + hstep, voffB); PG8_STAGE(PG8_SA(1, 0), a3, voffA);
;             PG8_WAIT_V(8); PG8_WAIT_L(0); PG8_BAR; PG8_MMA(1, 0, At, B0); PG8_MMA(1, 1, At, B1); PG8_BAR; PG8_SCHED;
;             } else {
;             PG8_LDB(B0, 0, 0); PG8_SCHED; PG8_LDA(At, 0, 0); PG8_STAGE(PG8_SA(1, 1), a1 + hstepA, voffA);
;             PG8_WAIT_L(8); PG8_BAR; PG8_WAIT_L(0); PG8_MMA(0, 0, At, B0); PG8_BAR; PG8_SCHED;
;             PG8_LDB(B1, 0, 1); PG8_STAGE(PG8_SB(0, 0), b2, voffB);
;             PG8_BAR; PG8_WAIT_L(0); PG8_MMA(0, 1, At, B1); PG8_BAR;
;             PG8_LDA(At, 0, 1); PG8_STAGE(PG8_SA(0, 0), a2, voffA);
;             PG8_BAR; PG8_WAIT_L(0); PG8_MMA(1, 0, At, B0); PG8_BAR; PG8_SCHED;
;             PG8_STAGE(PG8_SB(0, 1), b2 + hstep, voffB);
;             PG8_WAIT_V(6); PG8_BAR; PG8_MMA(1, 1, At, B1); PG8_BAR;
;             PG8_LDB(B0, 1, 0); PG8_SCHED; PG8_LDA(At, 1, 0); PG8_STAGE(PG8_SA(0, 1), a2 + hstepA, voffA);
;             PG8_WAIT_L(8); PG8_BAR; PG8_WAIT_L(0); PG8_MMA(0, 0, At, B0); PG8_BAR; PG8_SCHED;
;             PG8_LDB(B1, 1, 1); PG8_STAGE(PG8_SB(1, 0), b3, voffB);
;             PG8_BAR; PG8_WAIT_L(0); PG8_MMA(0, 1, At, B1); PG8_BAR;
;             PG8_LDA(At, 1, 1); PG8_STAGE(PG8_SA(1, 0), a3, voffA);
	s_add_i32 s96, 0, 0x18000
	s_add_i32 s97, 0, 0x1c000
	v_add_u32_e32 v144, s96, v191
	v_add_u32_e32 v160, s97, v191
	ds_read_b128 v[132:135], v144
	ds_read_b128 v[136:139], v144 offset:1024
	ds_read_b128 v[140:143], v144 offset:2048
	ds_read_b128 v[144:147], v144 offset:3072
	ds_read_b128 v[148:151], v160
	ds_read_b128 v[152:155], v160 offset:1024
	ds_read_b128 v[156:159], v160 offset:2048
	ds_read_b128 v[160:163], v160 offset:3072
	s_add_u32 s90, s90, 0x40000
	s_addc_u32 s91, s91, 0
	s_mov_b32 m0, s17
	ds_read_b128 v[164:167], v195 offset:32768
	ds_read_b128 v[168:171], v195 offset:33792
	ds_read_b128 v[182:185], v195 offset:34816
	ds_read_b128 v[208:211], v195 offset:35840
	ds_read_b128 v[212:215], v195 offset:36864
	ds_read_b128 v[216:219], v195 offset:37888
	ds_read_b128 v[220:223], v195 offset:38912
	ds_read_b128 v[228:231], v195 offset:39936
	global_load_lds_dwordx4 v176, s[90:91]
	s_mov_b32 m0, s18
	s_nop 0
	global_load_lds_dwordx4 v174, s[90:91]
	s_waitcnt vmcnt(8)
	s_waitcnt lgkmcnt(0)
	s_barrier
	s_waitcnt lgkmcnt(0)
	v_mfma_f32_16x16x32_bf16 v[128:131], v[132:135], v[164:167], v[128:131]
	v_mfma_f32_16x16x32_bf16 v[124:127], v[140:143], v[164:167], v[124:127]
	v_mfma_f32_16x16x32_bf16 v[112:115], v[132:135], v[182:185], v[112:115]
	v_mfma_f32_16x16x32_bf16 v[108:111], v[140:143], v[182:185], v[108:111]
	v_mfma_f32_16x16x32_bf16 v[96:99], v[132:135], v[212:215], v[96:99]
	v_mfma_f32_16x16x32_bf16 v[92:95], v[140:143], v[212:215], v[92:95]
	v_mfma_f32_16x16x32_bf16 v[80:83], v[132:135], v[220:223], v[80:83]
	v_mfma_f32_16x16x32_bf16 v[76:79], v[140:143], v[220:223], v[76:79]
	v_mfma_f32_16x16x32_bf16 v[128:131], v[136:139], v[168:171], v[128:131]
	v_mfma_f32_16x16x32_bf16 v[124:127], v[144:147], v[168:171], v[124:127]
	v_mfma_f32_16x16x32_bf16 v[112:115], v[136:139], v[208:211], v[112:115]
	v_mfma_f32_16x16x32_bf16 v[108:111], v[144:147], v[208:211], v[108:111]
	v_mfma_f32_16x16x32_bf16 v[96:99], v[136:139], v[216:219], v[96:99]
	v_mfma_f32_16x16x32_bf16 v[92:95], v[144:147], v[216:219], v[92:95]
	v_mfma_f32_16x16x32_bf16 v[80:83], v[136:139], v[228:231], v[80:83]
	v_mfma_f32_16x16x32_bf16 v[76:79], v[144:147], v[228:231], v[76:79]
	v_mfma_f32_16x16x32_bf16 v[120:123], v[148:151], v[164:167], v[120:123]
	v_mfma_f32_16x16x32_bf16 v[116:119], v[156:159], v[164:167], v[116:119]
	v_mfma_f32_16x16x32_bf16 v[104:107], v[148:151], v[182:185], v[104:107]
	v_mfma_f32_16x16x32_bf16 v[100:103], v[156:159], v[182:185], v[100:103]
	v_mfma_f32_16x16x32_bf16 v[88:91], v[148:151], v[212:215], v[88:91]
	v_mfma_f32_16x16x32_bf16 v[84:87], v[156:159], v[212:215], v[84:87]
	v_mfma_f32_16x16x32_bf16 v[72:75], v[148:151], v[220:223], v[72:75]
	v_mfma_f32_16x16x32_bf16 v[68:71], v[156:159], v[220:223], v[68:71]
	v_mfma_f32_16x16x32_bf16 v[120:123], v[152:155], v[168:171], v[120:123]
	v_mfma_f32_16x16x32_bf16 v[116:119], v[160:163], v[168:171], v[116:119]
	v_mfma_f32_16x16x32_bf16 v[104:107], v[152:155], v[208:211], v[104:107]
	v_mfma_f32_16x16x32_bf16 v[100:103], v[160:163], v[208:211], v[100:103]
	v_mfma_f32_16x16x32_bf16 v[88:91], v[152:155], v[216:219], v[88:91]
	v_mfma_f32_16x16x32_bf16 v[84:87], v[160:163], v[216:219], v[84:87]
	v_mfma_f32_16x16x32_bf16 v[72:75], v[152:155], v[228:231], v[72:75]
	v_mfma_f32_16x16x32_bf16 v[68:71], v[160:163], v[228:231], v[68:71]
	s_barrier
	s_add_i32 s90, s96, s7
	v_lshl_add_u64 v[188:189], v[188:189], 0, s[34:35]
	s_mov_b32 m0, s90
	ds_read_b128 v[164:167], v195 offset:49152
	ds_read_b128 v[168:171], v195 offset:50176
	ds_read_b128 v[182:185], v195 offset:51200
	ds_read_b128 v[208:211], v195 offset:52224
	ds_read_b128 v[212:215], v195 offset:53248
	ds_read_b128 v[216:219], v195 offset:54272
	ds_read_b128 v[220:223], v195 offset:55296
	ds_read_b128 v[228:231], v195 offset:56320
	global_load_lds_dwordx4 v[188:189], off
	s_add_i32 m0, s90, 0x2000
	s_add_u32 s44, s44, 0x40080
	v_lshl_add_u64 v[188:189], v[192:193], 0, s[34:35]
	s_addc_u32 s45, s45, 0
	s_add_i32 s90, s97, s7
	global_load_lds_dwordx4 v[188:189], off
	s_mov_b32 m0, s90
	s_nop 0
	global_load_lds_dwordx4 v2, s[44:45]
	s_add_i32 m0, s90, 0x2000
	s_nop 0
	global_load_lds_dwordx4 v172, s[44:45]
	v_lshl_add_u64 v[188:189], v[224:225], 0, s[34:35]
	s_mov_b32 m0, s19
	s_nop 0
	global_load_lds_dwordx4 v[188:189], off
	v_lshl_add_u64 v[188:189], v[232:233], 0, s[34:35]
	s_mov_b32 m0, s20
	s_nop 0
	global_load_lds_dwordx4 v[188:189], off
	s_waitcnt vmcnt(8)
	s_waitcnt lgkmcnt(0)
	s_barrier
	s_waitcnt lgkmcnt(0)
	v_mfma_f32_16x16x32_bf16 v[64:67], v[132:135], v[164:167], v[64:67]
	v_mfma_f32_16x16x32_bf16 v[60:63], v[140:143], v[164:167], v[60:63]
	v_mfma_f32_16x16x32_bf16 v[48:51], v[132:135], v[182:185], v[48:51]
	v_mfma_f32_16x16x32_bf16 v[44:47], v[140:143], v[182:185], v[44:47]
	v_mfma_f32_16x16x32_bf16 v[32:35], v[132:135], v[212:215], v[32:35]
	v_mfma_f32_16x16x32_bf16 v[28:31], v[140:143], v[212:215], v[28:31]
	v_mfma_f32_16x16x32_bf16 v[16:19], v[132:135], v[220:223], v[16:19]
	v_mfma_f32_16x16x32_bf16 v[12:15], v[140:143], v[220:223], v[12:15]
	v_mfma_f32_16x16x32_bf16 v[64:67], v[136:139], v[168:171], v[64:67]
	v_mfma_f32_16x16x32_bf16 v[60:63], v[144:147], v[168:171], v[60:63]
	v_mfma_f32_16x16x32_bf16 v[48:51], v[136:139], v[208:211], v[48:51]
	v_mfma_f32_16x16x32_bf16 v[44:47], v[144:147], v[208:211], v[44:47]
	v_mfma_f32_16x16x32_bf16 v[32:35], v[136:139], v[216:219], v[32:35]
	v_mfma_f32_16x16x32_bf16 v[28:31], v[144:147], v[216:219], v[28:31]
	v_mfma_f32_16x16x32_bf16 v[16:19], v[136:139], v[228:231], v[16:19]
	v_mfma_f32_16x16x32_bf16 v[12:15], v[144:147], v[228:231], v[12:15]
	v_mfma_f32_16x16x32_bf16 v[56:59], v[148:151], v[164:167], v[56:59]
	v_mfma_f32_16x16x32_bf16 v[52:55], v[156:159], v[164:167], v[52:55]
	v_mfma_f32_16x16x32_bf16 v[40:43], v[148:151], v[182:185], v[40:43]
	v_mfma_f32_16x16x32_bf16 v[36:39], v[156:159], v[182:185], v[36:39]
	v_mfma_f32_16x16x32_bf16 v[24:27], v[148:151], v[212:215], v[24:27]
	v_mfma_f32_16x16x32_bf16 v[20:23], v[156:159], v[212:215], v[20:23]
	v_mfma_f32_16x16x32_bf16 v[8:11], v[148:151], v[220:223], v[8:11]
	v_mfma_f32_16x16x32_bf16 v[4:7], v[156:159], v[220:223], v[4:7]
	v_mfma_f32_16x16x32_bf16 v[56:59], v[152:155], v[168:171], v[56:59]
	v_mfma_f32_16x16x32_bf16 v[52:55], v[160:163], v[168:171], v[52:55]
	v_mfma_f32_16x16x32_bf16 v[40:43], v[152:155], v[208:211], v[40:43]
	v_mfma_f32_16x16x32_bf16 v[36:39], v[160:163], v[208:211], v[36:39]
	v_mfma_f32_16x16x32_bf16 v[24:27], v[152:155], v[216:219], v[24:27]
	v_mfma_f32_16x16x32_bf16 v[20:23], v[160:163], v[216:219], v[20:23]
	v_mfma_f32_16x16x32_bf16 v[8:11], v[152:155], v[228:231], v[8:11]
	v_mfma_f32_16x16x32_bf16 v[4:7], v[160:163], v[228:231], v[4:7]
	s_barrier
	s_add_u32 s42, s42, 0x100
	s_addc_u32 s43, s43, 0
	s_add_u32 s92, s92, 0x100
	s_addc_u32 s94, s94, 0
	s_cmp_gt_u32 s95, 13
	s_mov_b32 s44, s95
	s_cbranch_scc0 .LBB0_600
	s_waitcnt vmcnt(0)
	s_and_b64 vcc, exec, s[64:65]
	s_cbranch_vccnz .LBB0_604
	s_cmpk_lt_i32 s73, 0xf4
	s_mov_b64 s[4:5], -1
	s_cbranch_scc1 .LBB0_605

; #define PG8_STAGE(bufoff, gbase, voff) do { _Pragma("unroll") for (int _i = 0; _i < 2; ++_i) \
;         __builtin_amdgcn_global_load_lds((const unsigned*)((const char*)(gbase) + (voff)[_i]), (PG8_LAS unsigned*)(lds + (bufoff) + ldsw + _i * 8192), 16, 0, 0); } while (0)
; #define PG8_LDA(dst, b, h) do { _Pragma("unroll") for (int m = 0; m < 4; ++m) _Pragma("unroll") for (int k = 0; k < 2; ++k) dst[m][k] = *(const PG8_LAS bf16x8*)(lds + PG8_SA(b, h) + aoff + m * 2048 + k * 1024); } while (0)
; #define PG8_LDB(dst, b, h) do { _Pragma("unroll") for (int n = 0; n < 2; ++n) _Pragma("unroll") for (int k = 0; k < 2; ++k) dst[n][k] = *(const PG8_LAS bf16x8*)(lds + PG8_SB(b, h) + boff + n * 2048 + k * 1024); } while (0)
; #define PG8_WAIT_V(n) asm volatile("s_waitcnt vmcnt(" #n ")" ::: "memory")
; #define PG8_WAIT_V8_UNLESS_FIRST(t) asm volatile("s_cmp_eq_u32 %0, 0\n\ts_cbranch_scc1 .Lpg8skip%=\n\ts_waitcnt vmcnt(8)\n.Lpg8skip%=:" :: "s"(t) : "scc", "memory")
; #define PG8_WAIT_L(n) asm volatile("s_waitcnt lgkmcnt(" #n ")" ::: "memory")
; #define PG8_BAR __builtin_amdgcn_s_barrier()
; template <class Epi, class Sched, bool ALIGN_EPI = false, bool SP2 = false, bool FP8 = false, bool ABLK = false>
; __device__ __forceinline__ void gemm_phase(PG8_LAS unsigned char* lds, const Gemm g, const Sched& S, const Epi& E) {
;     ...
;             PG8_LDB(B0, 0, 0); PG8_LDB(B1, 0, 1); PG8_SCHED; PG8_LDA(At, 0, 0); PG8_STAGE(PG8_SA(1, 1), a1 + hstepA, voffA);
;             PG8_WAIT_V8_UNLESS_FIRST(t); PG8_WAIT_L(0); PG8_BAR; PG8_MMA(0, 0, At, B0); PG8_MMA(0, 1, At, B1); PG8_BAR; PG8_SCHED;
;             PG8_LDA(At, 0, 1); PG8_STAGE(PG8_SB(0, 0), b2, voffB); PG8_STAGE(PG8_SB(0, 1), b2 + hstep, voffB); PG8_STAGE(PG8_SA(0, 0), a2, voffA);
;             PG8_WAIT_V8_UNLESS_FIRST(t); PG8_WAIT_L(0); PG8_BAR; PG8_MMA(1, 0, At, B0); PG8_MMA(1, 1, At, B1); PG8_BAR; PG8_SCHED;
;             PG8_LDB(B0, 1, 0); PG8_LDB(B1, 1, 1); PG8_SCHED; PG8_LDA(At, 1, 0); PG8_STAGE(PG8_SA(0, 1), a2 + hstepA, voffA);
;             PG8_WAIT_V(8); PG8_WAIT_L(0); PG8_BAR; PG8_MMA(0, 0, At, B0); PG8_MMA(0, 1, At, B1); PG8_BAR; PG8_SCHED;
;             PG8_LDA(At, 1, 1); PG8_STAGE(PG8_SB(1, 0), b3, voffB); PG8_STAGE(PG8_SB(1, 1), b3 + hstep, voffB); PG8_STAGE(PG8_SA(1, 0), a3, voffA);
;             PG8_WAIT_V(8); PG8_WAIT_L(0); PG8_BAR; PG8_MMA(1, 0, At, B0); PG8_MMA(1, 1, At, B1); PG8_BAR; PG8_SCHED;
.Lpg8skip6:
	s_waitcnt lgkmcnt(0)
	s_barrier
	s_waitcnt lgkmcnt(0)
	v_mfma_f32_16x16x32_bf16 v[152:155], v[124:127], v[174:177], v[152:155]
	v_mfma_f32_16x16x32_bf16 v[148:151], v[132:135], v[174:177], v[148:151]
	v_mfma_f32_16x16x32_bf16 v[112:115], v[124:127], v[182:185], v[112:115]
	v_mfma_f32_16x16x32_bf16 v[108:111], v[132:135], v[182:185], v[108:111]
	v_mfma_f32_16x16x32_bf16 v[96:99], v[124:127], v[190:193], v[96:99]
	v_mfma_f32_16x16x32_bf16 v[92:95], v[132:135], v[190:193], v[92:95]
	v_mfma_f32_16x16x32_bf16 v[80:83], v[124:127], v[214:217], v[80:83]
	v_mfma_f32_16x16x32_bf16 v[76:79], v[132:135], v[214:217], v[76:79]
	v_mfma_f32_16x16x32_bf16 v[152:155], v[128:131], v[178:181], v[152:155]
	v_mfma_f32_16x16x32_bf16 v[148:151], v[136:139], v[178:181], v[148:151]
	v_mfma_f32_16x16x32_bf16 v[112:115], v[128:131], v[186:189], v[112:115]
	v_mfma_f32_16x16x32_bf16 v[108:111], v[136:139], v[186:189], v[108:111]
	v_mfma_f32_16x16x32_bf16 v[96:99], v[128:131], v[210:213], v[96:99]
	v_mfma_f32_16x16x32_bf16 v[92:95], v[136:139], v[210:213], v[92:95]
	v_mfma_f32_16x16x32_bf16 v[80:83], v[128:131], v[218:221], v[80:83]
	v_mfma_f32_16x16x32_bf16 v[76:79], v[136:139], v[218:221], v[76:79]
	v_mfma_f32_16x16x32_bf16 v[120:123], v[140:143], v[174:177], v[120:123]
	v_mfma_f32_16x16x32_bf16 v[116:119], v[156:159], v[174:177], v[116:119]
	v_mfma_f32_16x16x32_bf16 v[104:107], v[140:143], v[182:185], v[104:107]
	v_mfma_f32_16x16x32_bf16 v[100:103], v[156:159], v[182:185], v[100:103]
	v_mfma_f32_16x16x32_bf16 v[88:91], v[140:143], v[190:193], v[88:91]
	v_mfma_f32_16x16x32_bf16 v[84:87], v[156:159], v[190:193], v[84:87]
	v_mfma_f32_16x16x32_bf16 v[72:75], v[140:143], v[214:217], v[72:75]
	v_mfma_f32_16x16x32_bf16 v[68:71], v[156:159], v[214:217], v[68:71]
	v_mfma_f32_16x16x32_bf16 v[120:123], v[144:147], v[178:181], v[120:123]
	v_mfma_f32_16x16x32_bf16 v[116:119], v[170:173], v[178:181], v[116:119]
	v_mfma_f32_16x16x32_bf16 v[104:107], v[144:147], v[186:189], v[104:107]
	v_mfma_f32_16x16x32_bf16 v[100:103], v[170:173], v[186:189], v[100:103]
	v_mfma_f32_16x16x32_bf16 v[88:91], v[144:147], v[210:213], v[88:91]
	v_mfma_f32_16x16x32_bf16 v[84:87], v[170:173], v[210:213], v[84:87]
	v_mfma_f32_16x16x32_bf16 v[72:75], v[144:147], v[218:221], v[72:75]
	v_mfma_f32_16x16x32_bf16 v[68:71], v[170:173], v[218:221], v[68:71]
	s_barrier
	s_add_i32 s73, s73, s17
	v_lshl_add_u64 v[204:205], s[60:61], 0, v[2:3]
	s_mov_b32 m0, s73
	ds_read_b128 v[174:177], v208 offset:16384
	ds_read_b128 v[178:181], v208 offset:17408
	ds_read_b128 v[182:185], v208 offset:18432
	ds_read_b128 v[186:189], v208 offset:19456
	ds_read_b128 v[190:193], v208 offset:20480
	ds_read_b128 v[210:213], v208 offset:21504
	ds_read_b128 v[214:217], v208 offset:22528
	ds_read_b128 v[218:221], v208 offset:23552
	global_load_lds_dwordx4 v2, s[60:61]
	s_add_i32 m0, s73, 0x2000
	s_add_u32 s74, s60, 0x40000
	v_lshl_add_u64 v[206:207], s[60:61], 0, v[160:161]
	s_addc_u32 s75, s61, 0
	s_add_i32 s73, s76, s17
	global_load_lds_dwordx4 v160, s[60:61]
	s_mov_b32 m0, s73
	v_lshl_add_u64 v[224:225], s[62:63], 0, v[162:163]
	global_load_lds_dwordx4 v2, s[74:75]
	s_add_i32 m0, s73, 0x2000
	s_nop 0
	global_load_lds_dwordx4 v160, s[74:75]
	v_lshl_add_u64 v[222:223], s[62:63], 0, v[164:165]
	s_mov_b32 m0, s18
	s_nop 0
	global_load_lds_dwordx4 v164, s[62:63]
	s_mov_b32 m0, s19
	s_nop 0
	global_load_lds_dwordx4 v162, s[62:63]
	s_cmp_eq_u32 s72, 0
	s_cbranch_scc1 .Lpg8skip7
	s_waitcnt vmcnt(8)
.Lpg8skip7:
	s_waitcnt lgkmcnt(0)
	s_barrier
	s_waitcnt lgkmcnt(0)
	v_mfma_f32_16x16x32_bf16 v[64:67], v[124:127], v[174:177], v[64:67]
	v_mfma_f32_16x16x32_bf16 v[60:63], v[132:135], v[174:177], v[60:63]
	v_mfma_f32_16x16x32_bf16 v[48:51], v[124:127], v[182:185], v[48:51]
	v_mfma_f32_16x16x32_bf16 v[44:47], v[132:135], v[182:185], v[44:47]
	v_mfma_f32_16x16x32_bf16 v[32:35], v[124:127], v[190:193], v[32:35]
	v_mfma_f32_16x16x32_bf16 v[28:31], v[132:135], v[190:193], v[28:31]
	v_mfma_f32_16x16x32_bf16 v[16:19], v[124:127], v[214:217], v[16:19]
	v_mfma_f32_16x16x32_bf16 v[12:15], v[132:135], v[214:217], v[12:15]
	v_mfma_f32_16x16x32_bf16 v[64:67], v[128:131], v[178:181], v[64:67]
	v_mfma_f32_16x16x32_bf16 v[60:63], v[136:139], v[178:181], v[60:63]
	v_mfma_f32_16x16x32_bf16 v[48:51], v[128:131], v[186:189], v[48:51]
	v_mfma_f32_16x16x32_bf16 v[44:47], v[136:139], v[186:189], v[44:47]
	v_mfma_f32_16x16x32_bf16 v[32:35], v[128:131], v[210:213], v[32:35]
	v_mfma_f32_16x16x32_bf16 v[28:31], v[136:139], v[210:213], v[28:31]
	v_mfma_f32_16x16x32_bf16 v[16:19], v[128:131], v[218:221], v[16:19]
	v_mfma_f32_16x16x32_bf16 v[12:15], v[136:139], v[218:221], v[12:15]
	v_mfma_f32_16x16x32_bf16 v[56:59], v[140:143], v[174:177], v[56:59]
	v_mfma_f32_16x16x32_bf16 v[52:55], v[156:159], v[174:177], v[52:55]
	v_mfma_f32_16x16x32_bf16 v[40:43], v[140:143], v[182:185], v[40:43]
	v_mfma_f32_16x16x32_bf16 v[36:39], v[156:159], v[182:185], v[36:39]
	v_mfma_f32_16x16x32_bf16 v[24:27], v[140:143], v[190:193], v[24:27]
	v_mfma_f32_16x16x32_bf16 v[20:23], v[156:159], v[190:193], v[20:23]
	v_mfma_f32_16x16x32_bf16 v[8:11], v[140:143], v[214:217], v[8:11]
	v_mfma_f32_16x16x32_bf16 v[4:7], v[156:159], v[214:217], v[4:7]
	v_mfma_f32_16x16x32_bf16 v[56:59], v[144:147], v[178:181], v[56:59]
	v_mfma_f32_16x16x32_bf16 v[52:55], v[170:173], v[178:181], v[52:55]
	v_mfma_f32_16x16x32_bf16 v[40:43], v[144:147], v[186:189], v[40:43]
	v_mfma_f32_16x16x32_bf16 v[36:39], v[170:173], v[186:189], v[36:39]
	v_mfma_f32_16x16x32_bf16 v[24:27], v[144:147], v[210:213], v[24:27]
	v_mfma_f32_16x16x32_bf16 v[20:23], v[170:173], v[210:213], v[20:23]
	v_mfma_f32_16x16x32_bf16 v[8:11], v[144:147], v[218:221], v[8:11]
	v_mfma_f32_16x16x32_bf16 v[4:7], v[170:173], v[218:221], v[4:7]
	s_barrier
; #define PG8_BAR __builtin_amdgcn_s_barrier()
; template <class Epi, class Sched, bool ALIGN_EPI = false, bool SP2 = false, bool FP8 = false, bool ABLK = false>
; __device__ __forceinline__ void gemm_phase(PG8_LAS unsigned char* lds, const Gemm g, const Sched& S, const Epi& E) {
;     ...
;             PG8_LDB(B0, 0, 0); PG8_LDB(B1, 0, 1); PG8_SCHED; PG8_LDA(At, 0, 0); PG8_STAGE(PG8_SA(1, 1), a1 + hstepA, voffA);
;             PG8_WAIT_V8_UNLESS_FIRST(t); PG8_WAIT_L(0); PG8_BAR; PG8_MMA(0, 0, At, B0); PG8_MMA(0, 1, At, B1); PG8_BAR; PG8_SCHED;
;             PG8_LDA(At, 0, 1); PG8_STAGE(PG8_SB(0, 0), b2, voffB); PG8_STAGE(PG8_SB(0, 1), b2 + hstep, voffB); PG8_STAGE(PG8_SA(0, 0), a2, voffA);
;             PG8_WAIT_V8_UNLESS_FIRST(t); PG8_WAIT_L(0); PG8_BAR; PG8_MMA(1, 0, At, B0); PG8_MMA(1, 1, At, B1); PG8_BAR; PG8_SCHED;
;             PG8_LDB(B0, 1, 0); PG8_LDB(B1, 1, 1); PG8_SCHED; PG8_LDA(At, 1, 0); PG8_STAGE(PG8_SA(0, 1), a2 + hstepA, voffA);
;             PG8_WAIT_V(8); PG8_WAIT_L(0); PG8_BAR; PG8_MMA(0, 0, At, B0); PG8_MMA(0, 1, At, B1); PG8_BAR; PG8_SCHED;
;             PG8_LDA(At, 1, 1); PG8_STAGE(PG8_SB(1, 0), b3, voffB); PG8_STAGE(PG8_SB(1, 1), b3 + hstep, voffB); PG8_STAGE(PG8_SA(1, 0), a3, voffA);
;             PG8_WAIT_V(8); PG8_WAIT_L(0); PG8_BAR; PG8_MMA(1, 0, At, B0); PG8_MMA(1, 1, At, B1); PG8_BAR; PG8_SCHED;
;             } else {
;             PG8_LDB(B0, 0, 0); PG8_SCHED; PG8_LDA(At, 0, 0); PG8_STAGE(PG8_SA(1, 1), a1 + hstepA, voffA);
;             PG8_WAIT_L(8); PG8_BAR; PG8_WAIT_L(0); PG8_MMA(0, 0, At, B0); PG8_BAR; PG8_SCHED;
;             PG8_LDB(B1, 0, 1); PG8_STAGE(PG8_SB(0, 0), b2, voffB);
;             PG8_BAR; PG8_WAIT_L(0); PG8_MMA(0, 1, At, B1); PG8_BAR;
;             PG8_LDA(At, 0, 1); PG8_STAGE(PG8_SA(0, 0), a2, voffA);
;             PG8_BAR; PG8_WAIT_L(0); PG8_MMA(1, 0, At, B0); PG8_BAR; PG8_SCHED;
;             PG8_STAGE(PG8_SB(0, 1), b2 + hstep, voffB);
;             PG8_WAIT_V(6); PG8_BAR; PG8_MMA(1, 1, At, B1); PG8_BAR;
;             PG8_LDB(B0, 1, 0); PG8_SCHED; PG8_LDA(At, 1, 0); PG8_STAGE(PG8_SA(0, 1), a2 + hstepA, voffA);
;             PG8_WAIT_L(8); PG8_BAR; PG8_WAIT_L(0); PG8_MMA(0, 0, At, B0); PG8_BAR; PG8_SCHED;
;             PG8_LDB(B1, 1, 1); PG8_STAGE(PG8_SB(1, 0), b3, voffB);
;             PG8_BAR; PG8_WAIT_L(0); PG8_MMA(0, 1, At, B1); PG8_BAR;
;             PG8_LDA(At, 1, 1); PG8_STAGE(PG8_SA(1, 0), a3, voffA);
	s_add_i32 s73, 0, 0x18000
	s_add_i32 s74, 0, 0x1c000
	v_add_u32_e32 v136, s73, v195
	v_add_u32_e32 v170, s74, v195
	ds_read_b128 v[124:127], v136
	ds_read_b128 v[128:131], v136 offset:1024
	ds_read_b128 v[132:135], v136 offset:2048
	ds_read_b128 v[136:139], v136 offset:3072
	ds_read_b128 v[140:143], v170
	ds_read_b128 v[144:147], v170 offset:1024
	ds_read_b128 v[156:159], v170 offset:2048
	ds_read_b128 v[170:173], v170 offset:3072
	s_add_u32 s62, s62, 0x40000
	s_addc_u32 s63, s63, 0
	s_mov_b32 m0, s20
	ds_read_b128 v[174:177], v208 offset:32768
	ds_read_b128 v[178:181], v208 offset:33792
	ds_read_b128 v[182:185], v208 offset:34816
	ds_read_b128 v[186:189], v208 offset:35840
	ds_read_b128 v[190:193], v208 offset:36864
	ds_read_b128 v[210:213], v208 offset:37888
	ds_read_b128 v[214:217], v208 offset:38912
	ds_read_b128 v[218:221], v208 offset:39936
	global_load_lds_dwordx4 v164, s[62:63]
	s_mov_b32 m0, s21
	s_nop 0
	global_load_lds_dwordx4 v162, s[62:63]
	s_waitcnt vmcnt(8)
	s_waitcnt lgkmcnt(0)
	s_barrier
	s_waitcnt lgkmcnt(0)
	v_mfma_f32_16x16x32_bf16 v[152:155], v[124:127], v[174:177], v[152:155]
	v_mfma_f32_16x16x32_bf16 v[148:151], v[132:135], v[174:177], v[148:151]
	v_mfma_f32_16x16x32_bf16 v[112:115], v[124:127], v[182:185], v[112:115]
	v_mfma_f32_16x16x32_bf16 v[108:111], v[132:135], v[182:185], v[108:111]
	v_mfma_f32_16x16x32_bf16 v[96:99], v[124:127], v[190:193], v[96:99]
	v_mfma_f32_16x16x32_bf16 v[92:95], v[132:135], v[190:193], v[92:95]
	v_mfma_f32_16x16x32_bf16 v[80:83], v[124:127], v[214:217], v[80:83]
	v_mfma_f32_16x16x32_bf16 v[76:79], v[132:135], v[214:217], v[76:79]
	v_mfma_f32_16x16x32_bf16 v[152:155], v[128:131], v[178:181], v[152:155]
	v_mfma_f32_16x16x32_bf16 v[148:151], v[136:139], v[178:181], v[148:151]
	v_mfma_f32_16x16x32_bf16 v[112:115], v[128:131], v[186:189], v[112:115]
	v_mfma_f32_16x16x32_bf16 v[108:111], v[136:139], v[186:189], v[108:111]
	v_mfma_f32_16x16x32_bf16 v[96:99], v[128:131], v[210:213], v[96:99]
	v_mfma_f32_16x16x32_bf16 v[92:95], v[136:139], v[210:213], v[92:95]
	v_mfma_f32_16x16x32_bf16 v[80:83], v[128:131], v[218:221], v[80:83]
	v_mfma_f32_16x16x32_bf16 v[76:79], v[136:139], v[218:221], v[76:79]
	v_mfma_f32_16x16x32_bf16 v[120:123], v[140:143], v[174:177], v[120:123]
	v_mfma_f32_16x16x32_bf16 v[116:119], v[156:159], v[174:177], v[116:119]
	v_mfma_f32_16x16x32_bf16 v[104:107], v[140:143], v[182:185], v[104:107]
	v_mfma_f32_16x16x32_bf16 v[100:103], v[156:159], v[182:185], v[100:103]
	v_mfma_f32_16x16x32_bf16 v[88:91], v[140:143], v[190:193], v[88:91]
	v_mfma_f32_16x16x32_bf16 v[84:87], v[156:159], v[190:193], v[84:87]
	v_mfma_f32_16x16x32_bf16 v[72:75], v[140:143], v[214:217], v[72:75]
	v_mfma_f32_16x16x32_bf16 v[68:71], v[156:159], v[214:217], v[68:71]
	v_mfma_f32_16x16x32_bf16 v[120:123], v[144:147], v[178:181], v[120:123]
	v_mfma_f32_16x16x32_bf16 v[116:119], v[170:173], v[178:181], v[116:119]
	v_mfma_f32_16x16x32_bf16 v[104:107], v[144:147], v[186:189], v[104:107]
	v_mfma_f32_16x16x32_bf16 v[100:103], v[170:173], v[186:189], v[100:103]
	v_mfma_f32_16x16x32_bf16 v[88:91], v[144:147], v[210:213], v[88:91]
	v_mfma_f32_16x16x32_bf16 v[84:87], v[170:173], v[210:213], v[84:87]
	v_mfma_f32_16x16x32_bf16 v[72:75], v[144:147], v[218:221], v[72:75]
	v_mfma_f32_16x16x32_bf16 v[68:71], v[170:173], v[218:221], v[68:71]
	s_barrier
	s_add_i32 s62, s73, s17
	v_lshl_add_u64 v[204:205], v[204:205], 0, s[34:35]
	s_mov_b32 m0, s62
	ds_read_b128 v[174:177], v208 offset:49152
	ds_read_b128 v[178:181], v208 offset:50176
	ds_read_b128 v[182:185], v208 offset:51200
	ds_read_b128 v[186:189], v208 offset:52224
	ds_read_b128 v[190:193], v208 offset:53248
	ds_read_b128 v[210:213], v208 offset:54272
	ds_read_b128 v[214:217], v208 offset:55296
	ds_read_b128 v[218:221], v208 offset:56320
	global_load_lds_dwordx4 v[204:205], off
	s_add_i32 m0, s62, 0x2000
	s_add_u32 s60, s60, 0x40080
	v_lshl_add_u64 v[204:205], v[206:207], 0, s[34:35]
	s_addc_u32 s61, s61, 0
	s_add_i32 s62, s74, s17
	global_load_lds_dwordx4 v[204:205], off
	s_mov_b32 m0, s62
	s_nop 0
	global_load_lds_dwordx4 v2, s[60:61]
	s_add_i32 m0, s62, 0x2000
	s_nop 0
	global_load_lds_dwordx4 v160, s[60:61]
	v_lshl_add_u64 v[204:205], v[222:223], 0, s[34:35]
	s_mov_b32 m0, s65
	s_nop 0
	global_load_lds_dwordx4 v[204:205], off
	v_lshl_add_u64 v[204:205], v[224:225], 0, s[34:35]
	s_mov_b32 m0, s66
	s_nop 0
	global_load_lds_dwordx4 v[204:205], off
	s_waitcnt vmcnt(8)
	s_waitcnt lgkmcnt(0)
	s_barrier
	s_waitcnt lgkmcnt(0)
	v_mfma_f32_16x16x32_bf16 v[64:67], v[124:127], v[174:177], v[64:67]
	v_mfma_f32_16x16x32_bf16 v[60:63], v[132:135], v[174:177], v[60:63]
	v_mfma_f32_16x16x32_bf16 v[48:51], v[124:127], v[182:185], v[48:51]
	v_mfma_f32_16x16x32_bf16 v[44:47], v[132:135], v[182:185], v[44:47]
	v_mfma_f32_16x16x32_bf16 v[32:35], v[124:127], v[190:193], v[32:35]
	v_mfma_f32_16x16x32_bf16 v[28:31], v[132:135], v[190:193], v[28:31]
	v_mfma_f32_16x16x32_bf16 v[16:19], v[124:127], v[214:217], v[16:19]
	v_mfma_f32_16x16x32_bf16 v[12:15], v[132:135], v[214:217], v[12:15]
	v_mfma_f32_16x16x32_bf16 v[64:67], v[128:131], v[178:181], v[64:67]
	v_mfma_f32_16x16x32_bf16 v[60:63], v[136:139], v[178:181], v[60:63]
	v_mfma_f32_16x16x32_bf16 v[48:51], v[128:131], v[186:189], v[48:51]
	v_mfma_f32_16x16x32_bf16 v[44:47], v[136:139], v[186:189], v[44:47]
	v_mfma_f32_16x16x32_bf16 v[32:35], v[128:131], v[210:213], v[32:35]
	v_mfma_f32_16x16x32_bf16 v[28:31], v[136:139], v[210:213], v[28:31]
	v_mfma_f32_16x16x32_bf16 v[16:19], v[128:131], v[218:221], v[16:19]
	v_mfma_f32_16x16x32_bf16 v[12:15], v[136:139], v[218:221], v[12:15]
	v_mfma_f32_16x16x32_bf16 v[56:59], v[140:143], v[174:177], v[56:59]
	v_mfma_f32_16x16x32_bf16 v[52:55], v[156:159], v[174:177], v[52:55]
	v_mfma_f32_16x16x32_bf16 v[40:43], v[140:143], v[182:185], v[40:43]
	v_mfma_f32_16x16x32_bf16 v[36:39], v[156:159], v[182:185], v[36:39]
	v_mfma_f32_16x16x32_bf16 v[24:27], v[140:143], v[190:193], v[24:27]
	v_mfma_f32_16x16x32_bf16 v[20:23], v[156:159], v[190:193], v[20:23]
	v_mfma_f32_16x16x32_bf16 v[8:11], v[140:143], v[214:217], v[8:11]
	v_mfma_f32_16x16x32_bf16 v[4:7], v[156:159], v[214:217], v[4:7]
	v_mfma_f32_16x16x32_bf16 v[56:59], v[144:147], v[178:181], v[56:59]
	v_mfma_f32_16x16x32_bf16 v[52:55], v[170:173], v[178:181], v[52:55]
	v_mfma_f32_16x16x32_bf16 v[40:43], v[144:147], v[186:189], v[40:43]
	v_mfma_f32_16x16x32_bf16 v[36:39], v[170:173], v[186:189], v[36:39]
	v_mfma_f32_16x16x32_bf16 v[24:27], v[144:147], v[210:213], v[24:27]
	v_mfma_f32_16x16x32_bf16 v[20:23], v[170:173], v[210:213], v[20:23]
	v_mfma_f32_16x16x32_bf16 v[8:11], v[144:147], v[218:221], v[8:11]
	v_mfma_f32_16x16x32_bf16 v[4:7], v[170:173], v[218:221], v[4:7]
	s_barrier
	s_add_u32 s42, s42, 0x100
	s_addc_u32 s43, s43, 0
	s_add_u32 s70, s70, 0x100
	s_addc_u32 s71, s71, 0
	s_cmp_gt_u32 s72, 13
	s_mov_b32 s60, s72
	s_cbranch_scc0 .LBB0_1411
	s_waitcnt vmcnt(0)
	s_and_b64 vcc, exec, s[50:51]
	s_cbranch_vccz .LBB0_1414
	s_barrier

; #define PG8_STAGE(bufoff, gbase, voff) do { _Pragma("unroll") for (int _i = 0; _i < 2; ++_i) \
;         __builtin_amdgcn_global_load_lds((const unsigned*)((const char*)(gbase) + (voff)[_i]), (PG8_LAS unsigned*)(lds + (bufoff) + ldsw + _i * 8192), 16, 0, 0); } while (0)
; #define PG8_LDA(dst, b, h) do { _Pragma("unroll") for (int m = 0; m < 4; ++m) _Pragma("unroll") for (int k = 0; k < 2; ++k) dst[m][k] = *(const PG8_LAS bf16x8*)(lds + PG8_SA(b, h) + aoff + m * 2048 + k * 1024); } while (0)
; #define PG8_LDB(dst, b, h) do { _Pragma("unroll") for (int n = 0; n < 2; ++n) _Pragma("unroll") for (int k = 0; k < 2; ++k) dst[n][k] = *(const PG8_LAS bf16x8*)(lds + PG8_SB(b, h) + boff + n * 2048 + k * 1024); } while (0)
; #define PG8_WAIT_V(n) asm volatile("s_waitcnt vmcnt(" #n ")" ::: "memory")
; #define PG8_WAIT_V8_UNLESS_FIRST(t) asm volatile("s_cmp_eq_u32 %0, 0\n\ts_cbranch_scc1 .Lpg8skip%=\n\ts_waitcnt vmcnt(8)\n.Lpg8skip%=:" :: "s"(t) : "scc", "memory")
; #define PG8_WAIT_L(n) asm volatile("s_waitcnt lgkmcnt(" #n ")" ::: "memory")
; #define PG8_BAR __builtin_amdgcn_s_barrier()
; template <class Epi, class Sched, bool ALIGN_EPI = false, bool SP2 = false, bool FP8 = false, bool ABLK = false>
; __device__ __forceinline__ void gemm_phase(PG8_LAS unsigned char* lds, const Gemm g, const Sched& S, const Epi& E) {
;     ...
;             PG8_LDB(B0, 0, 0); PG8_LDB(B1, 0, 1); PG8_SCHED; PG8_LDA(At, 0, 0); PG8_STAGE(PG8_SA(1, 1), a1 + hstepA, voffA);
;             PG8_WAIT_V8_UNLESS_FIRST(t); PG8_WAIT_L(0); PG8_BAR; PG8_MMA(0, 0, At, B0); PG8_MMA(0, 1, At, B1); PG8_BAR; PG8_SCHED;
;             PG8_LDA(At, 0, 1); PG8_STAGE(PG8_SB(0, 0), b2, voffB); PG8_STAGE(PG8_SB(0, 1), b2 + hstep, voffB); PG8_STAGE(PG8_SA(0, 0), a2, voffA);
;             PG8_WAIT_V8_UNLESS_FIRST(t); PG8_WAIT_L(0); PG8_BAR; PG8_MMA(1, 0, At, B0); PG8_MMA(1, 1, At, B1); PG8_BAR; PG8_SCHED;
;             PG8_LDB(B0, 1, 0); PG8_LDB(B1, 1, 1); PG8_SCHED; PG8_LDA(At, 1, 0); PG8_STAGE(PG8_SA(0, 1), a2 + hstepA, voffA);
;             PG8_WAIT_V(8); PG8_WAIT_L(0); PG8_BAR; PG8_MMA(0, 0, At, B0); PG8_MMA(0, 1, At, B1); PG8_BAR; PG8_SCHED;
;             PG8_LDA(At, 1, 1); PG8_STAGE(PG8_SB(1, 0), b3, voffB); PG8_STAGE(PG8_SB(1, 1), b3 + hstep, voffB); PG8_STAGE(PG8_SA(1, 0), a3, voffA);
;             PG8_WAIT_V(8); PG8_WAIT_L(0); PG8_BAR; PG8_MMA(1, 0, At, B0); PG8_MMA(1, 1, At, B1); PG8_BAR; PG8_SCHED;
.Lpg8skip8:
	s_waitcnt lgkmcnt(0)
	s_barrier
	s_waitcnt lgkmcnt(0)
	v_mfma_scale_f32_16x16x128_f8f6f4 v[160:163], v[28:35], v[174:181], v[160:163], v245, v245 op_sel_hi:[0,0,0]
	v_mfma_scale_f32_16x16x128_f8f6f4 v[156:159], v[20:27], v[174:181], v[156:159], v245, v245 op_sel_hi:[0,0,0]
	v_mfma_scale_f32_16x16x128_f8f6f4 v[144:147], v[28:35], v[186:193], v[144:147], v245, v245 op_sel_hi:[0,0,0]
	v_mfma_scale_f32_16x16x128_f8f6f4 v[140:143], v[20:27], v[186:193], v[140:143], v245, v245 op_sel_hi:[0,0,0]
	v_mfma_scale_f32_16x16x128_f8f6f4 v[128:131], v[28:35], v[208:215], v[128:131], v245, v245 op_sel_hi:[0,0,0]
	v_mfma_scale_f32_16x16x128_f8f6f4 v[124:127], v[20:27], v[208:215], v[124:127], v245, v245 op_sel_hi:[0,0,0]
	v_mfma_scale_f32_16x16x128_f8f6f4 v[112:115], v[28:35], v[216:223], v[112:115], v245, v245 op_sel_hi:[0,0,0]
	v_mfma_scale_f32_16x16x128_f8f6f4 v[108:111], v[20:27], v[216:223], v[108:111], v245, v245 op_sel_hi:[0,0,0]
	v_mfma_scale_f32_16x16x128_f8f6f4 v[152:155], v[12:19], v[174:181], v[152:155], v245, v245 op_sel_hi:[0,0,0]
	v_mfma_scale_f32_16x16x128_f8f6f4 v[148:151], v[4:11], v[174:181], v[148:151], v245, v245 op_sel_hi:[0,0,0]
	v_mfma_scale_f32_16x16x128_f8f6f4 v[136:139], v[12:19], v[186:193], v[136:139], v245, v245 op_sel_hi:[0,0,0]
	v_mfma_scale_f32_16x16x128_f8f6f4 v[132:135], v[4:11], v[186:193], v[132:135], v245, v245 op_sel_hi:[0,0,0]
	v_mfma_scale_f32_16x16x128_f8f6f4 v[120:123], v[12:19], v[208:215], v[120:123], v245, v245 op_sel_hi:[0,0,0]
	v_mfma_scale_f32_16x16x128_f8f6f4 v[116:119], v[4:11], v[208:215], v[116:119], v245, v245 op_sel_hi:[0,0,0]
	v_mfma_scale_f32_16x16x128_f8f6f4 v[104:107], v[12:19], v[216:223], v[104:107], v245, v245 op_sel_hi:[0,0,0]
	v_mfma_scale_f32_16x16x128_f8f6f4 v[100:103], v[4:11], v[216:223], v[100:103], v245, v245 op_sel_hi:[0,0,0]
	s_barrier
	s_add_i32 s70, s70, s17
	v_lshl_add_u64 v[174:175], s[58:59], 0, v[2:3]
	s_mov_b32 m0, s70
	ds_read_b128 v[186:189], v184 offset:16384
	ds_read_b128 v[190:193], v184 offset:17408
	ds_read_b128 v[208:211], v184 offset:18432
	ds_read_b128 v[212:215], v184 offset:19456
	ds_read_b128 v[216:219], v184 offset:20480
	ds_read_b128 v[220:223], v184 offset:21504
	ds_read_b128 v[228:231], v184 offset:22528
	ds_read_b128 v[232:235], v184 offset:23552
	global_load_lds_dwordx4 v2, s[58:59]
	s_add_i32 m0, s70, 0x2000
	s_add_u32 s72, s58, 0x20000
	v_lshl_add_u64 v[176:177], s[58:59], 0, v[164:165]
	s_addc_u32 s73, s59, 0
	s_add_i32 s70, s71, s17
	global_load_lds_dwordx4 v164, s[58:59]
	s_mov_b32 m0, s70
	v_lshl_add_u64 v[180:181], s[60:61], 0, v[166:167]
	global_load_lds_dwordx4 v2, s[72:73]
	s_add_i32 m0, s70, 0x2000
	s_nop 0
	global_load_lds_dwordx4 v164, s[72:73]
	v_lshl_add_u64 v[178:179], s[60:61], 0, v[168:169]
	s_mov_b32 m0, s18
	s_nop 0
	global_load_lds_dwordx4 v168, s[60:61]
	s_mov_b32 m0, s19
	s_nop 0
	global_load_lds_dwordx4 v166, s[60:61]
	s_cmp_eq_u32 s69, 0
	s_cbranch_scc1 .Lpg8skip9
	s_waitcnt vmcnt(8)
.Lpg8skip9:
	s_waitcnt lgkmcnt(0)
	s_barrier
	s_waitcnt lgkmcnt(0)
	v_mfma_scale_f32_16x16x128_f8f6f4 v[96:99], v[28:35], v[186:193], v[96:99], v245, v245 op_sel_hi:[0,0,0]
	v_mfma_scale_f32_16x16x128_f8f6f4 v[92:95], v[20:27], v[186:193], v[92:95], v245, v245 op_sel_hi:[0,0,0]
	v_mfma_scale_f32_16x16x128_f8f6f4 v[80:83], v[28:35], v[208:215], v[80:83], v245, v245 op_sel_hi:[0,0,0]
	v_mfma_scale_f32_16x16x128_f8f6f4 v[76:79], v[20:27], v[208:215], v[76:79], v245, v245 op_sel_hi:[0,0,0]
	v_mfma_scale_f32_16x16x128_f8f6f4 v[64:67], v[28:35], v[216:223], v[64:67], v245, v245 op_sel_hi:[0,0,0]
	v_mfma_scale_f32_16x16x128_f8f6f4 v[60:63], v[20:27], v[216:223], v[60:63], v245, v245 op_sel_hi:[0,0,0]
	v_mfma_scale_f32_16x16x128_f8f6f4 v[48:51], v[28:35], v[228:235], v[48:51], v245, v245 op_sel_hi:[0,0,0]
	v_mfma_scale_f32_16x16x128_f8f6f4 v[44:47], v[20:27], v[228:235], v[44:47], v245, v245 op_sel_hi:[0,0,0]
	v_mfma_scale_f32_16x16x128_f8f6f4 v[88:91], v[12:19], v[186:193], v[88:91], v245, v245 op_sel_hi:[0,0,0]
	v_mfma_scale_f32_16x16x128_f8f6f4 v[84:87], v[4:11], v[186:193], v[84:87], v245, v245 op_sel_hi:[0,0,0]
	v_mfma_scale_f32_16x16x128_f8f6f4 v[72:75], v[12:19], v[208:215], v[72:75], v245, v245 op_sel_hi:[0,0,0]
	v_mfma_scale_f32_16x16x128_f8f6f4 v[68:71], v[4:11], v[208:215], v[68:71], v245, v245 op_sel_hi:[0,0,0]
	v_mfma_scale_f32_16x16x128_f8f6f4 v[56:59], v[12:19], v[216:223], v[56:59], v245, v245 op_sel_hi:[0,0,0]
	v_mfma_scale_f32_16x16x128_f8f6f4 v[52:55], v[4:11], v[216:223], v[52:55], v245, v245 op_sel_hi:[0,0,0]
	v_mfma_scale_f32_16x16x128_f8f6f4 v[40:43], v[12:19], v[228:235], v[40:43], v245, v245 op_sel_hi:[0,0,0]
	v_mfma_scale_f32_16x16x128_f8f6f4 v[36:39], v[4:11], v[228:235], v[36:39], v245, v245 op_sel_hi:[0,0,0]
	s_barrier
	s_add_i32 s70, 0, 0x18000
	s_add_i32 s71, 0, 0x1c000
	v_add_u32_e32 v16, s70, v183
	v_add_u32_e32 v32, s71, v183
	ds_read_b128 v[4:7], v16
	ds_read_b128 v[8:11], v16 offset:1024
	ds_read_b128 v[12:15], v16 offset:2048
	ds_read_b128 v[16:19], v16 offset:3072
	ds_read_b128 v[20:23], v32
	ds_read_b128 v[24:27], v32 offset:1024
	ds_read_b128 v[28:31], v32 offset:2048
	ds_read_b128 v[32:35], v32 offset:3072
	s_add_u32 s60, s60, 0x20000
	s_addc_u32 s61, s61, 0
	s_mov_b32 m0, s20
	ds_read_b128 v[186:189], v184 offset:32768
	ds_read_b128 v[190:193], v184 offset:33792
	ds_read_b128 v[208:211], v184 offset:34816
	ds_read_b128 v[212:215], v184 offset:35840
	ds_read_b128 v[216:219], v184 offset:36864
	ds_read_b128 v[220:223], v184 offset:37888
	ds_read_b128 v[228:231], v184 offset:38912
	ds_read_b128 v[232:235], v184 offset:39936
	global_load_lds_dwordx4 v168, s[60:61]
	s_mov_b32 m0, s21
	s_nop 0
	global_load_lds_dwordx4 v166, s[60:61]
	s_waitcnt vmcnt(8)
	s_waitcnt lgkmcnt(0)
	s_barrier
; #define PG8_BAR __builtin_amdgcn_s_barrier()
; template <class Epi, class Sched, bool ALIGN_EPI = false, bool SP2 = false, bool FP8 = false, bool ABLK = false>
; __device__ __forceinline__ void gemm_phase(PG8_LAS unsigned char* lds, const Gemm g, const Sched& S, const Epi& E) {
;     ...
;             PG8_LDB(B0, 0, 0); PG8_LDB(B1, 0, 1); PG8_SCHED; PG8_LDA(At, 0, 0); PG8_STAGE(PG8_SA(1, 1), a1 + hstepA, voffA);
;             PG8_WAIT_V8_UNLESS_FIRST(t); PG8_WAIT_L(0); PG8_BAR; PG8_MMA(0, 0, At, B0); PG8_MMA(0, 1, At, B1); PG8_BAR; PG8_SCHED;
;             PG8_LDA(At, 0, 1); PG8_STAGE(PG8_SB(0, 0), b2, voffB); PG8_STAGE(PG8_SB(0, 1), b2 + hstep, voffB); PG8_STAGE(PG8_SA(0, 0), a2, voffA);
;             PG8_WAIT_V8_UNLESS_FIRST(t); PG8_WAIT_L(0); PG8_BAR; PG8_MMA(1, 0, At, B0); PG8_MMA(1, 1, At, B1); PG8_BAR; PG8_SCHED;
;             PG8_LDB(B0, 1, 0); PG8_LDB(B1, 1, 1); PG8_SCHED; PG8_LDA(At, 1, 0); PG8_STAGE(PG8_SA(0, 1), a2 + hstepA, voffA);
;             PG8_WAIT_V(8); PG8_WAIT_L(0); PG8_BAR; PG8_MMA(0, 0, At, B0); PG8_MMA(0, 1, At, B1); PG8_BAR; PG8_SCHED;
;             PG8_LDA(At, 1, 1); PG8_STAGE(PG8_SB(1, 0), b3, voffB); PG8_STAGE(PG8_SB(1, 1), b3 + hstep, voffB); PG8_STAGE(PG8_SA(1, 0), a3, voffA);
;             PG8_WAIT_V(8); PG8_WAIT_L(0); PG8_BAR; PG8_MMA(1, 0, At, B0); PG8_MMA(1, 1, At, B1); PG8_BAR; PG8_SCHED;
;             } else {
;             PG8_LDB(B0, 0, 0); PG8_SCHED; PG8_LDA(At, 0, 0); PG8_STAGE(PG8_SA(1, 1), a1 + hstepA, voffA);
;             PG8_WAIT_L(8); PG8_BAR; PG8_WAIT_L(0); PG8_MMA(0, 0, At, B0); PG8_BAR; PG8_SCHED;
;             PG8_LDB(B1, 0, 1); PG8_STAGE(PG8_SB(0, 0), b2, voffB);
;             PG8_BAR; PG8_WAIT_L(0); PG8_MMA(0, 1, At, B1); PG8_BAR;
;             PG8_LDA(At, 0, 1); PG8_STAGE(PG8_SA(0, 0), a2, voffA);
;             PG8_BAR; PG8_WAIT_L(0); PG8_MMA(1, 0, At, B0); PG8_BAR; PG8_SCHED;
;             PG8_STAGE(PG8_SB(0, 1), b2 + hstep, voffB);
;             PG8_WAIT_V(6); PG8_BAR; PG8_MMA(1, 1, At, B1); PG8_BAR;
;             PG8_LDB(B0, 1, 0); PG8_SCHED; PG8_LDA(At, 1, 0); PG8_STAGE(PG8_SA(0, 1), a2 + hstepA, voffA);
;             PG8_WAIT_L(8); PG8_BAR; PG8_WAIT_L(0); PG8_MMA(0, 0, At, B0); PG8_BAR; PG8_SCHED;
;             PG8_LDB(B1, 1, 1); PG8_STAGE(PG8_SB(1, 0), b3, voffB);
;             PG8_BAR; PG8_WAIT_L(0); PG8_MMA(0, 1, At, B1); PG8_BAR;
;             PG8_LDA(At, 1, 1); PG8_STAGE(PG8_SA(1, 0), a3, voffA);
	s_waitcnt lgkmcnt(0)
	v_mfma_scale_f32_16x16x128_f8f6f4 v[160:163], v[4:11], v[186:193], v[160:163], v245, v245 op_sel_hi:[0,0,0]
	v_mfma_scale_f32_16x16x128_f8f6f4 v[156:159], v[12:19], v[186:193], v[156:159], v245, v245 op_sel_hi:[0,0,0]
	v_mfma_scale_f32_16x16x128_f8f6f4 v[144:147], v[4:11], v[208:215], v[144:147], v245, v245 op_sel_hi:[0,0,0]
	v_mfma_scale_f32_16x16x128_f8f6f4 v[140:143], v[12:19], v[208:215], v[140:143], v245, v245 op_sel_hi:[0,0,0]
	v_mfma_scale_f32_16x16x128_f8f6f4 v[128:131], v[4:11], v[216:223], v[128:131], v245, v245 op_sel_hi:[0,0,0]
	v_mfma_scale_f32_16x16x128_f8f6f4 v[124:127], v[12:19], v[216:223], v[124:127], v245, v245 op_sel_hi:[0,0,0]
	v_mfma_scale_f32_16x16x128_f8f6f4 v[112:115], v[4:11], v[228:235], v[112:115], v245, v245 op_sel_hi:[0,0,0]
	v_mfma_scale_f32_16x16x128_f8f6f4 v[108:111], v[12:19], v[228:235], v[108:111], v245, v245 op_sel_hi:[0,0,0]
	v_mfma_scale_f32_16x16x128_f8f6f4 v[152:155], v[20:27], v[186:193], v[152:155], v245, v245 op_sel_hi:[0,0,0]
	v_mfma_scale_f32_16x16x128_f8f6f4 v[148:151], v[28:35], v[186:193], v[148:151], v245, v245 op_sel_hi:[0,0,0]
	v_mfma_scale_f32_16x16x128_f8f6f4 v[136:139], v[20:27], v[208:215], v[136:139], v245, v245 op_sel_hi:[0,0,0]
	v_mfma_scale_f32_16x16x128_f8f6f4 v[132:135], v[28:35], v[208:215], v[132:135], v245, v245 op_sel_hi:[0,0,0]
	v_mfma_scale_f32_16x16x128_f8f6f4 v[120:123], v[20:27], v[216:223], v[120:123], v245, v245 op_sel_hi:[0,0,0]
	v_mfma_scale_f32_16x16x128_f8f6f4 v[116:119], v[28:35], v[216:223], v[116:119], v245, v245 op_sel_hi:[0,0,0]
	v_mfma_scale_f32_16x16x128_f8f6f4 v[104:107], v[20:27], v[228:235], v[104:107], v245, v245 op_sel_hi:[0,0,0]
	v_mfma_scale_f32_16x16x128_f8f6f4 v[100:103], v[28:35], v[228:235], v[100:103], v245, v245 op_sel_hi:[0,0,0]
	s_barrier
	s_add_i32 s60, s70, s17
	v_lshl_add_u64 v[174:175], v[174:175], 0, s[34:35]
	s_mov_b32 m0, s60
	ds_read_b128 v[186:189], v184 offset:49152
	ds_read_b128 v[190:193], v184 offset:50176
	ds_read_b128 v[208:211], v184 offset:51200
	ds_read_b128 v[212:215], v184 offset:52224
	ds_read_b128 v[216:219], v184 offset:53248
	ds_read_b128 v[220:223], v184 offset:54272
	ds_read_b128 v[228:231], v184 offset:55296
	ds_read_b128 v[232:235], v184 offset:56320
	global_load_lds_dwordx4 v[174:175], off
	s_add_i32 m0, s60, 0x2000
	s_add_u32 s58, s58, 0x20080
	v_lshl_add_u64 v[174:175], v[176:177], 0, s[34:35]
	s_addc_u32 s59, s59, 0
	s_add_i32 s60, s71, s17
	global_load_lds_dwordx4 v[174:175], off
	s_mov_b32 m0, s60
	s_nop 0
	global_load_lds_dwordx4 v2, s[58:59]
	s_add_i32 m0, s60, 0x2000
	s_nop 0
	global_load_lds_dwordx4 v164, s[58:59]
	v_lshl_add_u64 v[174:175], v[178:179], 0, s[34:35]
	s_mov_b32 m0, s62
	s_nop 0
	global_load_lds_dwordx4 v[174:175], off
	v_lshl_add_u64 v[174:175], v[180:181], 0, s[34:35]
	s_mov_b32 m0, s63
	s_nop 0
	global_load_lds_dwordx4 v[174:175], off
	s_waitcnt vmcnt(8)
	s_waitcnt lgkmcnt(0)
	s_barrier
	s_waitcnt lgkmcnt(0)
	v_mfma_scale_f32_16x16x128_f8f6f4 v[96:99], v[4:11], v[186:193], v[96:99], v245, v245 op_sel_hi:[0,0,0]
	v_mfma_scale_f32_16x16x128_f8f6f4 v[92:95], v[12:19], v[186:193], v[92:95], v245, v245 op_sel_hi:[0,0,0]
	v_mfma_scale_f32_16x16x128_f8f6f4 v[80:83], v[4:11], v[208:215], v[80:83], v245, v245 op_sel_hi:[0,0,0]
	v_mfma_scale_f32_16x16x128_f8f6f4 v[76:79], v[12:19], v[208:215], v[76:79], v245, v245 op_sel_hi:[0,0,0]
	v_mfma_scale_f32_16x16x128_f8f6f4 v[64:67], v[4:11], v[216:223], v[64:67], v245, v245 op_sel_hi:[0,0,0]
	v_mfma_scale_f32_16x16x128_f8f6f4 v[60:63], v[12:19], v[216:223], v[60:63], v245, v245 op_sel_hi:[0,0,0]
	v_mfma_scale_f32_16x16x128_f8f6f4 v[48:51], v[4:11], v[228:235], v[48:51], v245, v245 op_sel_hi:[0,0,0]
	v_mfma_scale_f32_16x16x128_f8f6f4 v[44:47], v[12:19], v[228:235], v[44:47], v245, v245 op_sel_hi:[0,0,0]
	v_mfma_scale_f32_16x16x128_f8f6f4 v[88:91], v[20:27], v[186:193], v[88:91], v245, v245 op_sel_hi:[0,0,0]
	v_mfma_scale_f32_16x16x128_f8f6f4 v[84:87], v[28:35], v[186:193], v[84:87], v245, v245 op_sel_hi:[0,0,0]
	v_mfma_scale_f32_16x16x128_f8f6f4 v[72:75], v[20:27], v[208:215], v[72:75], v245, v245 op_sel_hi:[0,0,0]
	v_mfma_scale_f32_16x16x128_f8f6f4 v[68:71], v[28:35], v[208:215], v[68:71], v245, v245 op_sel_hi:[0,0,0]
	v_mfma_scale_f32_16x16x128_f8f6f4 v[56:59], v[20:27], v[216:223], v[56:59], v245, v245 op_sel_hi:[0,0,0]
	v_mfma_scale_f32_16x16x128_f8f6f4 v[52:55], v[28:35], v[216:223], v[52:55], v245, v245 op_sel_hi:[0,0,0]
	v_mfma_scale_f32_16x16x128_f8f6f4 v[40:43], v[20:27], v[228:235], v[40:43], v245, v245 op_sel_hi:[0,0,0]
	v_mfma_scale_f32_16x16x128_f8f6f4 v[36:39], v[28:35], v[228:235], v[36:39], v245, v245 op_sel_hi:[0,0,0]
	s_barrier
	s_add_u32 s56, s56, 0x100
	s_addc_u32 s57, s57, 0
	s_add_u32 s67, s67, 0x100
	s_addc_u32 s68, s68, 0
	s_cmp_gt_u32 s69, 5
	s_mov_b32 s58, s69
	s_cbranch_scc0 .LBB0_1498
	s_waitcnt vmcnt(0)
	s_nop 15
	s_nop 15
	s_and_b64 vcc, exec, s[46:47]
	s_cbranch_vccz .LBB0_1501
	s_barrier

; #define PG8_STAGE(bufoff, gbase, voff) do { _Pragma("unroll") for (int _i = 0; _i < 2; ++_i) \
;         __builtin_amdgcn_global_load_lds((const unsigned*)((const char*)(gbase) + (voff)[_i]), (PG8_LAS unsigned*)(lds + (bufoff) + ldsw + _i * 8192), 16, 0, 0); } while (0)
; #define PG8_LDA(dst, b, h) do { _Pragma("unroll") for (int m = 0; m < 4; ++m) _Pragma("unroll") for (int k = 0; k < 2; ++k) dst[m][k] = *(const PG8_LAS bf16x8*)(lds + PG8_SA(b, h) + aoff + m * 2048 + k * 1024); } while (0)
; #define PG8_LDB(dst, b, h) do { _Pragma("unroll") for (int n = 0; n < 2; ++n) _Pragma("unroll") for (int k = 0; k < 2; ++k) dst[n][k] = *(const PG8_LAS bf16x8*)(lds + PG8_SB(b, h) + boff + n * 2048 + k * 1024); } while (0)
; #define PG8_WAIT_V(n) asm volatile("s_waitcnt vmcnt(" #n ")" ::: "memory")
; #define PG8_WAIT_V8_UNLESS_FIRST(t) asm volatile("s_cmp_eq_u32 %0, 0\n\ts_cbranch_scc1 .Lpg8skip%=\n\ts_waitcnt vmcnt(8)\n.Lpg8skip%=:" :: "s"(t) : "scc", "memory")
; #define PG8_WAIT_L(n) asm volatile("s_waitcnt lgkmcnt(" #n ")" ::: "memory")
; #define PG8_BAR __builtin_amdgcn_s_barrier()
; template <class Epi, class Sched, bool ALIGN_EPI = false, bool SP2 = false, bool FP8 = false, bool ABLK = false>
; __device__ __forceinline__ void gemm_phase(PG8_LAS unsigned char* lds, const Gemm g, const Sched& S, const Epi& E) {
;     ...
;             PG8_LDB(B0, 0, 0); PG8_LDB(B1, 0, 1); PG8_SCHED; PG8_LDA(At, 0, 0); PG8_STAGE(PG8_SA(1, 1), a1 + hstepA, voffA);
;             PG8_WAIT_V8_UNLESS_FIRST(t); PG8_WAIT_L(0); PG8_BAR; PG8_MMA(0, 0, At, B0); PG8_MMA(0, 1, At, B1); PG8_BAR; PG8_SCHED;
;             PG8_LDA(At, 0, 1); PG8_STAGE(PG8_SB(0, 0), b2, voffB); PG8_STAGE(PG8_SB(0, 1), b2 + hstep, voffB); PG8_STAGE(PG8_SA(0, 0), a2, voffA);
;             PG8_WAIT_V8_UNLESS_FIRST(t); PG8_WAIT_L(0); PG8_BAR; PG8_MMA(1, 0, At, B0); PG8_MMA(1, 1, At, B1); PG8_BAR; PG8_SCHED;
;             PG8_LDB(B0, 1, 0); PG8_LDB(B1, 1, 1); PG8_SCHED; PG8_LDA(At, 1, 0); PG8_STAGE(PG8_SA(0, 1), a2 + hstepA, voffA);
;             PG8_WAIT_V(8); PG8_WAIT_L(0); PG8_BAR; PG8_MMA(0, 0, At, B0); PG8_MMA(0, 1, At, B1); PG8_BAR; PG8_SCHED;
;             PG8_LDA(At, 1, 1); PG8_STAGE(PG8_SB(1, 0), b3, voffB); PG8_STAGE(PG8_SB(1, 1), b3 + hstep, voffB); PG8_STAGE(PG8_SA(1, 0), a3, voffA);
;             PG8_WAIT_V(8); PG8_WAIT_L(0); PG8_BAR; PG8_MMA(1, 0, At, B0); PG8_MMA(1, 1, At, B1); PG8_BAR; PG8_SCHED;
.Lpg8skip10:
	s_waitcnt lgkmcnt(0)
	s_barrier
	s_waitcnt lgkmcnt(0)
	v_mfma_scale_f32_16x16x128_f8f6f4 v[160:163], v[28:35], v[174:181], v[160:163], v245, v245 op_sel_hi:[0,0,0]
	v_mfma_scale_f32_16x16x128_f8f6f4 v[156:159], v[20:27], v[174:181], v[156:159], v245, v245 op_sel_hi:[0,0,0]
	v_mfma_scale_f32_16x16x128_f8f6f4 v[144:147], v[28:35], v[182:189], v[144:147], v245, v245 op_sel_hi:[0,0,0]
	v_mfma_scale_f32_16x16x128_f8f6f4 v[140:143], v[20:27], v[182:189], v[140:143], v245, v245 op_sel_hi:[0,0,0]
	v_mfma_scale_f32_16x16x128_f8f6f4 v[128:131], v[28:35], v[210:217], v[128:131], v245, v245 op_sel_hi:[0,0,0]
	v_mfma_scale_f32_16x16x128_f8f6f4 v[124:127], v[20:27], v[210:217], v[124:127], v245, v245 op_sel_hi:[0,0,0]
	v_mfma_scale_f32_16x16x128_f8f6f4 v[112:115], v[28:35], v[218:225], v[112:115], v245, v245 op_sel_hi:[0,0,0]
	v_mfma_scale_f32_16x16x128_f8f6f4 v[108:111], v[20:27], v[218:225], v[108:111], v245, v245 op_sel_hi:[0,0,0]
	v_mfma_scale_f32_16x16x128_f8f6f4 v[152:155], v[12:19], v[174:181], v[152:155], v245, v245 op_sel_hi:[0,0,0]
	v_mfma_scale_f32_16x16x128_f8f6f4 v[148:151], v[4:11], v[174:181], v[148:151], v245, v245 op_sel_hi:[0,0,0]
	v_mfma_scale_f32_16x16x128_f8f6f4 v[136:139], v[12:19], v[182:189], v[136:139], v245, v245 op_sel_hi:[0,0,0]
	v_mfma_scale_f32_16x16x128_f8f6f4 v[132:135], v[4:11], v[182:189], v[132:135], v245, v245 op_sel_hi:[0,0,0]
	v_mfma_scale_f32_16x16x128_f8f6f4 v[120:123], v[12:19], v[210:217], v[120:123], v245, v245 op_sel_hi:[0,0,0]
	v_mfma_scale_f32_16x16x128_f8f6f4 v[116:119], v[4:11], v[210:217], v[116:119], v245, v245 op_sel_hi:[0,0,0]
	v_mfma_scale_f32_16x16x128_f8f6f4 v[104:107], v[12:19], v[218:225], v[104:107], v245, v245 op_sel_hi:[0,0,0]
	v_mfma_scale_f32_16x16x128_f8f6f4 v[100:103], v[4:11], v[218:225], v[100:103], v245, v245 op_sel_hi:[0,0,0]
	s_barrier
	s_add_i32 s73, s73, s17
	v_lshl_add_u64 v[174:175], s[60:61], 0, v[2:3]
	s_mov_b32 m0, s73
	ds_read_b128 v[182:185], v208 offset:16384
	ds_read_b128 v[186:189], v208 offset:17408
	ds_read_b128 v[210:213], v208 offset:18432
	ds_read_b128 v[214:217], v208 offset:19456
	ds_read_b128 v[218:221], v208 offset:20480
	ds_read_b128 v[222:225], v208 offset:21504
	ds_read_b128 v[228:231], v208 offset:22528
	ds_read_b128 v[232:235], v208 offset:23552
	global_load_lds_dwordx4 v2, s[60:61]
	s_add_i32 m0, s73, 0x2000
	s_add_u32 s76, s60, 0x20000
	v_lshl_add_u64 v[176:177], s[60:61], 0, v[164:165]
	s_addc_u32 s77, s61, 0
	s_add_i32 s73, s74, s17
	global_load_lds_dwordx4 v164, s[60:61]
	s_mov_b32 m0, s73
	v_lshl_add_u64 v[180:181], s[62:63], 0, v[166:167]
	global_load_lds_dwordx4 v2, s[76:77]
	s_add_i32 m0, s73, 0x2000
	s_nop 0
	global_load_lds_dwordx4 v164, s[76:77]
	v_lshl_add_u64 v[178:179], s[62:63], 0, v[168:169]
	s_mov_b32 m0, s18
	s_nop 0
	global_load_lds_dwordx4 v168, s[62:63]
	s_mov_b32 m0, s19
	s_nop 0
	global_load_lds_dwordx4 v166, s[62:63]
	s_cmp_eq_u32 s72, 0
	s_cbranch_scc1 .Lpg8skip11
	s_waitcnt vmcnt(8)
.Lpg8skip11:
	s_waitcnt lgkmcnt(0)
	s_barrier
	s_waitcnt lgkmcnt(0)
	v_mfma_scale_f32_16x16x128_f8f6f4 v[96:99], v[28:35], v[182:189], v[96:99], v245, v245 op_sel_hi:[0,0,0]
	v_mfma_scale_f32_16x16x128_f8f6f4 v[92:95], v[20:27], v[182:189], v[92:95], v245, v245 op_sel_hi:[0,0,0]
	v_mfma_scale_f32_16x16x128_f8f6f4 v[80:83], v[28:35], v[210:217], v[80:83], v245, v245 op_sel_hi:[0,0,0]
	v_mfma_scale_f32_16x16x128_f8f6f4 v[76:79], v[20:27], v[210:217], v[76:79], v245, v245 op_sel_hi:[0,0,0]
	v_mfma_scale_f32_16x16x128_f8f6f4 v[64:67], v[28:35], v[218:225], v[64:67], v245, v245 op_sel_hi:[0,0,0]
	v_mfma_scale_f32_16x16x128_f8f6f4 v[60:63], v[20:27], v[218:225], v[60:63], v245, v245 op_sel_hi:[0,0,0]
	v_mfma_scale_f32_16x16x128_f8f6f4 v[48:51], v[28:35], v[228:235], v[48:51], v245, v245 op_sel_hi:[0,0,0]
	v_mfma_scale_f32_16x16x128_f8f6f4 v[44:47], v[20:27], v[228:235], v[44:47], v245, v245 op_sel_hi:[0,0,0]
	v_mfma_scale_f32_16x16x128_f8f6f4 v[88:91], v[12:19], v[182:189], v[88:91], v245, v245 op_sel_hi:[0,0,0]
	v_mfma_scale_f32_16x16x128_f8f6f4 v[84:87], v[4:11], v[182:189], v[84:87], v245, v245 op_sel_hi:[0,0,0]
	v_mfma_scale_f32_16x16x128_f8f6f4 v[72:75], v[12:19], v[210:217], v[72:75], v245, v245 op_sel_hi:[0,0,0]
	v_mfma_scale_f32_16x16x128_f8f6f4 v[68:71], v[4:11], v[210:217], v[68:71], v245, v245 op_sel_hi:[0,0,0]
	v_mfma_scale_f32_16x16x128_f8f6f4 v[56:59], v[12:19], v[218:225], v[56:59], v245, v245 op_sel_hi:[0,0,0]
	v_mfma_scale_f32_16x16x128_f8f6f4 v[52:55], v[4:11], v[218:225], v[52:55], v245, v245 op_sel_hi:[0,0,0]
	v_mfma_scale_f32_16x16x128_f8f6f4 v[40:43], v[12:19], v[228:235], v[40:43], v245, v245 op_sel_hi:[0,0,0]
	v_mfma_scale_f32_16x16x128_f8f6f4 v[36:39], v[4:11], v[228:235], v[36:39], v245, v245 op_sel_hi:[0,0,0]
	s_barrier
	s_add_i32 s73, 0, 0x18000
	s_add_i32 s74, 0, 0x1c000
	v_add_u32_e32 v16, s73, v195
	v_add_u32_e32 v32, s74, v195
	ds_read_b128 v[4:7], v16
	ds_read_b128 v[8:11], v16 offset:1024
	ds_read_b128 v[12:15], v16 offset:2048
	ds_read_b128 v[16:19], v16 offset:3072
	ds_read_b128 v[20:23], v32
	ds_read_b128 v[24:27], v32 offset:1024
	ds_read_b128 v[28:31], v32 offset:2048
	ds_read_b128 v[32:35], v32 offset:3072
	s_add_u32 s62, s62, 0x20000
	s_addc_u32 s63, s63, 0
	s_mov_b32 m0, s20
	ds_read_b128 v[182:185], v208 offset:32768
	ds_read_b128 v[186:189], v208 offset:33792
	ds_read_b128 v[210:213], v208 offset:34816
	ds_read_b128 v[214:217], v208 offset:35840
	ds_read_b128 v[218:221], v208 offset:36864
	ds_read_b128 v[222:225], v208 offset:37888
	ds_read_b128 v[228:231], v208 offset:38912
	ds_read_b128 v[232:235], v208 offset:39936
	global_load_lds_dwordx4 v168, s[62:63]
	s_mov_b32 m0, s21
	s_nop 0
	global_load_lds_dwordx4 v166, s[62:63]
	s_waitcnt vmcnt(8)
	s_waitcnt lgkmcnt(0)
	s_barrier
; #define PG8_BAR __builtin_amdgcn_s_barrier()
; template <class Epi, class Sched, bool ALIGN_EPI = false, bool SP2 = false, bool FP8 = false, bool ABLK = false>
; __device__ __forceinline__ void gemm_phase(PG8_LAS unsigned char* lds, const Gemm g, const Sched& S, const Epi& E) {
;     ...
;             PG8_LDB(B0, 0, 0); PG8_LDB(B1, 0, 1); PG8_SCHED; PG8_LDA(At, 0, 0); PG8_STAGE(PG8_SA(1, 1), a1 + hstepA, voffA);
;             PG8_WAIT_V8_UNLESS_FIRST(t); PG8_WAIT_L(0); PG8_BAR; PG8_MMA(0, 0, At, B0); PG8_MMA(0, 1, At, B1); PG8_BAR; PG8_SCHED;
;             PG8_LDA(At, 0, 1); PG8_STAGE(PG8_SB(0, 0), b2, voffB); PG8_STAGE(PG8_SB(0, 1), b2 + hstep, voffB); PG8_STAGE(PG8_SA(0, 0), a2, voffA);
;             PG8_WAIT_V8_UNLESS_FIRST(t); PG8_WAIT_L(0); PG8_BAR; PG8_MMA(1, 0, At, B0); PG8_MMA(1, 1, At, B1); PG8_BAR; PG8_SCHED;
;             PG8_LDB(B0, 1, 0); PG8_LDB(B1, 1, 1); PG8_SCHED; PG8_LDA(At, 1, 0); PG8_STAGE(PG8_SA(0, 1), a2 + hstepA, voffA);
;             PG8_WAIT_V(8); PG8_WAIT_L(0); PG8_BAR; PG8_MMA(0, 0, At, B0); PG8_MMA(0, 1, At, B1); PG8_BAR; PG8_SCHED;
;             PG8_LDA(At, 1, 1); PG8_STAGE(PG8_SB(1, 0), b3, voffB); PG8_STAGE(PG8_SB(1, 1), b3 + hstep, voffB); PG8_STAGE(PG8_SA(1, 0), a3, voffA);
;             PG8_WAIT_V(8); PG8_WAIT_L(0); PG8_BAR; PG8_MMA(1, 0, At, B0); PG8_MMA(1, 1, At, B1); PG8_BAR; PG8_SCHED;
;             } else {
;             PG8_LDB(B0, 0, 0); PG8_SCHED; PG8_LDA(At, 0, 0); PG8_STAGE(PG8_SA(1, 1), a1 + hstepA, voffA);
;             PG8_WAIT_L(8); PG8_BAR; PG8_WAIT_L(0); PG8_MMA(0, 0, At, B0); PG8_BAR; PG8_SCHED;
;             PG8_LDB(B1, 0, 1); PG8_STAGE(PG8_SB(0, 0), b2, voffB);
;             PG8_BAR; PG8_WAIT_L(0); PG8_MMA(0, 1, At, B1); PG8_BAR;
;             PG8_LDA(At, 0, 1); PG8_STAGE(PG8_SA(0, 0), a2, voffA);
;             PG8_BAR; PG8_WAIT_L(0); PG8_MMA(1, 0, At, B0); PG8_BAR; PG8_SCHED;
;             PG8_STAGE(PG8_SB(0, 1), b2 + hstep, voffB);
;             PG8_WAIT_V(6); PG8_BAR; PG8_MMA(1, 1, At, B1); PG8_BAR;
;             PG8_LDB(B0, 1, 0); PG8_SCHED; PG8_LDA(At, 1, 0); PG8_STAGE(PG8_SA(0, 1), a2 + hstepA, voffA);
;             PG8_WAIT_L(8); PG8_BAR; PG8_WAIT_L(0); PG8_MMA(0, 0, At, B0); PG8_BAR; PG8_SCHED;
;             PG8_LDB(B1, 1, 1); PG8_STAGE(PG8_SB(1, 0), b3, voffB);
;             PG8_BAR; PG8_WAIT_L(0); PG8_MMA(0, 1, At, B1); PG8_BAR;
;             PG8_LDA(At, 1, 1); PG8_STAGE(PG8_SA(1, 0), a3, voffA);
	s_waitcnt lgkmcnt(0)
	v_mfma_scale_f32_16x16x128_f8f6f4 v[160:163], v[4:11], v[182:189], v[160:163], v245, v245 op_sel_hi:[0,0,0]
	v_mfma_scale_f32_16x16x128_f8f6f4 v[156:159], v[12:19], v[182:189], v[156:159], v245, v245 op_sel_hi:[0,0,0]
	v_mfma_scale_f32_16x16x128_f8f6f4 v[144:147], v[4:11], v[210:217], v[144:147], v245, v245 op_sel_hi:[0,0,0]
	v_mfma_scale_f32_16x16x128_f8f6f4 v[140:143], v[12:19], v[210:217], v[140:143], v245, v245 op_sel_hi:[0,0,0]
	v_mfma_scale_f32_16x16x128_f8f6f4 v[128:131], v[4:11], v[218:225], v[128:131], v245, v245 op_sel_hi:[0,0,0]
	v_mfma_scale_f32_16x16x128_f8f6f4 v[124:127], v[12:19], v[218:225], v[124:127], v245, v245 op_sel_hi:[0,0,0]
	v_mfma_scale_f32_16x16x128_f8f6f4 v[112:115], v[4:11], v[228:235], v[112:115], v245, v245 op_sel_hi:[0,0,0]
	v_mfma_scale_f32_16x16x128_f8f6f4 v[108:111], v[12:19], v[228:235], v[108:111], v245, v245 op_sel_hi:[0,0,0]
	v_mfma_scale_f32_16x16x128_f8f6f4 v[152:155], v[20:27], v[182:189], v[152:155], v245, v245 op_sel_hi:[0,0,0]
	v_mfma_scale_f32_16x16x128_f8f6f4 v[148:151], v[28:35], v[182:189], v[148:151], v245, v245 op_sel_hi:[0,0,0]
	v_mfma_scale_f32_16x16x128_f8f6f4 v[136:139], v[20:27], v[210:217], v[136:139], v245, v245 op_sel_hi:[0,0,0]
	v_mfma_scale_f32_16x16x128_f8f6f4 v[132:135], v[28:35], v[210:217], v[132:135], v245, v245 op_sel_hi:[0,0,0]
	v_mfma_scale_f32_16x16x128_f8f6f4 v[120:123], v[20:27], v[218:225], v[120:123], v245, v245 op_sel_hi:[0,0,0]
	v_mfma_scale_f32_16x16x128_f8f6f4 v[116:119], v[28:35], v[218:225], v[116:119], v245, v245 op_sel_hi:[0,0,0]
	v_mfma_scale_f32_16x16x128_f8f6f4 v[104:107], v[20:27], v[228:235], v[104:107], v245, v245 op_sel_hi:[0,0,0]
	v_mfma_scale_f32_16x16x128_f8f6f4 v[100:103], v[28:35], v[228:235], v[100:103], v245, v245 op_sel_hi:[0,0,0]
	s_barrier
	s_add_i32 s62, s73, s17
	v_lshl_add_u64 v[174:175], v[174:175], 0, s[34:35]
	s_mov_b32 m0, s62
	ds_read_b128 v[182:185], v208 offset:49152
	ds_read_b128 v[186:189], v208 offset:50176
	ds_read_b128 v[210:213], v208 offset:51200
	ds_read_b128 v[214:217], v208 offset:52224
	ds_read_b128 v[218:221], v208 offset:53248
	ds_read_b128 v[222:225], v208 offset:54272
	ds_read_b128 v[228:231], v208 offset:55296
	ds_read_b128 v[232:235], v208 offset:56320
	global_load_lds_dwordx4 v[174:175], off
	s_add_i32 m0, s62, 0x2000
	s_add_u32 s60, s60, 0x20080
	v_lshl_add_u64 v[174:175], v[176:177], 0, s[34:35]
	s_addc_u32 s61, s61, 0
	s_add_i32 s62, s74, s17
	global_load_lds_dwordx4 v[174:175], off
	s_mov_b32 m0, s62
	s_nop 0
	global_load_lds_dwordx4 v2, s[60:61]
	s_add_i32 m0, s62, 0x2000
	s_nop 0
	global_load_lds_dwordx4 v164, s[60:61]
	v_lshl_add_u64 v[174:175], v[178:179], 0, s[34:35]
	s_mov_b32 m0, s65
	s_nop 0
	global_load_lds_dwordx4 v[174:175], off
	v_lshl_add_u64 v[174:175], v[180:181], 0, s[34:35]
	s_mov_b32 m0, s66
	s_nop 0
	global_load_lds_dwordx4 v[174:175], off
	s_waitcnt vmcnt(8)
	s_waitcnt lgkmcnt(0)
	s_barrier
	s_waitcnt lgkmcnt(0)
	v_mfma_scale_f32_16x16x128_f8f6f4 v[96:99], v[4:11], v[182:189], v[96:99], v245, v245 op_sel_hi:[0,0,0]
	v_mfma_scale_f32_16x16x128_f8f6f4 v[92:95], v[12:19], v[182:189], v[92:95], v245, v245 op_sel_hi:[0,0,0]
	v_mfma_scale_f32_16x16x128_f8f6f4 v[80:83], v[4:11], v[210:217], v[80:83], v245, v245 op_sel_hi:[0,0,0]
	v_mfma_scale_f32_16x16x128_f8f6f4 v[76:79], v[12:19], v[210:217], v[76:79], v245, v245 op_sel_hi:[0,0,0]
	v_mfma_scale_f32_16x16x128_f8f6f4 v[64:67], v[4:11], v[218:225], v[64:67], v245, v245 op_sel_hi:[0,0,0]
	v_mfma_scale_f32_16x16x128_f8f6f4 v[60:63], v[12:19], v[218:225], v[60:63], v245, v245 op_sel_hi:[0,0,0]
	v_mfma_scale_f32_16x16x128_f8f6f4 v[48:51], v[4:11], v[228:235], v[48:51], v245, v245 op_sel_hi:[0,0,0]
	v_mfma_scale_f32_16x16x128_f8f6f4 v[44:47], v[12:19], v[228:235], v[44:47], v245, v245 op_sel_hi:[0,0,0]
	v_mfma_scale_f32_16x16x128_f8f6f4 v[88:91], v[20:27], v[182:189], v[88:91], v245, v245 op_sel_hi:[0,0,0]
	v_mfma_scale_f32_16x16x128_f8f6f4 v[84:87], v[28:35], v[182:189], v[84:87], v245, v245 op_sel_hi:[0,0,0]
	v_mfma_scale_f32_16x16x128_f8f6f4 v[72:75], v[20:27], v[210:217], v[72:75], v245, v245 op_sel_hi:[0,0,0]
	v_mfma_scale_f32_16x16x128_f8f6f4 v[68:71], v[28:35], v[210:217], v[68:71], v245, v245 op_sel_hi:[0,0,0]
	v_mfma_scale_f32_16x16x128_f8f6f4 v[56:59], v[20:27], v[218:225], v[56:59], v245, v245 op_sel_hi:[0,0,0]
	v_mfma_scale_f32_16x16x128_f8f6f4 v[52:55], v[28:35], v[218:225], v[52:55], v245, v245 op_sel_hi:[0,0,0]
	v_mfma_scale_f32_16x16x128_f8f6f4 v[40:43], v[20:27], v[228:235], v[40:43], v245, v245 op_sel_hi:[0,0,0]
	v_mfma_scale_f32_16x16x128_f8f6f4 v[36:39], v[28:35], v[228:235], v[36:39], v245, v245 op_sel_hi:[0,0,0]
	s_barrier
	s_add_u32 s42, s42, 0x100
	s_addc_u32 s43, s43, 0
	s_add_u32 s70, s70, 0x100
	s_addc_u32 s71, s71, 0
	s_cmp_gt_u32 s72, 5
	s_mov_b32 s60, s72
	s_cbranch_scc0 .LBB0_1587
	s_waitcnt vmcnt(0)
	s_nop 15
	s_nop 15
	s_and_b64 vcc, exec, s[50:51]
	s_cbranch_vccz .LBB0_1590
	s_barrier

; #define PG8_STAGE(bufoff, gbase, voff) do { _Pragma("unroll") for (int _i = 0; _i < 2; ++_i) \
;         __builtin_amdgcn_global_load_lds((const unsigned*)((const char*)(gbase) + (voff)[_i]), (PG8_LAS unsigned*)(lds + (bufoff) + ldsw + _i * 8192), 16, 0, 0); } while (0)
; #define PG8_LDA(dst, b, h) do { _Pragma("unroll") for (int m = 0; m < 4; ++m) _Pragma("unroll") for (int k = 0; k < 2; ++k) dst[m][k] = *(const PG8_LAS bf16x8*)(lds + PG8_SA(b, h) + aoff + m * 2048 + k * 1024); } while (0)
; #define PG8_LDB(dst, b, h) do { _Pragma("unroll") for (int n = 0; n < 2; ++n) _Pragma("unroll") for (int k = 0; k < 2; ++k) dst[n][k] = *(const PG8_LAS bf16x8*)(lds + PG8_SB(b, h) + boff + n * 2048 + k * 1024); } while (0)
; #define PG8_WAIT_V(n) asm volatile("s_waitcnt vmcnt(" #n ")" ::: "memory")
; #define PG8_WAIT_V8_UNLESS_FIRST(t) asm volatile("s_cmp_eq_u32 %0, 0\n\ts_cbranch_scc1 .Lpg8skip%=\n\ts_waitcnt vmcnt(8)\n.Lpg8skip%=:" :: "s"(t) : "scc", "memory")
; #define PG8_WAIT_L(n) asm volatile("s_waitcnt lgkmcnt(" #n ")" ::: "memory")
; #define PG8_BAR __builtin_amdgcn_s_barrier()
; template <class Epi, class Sched, bool ALIGN_EPI = false, bool SP2 = false, bool FP8 = false, bool ABLK = false>
; __device__ __forceinline__ void gemm_phase(PG8_LAS unsigned char* lds, const Gemm g, const Sched& S, const Epi& E) {
;     ...
;             PG8_LDB(B0, 0, 0); PG8_LDB(B1, 0, 1); PG8_SCHED; PG8_LDA(At, 0, 0); PG8_STAGE(PG8_SA(1, 1), a1 + hstepA, voffA);
;             PG8_WAIT_V8_UNLESS_FIRST(t); PG8_WAIT_L(0); PG8_BAR; PG8_MMA(0, 0, At, B0); PG8_MMA(0, 1, At, B1); PG8_BAR; PG8_SCHED;
;             PG8_LDA(At, 0, 1); PG8_STAGE(PG8_SB(0, 0), b2, voffB); PG8_STAGE(PG8_SB(0, 1), b2 + hstep, voffB); PG8_STAGE(PG8_SA(0, 0), a2, voffA);
;             PG8_WAIT_V8_UNLESS_FIRST(t); PG8_WAIT_L(0); PG8_BAR; PG8_MMA(1, 0, At, B0); PG8_MMA(1, 1, At, B1); PG8_BAR; PG8_SCHED;
;             PG8_LDB(B0, 1, 0); PG8_LDB(B1, 1, 1); PG8_SCHED; PG8_LDA(At, 1, 0); PG8_STAGE(PG8_SA(0, 1), a2 + hstepA, voffA);
;             PG8_WAIT_V(8); PG8_WAIT_L(0); PG8_BAR; PG8_MMA(0, 0, At, B0); PG8_MMA(0, 1, At, B1); PG8_BAR; PG8_SCHED;
;             PG8_LDA(At, 1, 1); PG8_STAGE(PG8_SB(1, 0), b3, voffB); PG8_STAGE(PG8_SB(1, 1), b3 + hstep, voffB); PG8_STAGE(PG8_SA(1, 0), a3, voffA);
;             PG8_WAIT_V(8); PG8_WAIT_L(0); PG8_BAR; PG8_MMA(1, 0, At, B0); PG8_MMA(1, 1, At, B1); PG8_BAR; PG8_SCHED;
.Lpg8skip12:
	s_waitcnt lgkmcnt(0)
	s_barrier
	s_waitcnt lgkmcnt(0)
	v_mfma_scale_f32_16x16x128_f8f6f4 v[160:163], v[28:35], v[174:181], v[160:163], v245, v245 op_sel_hi:[0,0,0]
	v_mfma_scale_f32_16x16x128_f8f6f4 v[156:159], v[20:27], v[174:181], v[156:159], v245, v245 op_sel_hi:[0,0,0]
	v_mfma_scale_f32_16x16x128_f8f6f4 v[144:147], v[28:35], v[186:193], v[144:147], v245, v245 op_sel_hi:[0,0,0]
	v_mfma_scale_f32_16x16x128_f8f6f4 v[140:143], v[20:27], v[186:193], v[140:143], v245, v245 op_sel_hi:[0,0,0]
	v_mfma_scale_f32_16x16x128_f8f6f4 v[128:131], v[28:35], v[208:215], v[128:131], v245, v245 op_sel_hi:[0,0,0]
	v_mfma_scale_f32_16x16x128_f8f6f4 v[124:127], v[20:27], v[208:215], v[124:127], v245, v245 op_sel_hi:[0,0,0]
	v_mfma_scale_f32_16x16x128_f8f6f4 v[112:115], v[28:35], v[216:223], v[112:115], v245, v245 op_sel_hi:[0,0,0]
	v_mfma_scale_f32_16x16x128_f8f6f4 v[108:111], v[20:27], v[216:223], v[108:111], v245, v245 op_sel_hi:[0,0,0]
	v_mfma_scale_f32_16x16x128_f8f6f4 v[152:155], v[12:19], v[174:181], v[152:155], v245, v245 op_sel_hi:[0,0,0]
	v_mfma_scale_f32_16x16x128_f8f6f4 v[148:151], v[4:11], v[174:181], v[148:151], v245, v245 op_sel_hi:[0,0,0]
	v_mfma_scale_f32_16x16x128_f8f6f4 v[136:139], v[12:19], v[186:193], v[136:139], v245, v245 op_sel_hi:[0,0,0]
	v_mfma_scale_f32_16x16x128_f8f6f4 v[132:135], v[4:11], v[186:193], v[132:135], v245, v245 op_sel_hi:[0,0,0]
	v_mfma_scale_f32_16x16x128_f8f6f4 v[120:123], v[12:19], v[208:215], v[120:123], v245, v245 op_sel_hi:[0,0,0]
	v_mfma_scale_f32_16x16x128_f8f6f4 v[116:119], v[4:11], v[208:215], v[116:119], v245, v245 op_sel_hi:[0,0,0]
	v_mfma_scale_f32_16x16x128_f8f6f4 v[104:107], v[12:19], v[216:223], v[104:107], v245, v245 op_sel_hi:[0,0,0]
	v_mfma_scale_f32_16x16x128_f8f6f4 v[100:103], v[4:11], v[216:223], v[100:103], v245, v245 op_sel_hi:[0,0,0]
	s_barrier
	s_add_i32 s76, s76, s19
	v_lshl_add_u64 v[174:175], s[62:63], 0, v[2:3]
	s_mov_b32 m0, s76
	ds_read_b128 v[186:189], v184 offset:16384
	ds_read_b128 v[190:193], v184 offset:17408
	ds_read_b128 v[208:211], v184 offset:18432
	ds_read_b128 v[212:215], v184 offset:19456
	ds_read_b128 v[216:219], v184 offset:20480
	ds_read_b128 v[220:223], v184 offset:21504
	ds_read_b128 v[228:231], v184 offset:22528
	ds_read_b128 v[232:235], v184 offset:23552
	global_load_lds_dwordx4 v2, s[62:63]
	s_add_i32 m0, s76, 0x2000
	s_add_u32 s84, s62, 0x20000
	v_lshl_add_u64 v[176:177], s[62:63], 0, v[164:165]
	s_addc_u32 s85, s63, 0
	s_add_i32 s76, s77, s19
	global_load_lds_dwordx4 v164, s[62:63]
	s_mov_b32 m0, s76
	v_lshl_add_u64 v[180:181], s[64:65], 0, v[166:167]
	global_load_lds_dwordx4 v2, s[84:85]
	s_add_i32 m0, s76, 0x2000
	s_nop 0
	global_load_lds_dwordx4 v164, s[84:85]
	v_lshl_add_u64 v[178:179], s[64:65], 0, v[168:169]
	s_mov_b32 m0, s20
	s_nop 0
	global_load_lds_dwordx4 v168, s[64:65]
	s_mov_b32 m0, s21
	s_nop 0
	global_load_lds_dwordx4 v166, s[64:65]
	s_cmp_eq_u32 s75, 0
	s_cbranch_scc1 .Lpg8skip13
	s_waitcnt vmcnt(8)
.Lpg8skip13:
	s_waitcnt lgkmcnt(0)
	s_barrier
	s_waitcnt lgkmcnt(0)
	v_mfma_scale_f32_16x16x128_f8f6f4 v[96:99], v[28:35], v[186:193], v[96:99], v245, v245 op_sel_hi:[0,0,0]
	v_mfma_scale_f32_16x16x128_f8f6f4 v[92:95], v[20:27], v[186:193], v[92:95], v245, v245 op_sel_hi:[0,0,0]
	v_mfma_scale_f32_16x16x128_f8f6f4 v[80:83], v[28:35], v[208:215], v[80:83], v245, v245 op_sel_hi:[0,0,0]
	v_mfma_scale_f32_16x16x128_f8f6f4 v[76:79], v[20:27], v[208:215], v[76:79], v245, v245 op_sel_hi:[0,0,0]
	v_mfma_scale_f32_16x16x128_f8f6f4 v[64:67], v[28:35], v[216:223], v[64:67], v245, v245 op_sel_hi:[0,0,0]
	v_mfma_scale_f32_16x16x128_f8f6f4 v[60:63], v[20:27], v[216:223], v[60:63], v245, v245 op_sel_hi:[0,0,0]
	v_mfma_scale_f32_16x16x128_f8f6f4 v[48:51], v[28:35], v[228:235], v[48:51], v245, v245 op_sel_hi:[0,0,0]
	v_mfma_scale_f32_16x16x128_f8f6f4 v[44:47], v[20:27], v[228:235], v[44:47], v245, v245 op_sel_hi:[0,0,0]
	v_mfma_scale_f32_16x16x128_f8f6f4 v[88:91], v[12:19], v[186:193], v[88:91], v245, v245 op_sel_hi:[0,0,0]
	v_mfma_scale_f32_16x16x128_f8f6f4 v[84:87], v[4:11], v[186:193], v[84:87], v245, v245 op_sel_hi:[0,0,0]
	v_mfma_scale_f32_16x16x128_f8f6f4 v[72:75], v[12:19], v[208:215], v[72:75], v245, v245 op_sel_hi:[0,0,0]
	v_mfma_scale_f32_16x16x128_f8f6f4 v[68:71], v[4:11], v[208:215], v[68:71], v245, v245 op_sel_hi:[0,0,0]
	v_mfma_scale_f32_16x16x128_f8f6f4 v[56:59], v[12:19], v[216:223], v[56:59], v245, v245 op_sel_hi:[0,0,0]
	v_mfma_scale_f32_16x16x128_f8f6f4 v[52:55], v[4:11], v[216:223], v[52:55], v245, v245 op_sel_hi:[0,0,0]
	v_mfma_scale_f32_16x16x128_f8f6f4 v[40:43], v[12:19], v[228:235], v[40:43], v245, v245 op_sel_hi:[0,0,0]
	v_mfma_scale_f32_16x16x128_f8f6f4 v[36:39], v[4:11], v[228:235], v[36:39], v245, v245 op_sel_hi:[0,0,0]
	s_barrier
	s_add_i32 s76, 0, 0x18000
	s_add_i32 s77, 0, 0x1c000
	v_add_u32_e32 v16, s76, v183
	v_add_u32_e32 v32, s77, v183
	ds_read_b128 v[4:7], v16
	ds_read_b128 v[8:11], v16 offset:1024
	ds_read_b128 v[12:15], v16 offset:2048
	ds_read_b128 v[16:19], v16 offset:3072
	ds_read_b128 v[20:23], v32
	ds_read_b128 v[24:27], v32 offset:1024
	ds_read_b128 v[28:31], v32 offset:2048
	ds_read_b128 v[32:35], v32 offset:3072
	s_add_u32 s64, s64, 0x20000
	s_addc_u32 s65, s65, 0
	s_mov_b32 m0, s22
	ds_read_b128 v[186:189], v184 offset:32768
	ds_read_b128 v[190:193], v184 offset:33792
	ds_read_b128 v[208:211], v184 offset:34816
	ds_read_b128 v[212:215], v184 offset:35840
	ds_read_b128 v[216:219], v184 offset:36864
	ds_read_b128 v[220:223], v184 offset:37888
	ds_read_b128 v[228:231], v184 offset:38912
	ds_read_b128 v[232:235], v184 offset:39936
	global_load_lds_dwordx4 v168, s[64:65]
	s_mov_b32 m0, s23
	s_nop 0
	global_load_lds_dwordx4 v166, s[64:65]
	s_waitcnt vmcnt(8)
	s_waitcnt lgkmcnt(0)
	s_barrier
; #define PG8_BAR __builtin_amdgcn_s_barrier()
; template <class Epi, class Sched, bool ALIGN_EPI = false, bool SP2 = false, bool FP8 = false, bool ABLK = false>
; __device__ __forceinline__ void gemm_phase(PG8_LAS unsigned char* lds, const Gemm g, const Sched& S, const Epi& E) {
;     ...
;             PG8_LDB(B0, 0, 0); PG8_LDB(B1, 0, 1); PG8_SCHED; PG8_LDA(At, 0, 0); PG8_STAGE(PG8_SA(1, 1), a1 + hstepA, voffA);
;             PG8_WAIT_V8_UNLESS_FIRST(t); PG8_WAIT_L(0); PG8_BAR; PG8_MMA(0, 0, At, B0); PG8_MMA(0, 1, At, B1); PG8_BAR; PG8_SCHED;
;             PG8_LDA(At, 0, 1); PG8_STAGE(PG8_SB(0, 0), b2, voffB); PG8_STAGE(PG8_SB(0, 1), b2 + hstep, voffB); PG8_STAGE(PG8_SA(0, 0), a2, voffA);
;             PG8_WAIT_V8_UNLESS_FIRST(t); PG8_WAIT_L(0); PG8_BAR; PG8_MMA(1, 0, At, B0); PG8_MMA(1, 1, At, B1); PG8_BAR; PG8_SCHED;
;             PG8_LDB(B0, 1, 0); PG8_LDB(B1, 1, 1); PG8_SCHED; PG8_LDA(At, 1, 0); PG8_STAGE(PG8_SA(0, 1), a2 + hstepA, voffA);
;             PG8_WAIT_V(8); PG8_WAIT_L(0); PG8_BAR; PG8_MMA(0, 0, At, B0); PG8_MMA(0, 1, At, B1); PG8_BAR; PG8_SCHED;
;             PG8_LDA(At, 1, 1); PG8_STAGE(PG8_SB(1, 0), b3, voffB); PG8_STAGE(PG8_SB(1, 1), b3 + hstep, voffB); PG8_STAGE(PG8_SA(1, 0), a3, voffA);
;             PG8_WAIT_V(8); PG8_WAIT_L(0); PG8_BAR; PG8_MMA(1, 0, At, B0); PG8_MMA(1, 1, At, B1); PG8_BAR; PG8_SCHED;
;             } else {
;             PG8_LDB(B0, 0, 0); PG8_SCHED; PG8_LDA(At, 0, 0); PG8_STAGE(PG8_SA(1, 1), a1 + hstepA, voffA);
;             PG8_WAIT_L(8); PG8_BAR; PG8_WAIT_L(0); PG8_MMA(0, 0, At, B0); PG8_BAR; PG8_SCHED;
;             PG8_LDB(B1, 0, 1); PG8_STAGE(PG8_SB(0, 0), b2, voffB);
;             PG8_BAR; PG8_WAIT_L(0); PG8_MMA(0, 1, At, B1); PG8_BAR;
;             PG8_LDA(At, 0, 1); PG8_STAGE(PG8_SA(0, 0), a2, voffA);
;             PG8_BAR; PG8_WAIT_L(0); PG8_MMA(1, 0, At, B0); PG8_BAR; PG8_SCHED;
;             PG8_STAGE(PG8_SB(0, 1), b2 + hstep, voffB);
;             PG8_WAIT_V(6); PG8_BAR; PG8_MMA(1, 1, At, B1); PG8_BAR;
;             PG8_LDB(B0, 1, 0); PG8_SCHED; PG8_LDA(At, 1, 0); PG8_STAGE(PG8_SA(0, 1), a2 + hstepA, voffA);
;             PG8_WAIT_L(8); PG8_BAR; PG8_WAIT_L(0); PG8_MMA(0, 0, At, B0); PG8_BAR; PG8_SCHED;
;             PG8_LDB(B1, 1, 1); PG8_STAGE(PG8_SB(1, 0), b3, voffB);
;             PG8_BAR; PG8_WAIT_L(0); PG8_MMA(0, 1, At, B1); PG8_BAR;
;             PG8_LDA(At, 1, 1); PG8_STAGE(PG8_SA(1, 0), a3, voffA);
	s_waitcnt lgkmcnt(0)
	v_mfma_scale_f32_16x16x128_f8f6f4 v[160:163], v[4:11], v[186:193], v[160:163], v245, v245 op_sel_hi:[0,0,0]
	v_mfma_scale_f32_16x16x128_f8f6f4 v[156:159], v[12:19], v[186:193], v[156:159], v245, v245 op_sel_hi:[0,0,0]
	v_mfma_scale_f32_16x16x128_f8f6f4 v[144:147], v[4:11], v[208:215], v[144:147], v245, v245 op_sel_hi:[0,0,0]
	v_mfma_scale_f32_16x16x128_f8f6f4 v[140:143], v[12:19], v[208:215], v[140:143], v245, v245 op_sel_hi:[0,0,0]
	v_mfma_scale_f32_16x16x128_f8f6f4 v[128:131], v[4:11], v[216:223], v[128:131], v245, v245 op_sel_hi:[0,0,0]
	v_mfma_scale_f32_16x16x128_f8f6f4 v[124:127], v[12:19], v[216:223], v[124:127], v245, v245 op_sel_hi:[0,0,0]
	v_mfma_scale_f32_16x16x128_f8f6f4 v[112:115], v[4:11], v[228:235], v[112:115], v245, v245 op_sel_hi:[0,0,0]
	v_mfma_scale_f32_16x16x128_f8f6f4 v[108:111], v[12:19], v[228:235], v[108:111], v245, v245 op_sel_hi:[0,0,0]
	v_mfma_scale_f32_16x16x128_f8f6f4 v[152:155], v[20:27], v[186:193], v[152:155], v245, v245 op_sel_hi:[0,0,0]
	v_mfma_scale_f32_16x16x128_f8f6f4 v[148:151], v[28:35], v[186:193], v[148:151], v245, v245 op_sel_hi:[0,0,0]
	v_mfma_scale_f32_16x16x128_f8f6f4 v[136:139], v[20:27], v[208:215], v[136:139], v245, v245 op_sel_hi:[0,0,0]
	v_mfma_scale_f32_16x16x128_f8f6f4 v[132:135], v[28:35], v[208:215], v[132:135], v245, v245 op_sel_hi:[0,0,0]
	v_mfma_scale_f32_16x16x128_f8f6f4 v[120:123], v[20:27], v[216:223], v[120:123], v245, v245 op_sel_hi:[0,0,0]
	v_mfma_scale_f32_16x16x128_f8f6f4 v[116:119], v[28:35], v[216:223], v[116:119], v245, v245 op_sel_hi:[0,0,0]
	v_mfma_scale_f32_16x16x128_f8f6f4 v[104:107], v[20:27], v[228:235], v[104:107], v245, v245 op_sel_hi:[0,0,0]
	v_mfma_scale_f32_16x16x128_f8f6f4 v[100:103], v[28:35], v[228:235], v[100:103], v245, v245 op_sel_hi:[0,0,0]
	s_barrier
	s_add_i32 s64, s76, s19
	v_lshl_add_u64 v[174:175], v[174:175], 0, s[34:35]
	s_mov_b32 m0, s64
	ds_read_b128 v[186:189], v184 offset:49152
	ds_read_b128 v[190:193], v184 offset:50176
	ds_read_b128 v[208:211], v184 offset:51200
	ds_read_b128 v[212:215], v184 offset:52224
	ds_read_b128 v[216:219], v184 offset:53248
	ds_read_b128 v[220:223], v184 offset:54272
	ds_read_b128 v[228:231], v184 offset:55296
	ds_read_b128 v[232:235], v184 offset:56320
	global_load_lds_dwordx4 v[174:175], off
	s_add_i32 m0, s64, 0x2000
	s_add_u32 s62, s62, 0x20080
	v_lshl_add_u64 v[174:175], v[176:177], 0, s[34:35]
	s_addc_u32 s63, s63, 0
	s_add_i32 s64, s77, s19
	global_load_lds_dwordx4 v[174:175], off
	s_mov_b32 m0, s64
	s_nop 0
	global_load_lds_dwordx4 v2, s[62:63]
	s_add_i32 m0, s64, 0x2000
	s_nop 0
	global_load_lds_dwordx4 v164, s[62:63]
	v_lshl_add_u64 v[174:175], v[178:179], 0, s[34:35]
	s_mov_b32 m0, s67
	s_nop 0
	global_load_lds_dwordx4 v[174:175], off
	v_lshl_add_u64 v[174:175], v[180:181], 0, s[34:35]
	s_mov_b32 m0, s68
	s_nop 0
	global_load_lds_dwordx4 v[174:175], off
	s_waitcnt vmcnt(8)
	s_waitcnt lgkmcnt(0)
	s_barrier
	s_waitcnt lgkmcnt(0)
	v_mfma_scale_f32_16x16x128_f8f6f4 v[96:99], v[4:11], v[186:193], v[96:99], v245, v245 op_sel_hi:[0,0,0]
	v_mfma_scale_f32_16x16x128_f8f6f4 v[92:95], v[12:19], v[186:193], v[92:95], v245, v245 op_sel_hi:[0,0,0]
	v_mfma_scale_f32_16x16x128_f8f6f4 v[80:83], v[4:11], v[208:215], v[80:83], v245, v245 op_sel_hi:[0,0,0]
	v_mfma_scale_f32_16x16x128_f8f6f4 v[76:79], v[12:19], v[208:215], v[76:79], v245, v245 op_sel_hi:[0,0,0]
	v_mfma_scale_f32_16x16x128_f8f6f4 v[64:67], v[4:11], v[216:223], v[64:67], v245, v245 op_sel_hi:[0,0,0]
	v_mfma_scale_f32_16x16x128_f8f6f4 v[60:63], v[12:19], v[216:223], v[60:63], v245, v245 op_sel_hi:[0,0,0]
	v_mfma_scale_f32_16x16x128_f8f6f4 v[48:51], v[4:11], v[228:235], v[48:51], v245, v245 op_sel_hi:[0,0,0]
	v_mfma_scale_f32_16x16x128_f8f6f4 v[44:47], v[12:19], v[228:235], v[44:47], v245, v245 op_sel_hi:[0,0,0]
	v_mfma_scale_f32_16x16x128_f8f6f4 v[88:91], v[20:27], v[186:193], v[88:91], v245, v245 op_sel_hi:[0,0,0]
	v_mfma_scale_f32_16x16x128_f8f6f4 v[84:87], v[28:35], v[186:193], v[84:87], v245, v245 op_sel_hi:[0,0,0]
	v_mfma_scale_f32_16x16x128_f8f6f4 v[72:75], v[20:27], v[208:215], v[72:75], v245, v245 op_sel_hi:[0,0,0]
	v_mfma_scale_f32_16x16x128_f8f6f4 v[68:71], v[28:35], v[208:215], v[68:71], v245, v245 op_sel_hi:[0,0,0]
	v_mfma_scale_f32_16x16x128_f8f6f4 v[56:59], v[20:27], v[216:223], v[56:59], v245, v245 op_sel_hi:[0,0,0]
	v_mfma_scale_f32_16x16x128_f8f6f4 v[52:55], v[28:35], v[216:223], v[52:55], v245, v245 op_sel_hi:[0,0,0]
	v_mfma_scale_f32_16x16x128_f8f6f4 v[40:43], v[20:27], v[228:235], v[40:43], v245, v245 op_sel_hi:[0,0,0]
	v_mfma_scale_f32_16x16x128_f8f6f4 v[36:39], v[28:35], v[228:235], v[36:39], v245, v245 op_sel_hi:[0,0,0]
	s_barrier
	s_add_u32 s60, s60, 0x100
	s_addc_u32 s61, s61, 0
	s_add_u32 s73, s73, 0x100
	s_addc_u32 s74, s74, 0
	s_cmp_gt_u32 s75, 5
	s_mov_b32 s62, s75
	s_cbranch_scc0 .LBB0_1671
	s_waitcnt vmcnt(0)
	s_nop 15
	s_nop 15
	s_and_b64 vcc, exec, s[50:51]
	s_cbranch_vccz .LBB0_1674
	s_barrier

; #define PG8_STAGE(bufoff, gbase, voff) do { _Pragma("unroll") for (int _i = 0; _i < 2; ++_i) \
;         __builtin_amdgcn_global_load_lds((const unsigned*)((const char*)(gbase) + (voff)[_i]), (PG8_LAS unsigned*)(lds + (bufoff) + ldsw + _i * 8192), 16, 0, 0); } while (0)
; #define PG8_LDA(dst, b, h) do { _Pragma("unroll") for (int m = 0; m < 4; ++m) _Pragma("unroll") for (int k = 0; k < 2; ++k) dst[m][k] = *(const PG8_LAS bf16x8*)(lds + PG8_SA(b, h) + aoff + m * 2048 + k * 1024); } while (0)
; #define PG8_LDB(dst, b, h) do { _Pragma("unroll") for (int n = 0; n < 2; ++n) _Pragma("unroll") for (int k = 0; k < 2; ++k) dst[n][k] = *(const PG8_LAS bf16x8*)(lds + PG8_SB(b, h) + boff + n * 2048 + k * 1024); } while (0)
; #define PG8_WAIT_V(n) asm volatile("s_waitcnt vmcnt(" #n ")" ::: "memory")
; #define PG8_WAIT_V8_UNLESS_FIRST(t) asm volatile("s_cmp_eq_u32 %0, 0\n\ts_cbranch_scc1 .Lpg8skip%=\n\ts_waitcnt vmcnt(8)\n.Lpg8skip%=:" :: "s"(t) : "scc", "memory")
; #define PG8_WAIT_L(n) asm volatile("s_waitcnt lgkmcnt(" #n ")" ::: "memory")
; #define PG8_BAR __builtin_amdgcn_s_barrier()
; template <class Epi, class Sched, bool ALIGN_EPI = false, bool SP2 = false, bool FP8 = false, bool ABLK = false>
; __device__ __forceinline__ void gemm_phase(PG8_LAS unsigned char* lds, const Gemm g, const Sched& S, const Epi& E) {
;     ...
;             PG8_LDB(B0, 0, 0); PG8_LDB(B1, 0, 1); PG8_SCHED; PG8_LDA(At, 0, 0); PG8_STAGE(PG8_SA(1, 1), a1 + hstepA, voffA);
;             PG8_WAIT_V8_UNLESS_FIRST(t); PG8_WAIT_L(0); PG8_BAR; PG8_MMA(0, 0, At, B0); PG8_MMA(0, 1, At, B1); PG8_BAR; PG8_SCHED;
;             PG8_LDA(At, 0, 1); PG8_STAGE(PG8_SB(0, 0), b2, voffB); PG8_STAGE(PG8_SB(0, 1), b2 + hstep, voffB); PG8_STAGE(PG8_SA(0, 0), a2, voffA);
;             PG8_WAIT_V8_UNLESS_FIRST(t); PG8_WAIT_L(0); PG8_BAR; PG8_MMA(1, 0, At, B0); PG8_MMA(1, 1, At, B1); PG8_BAR; PG8_SCHED;
;             PG8_LDB(B0, 1, 0); PG8_LDB(B1, 1, 1); PG8_SCHED; PG8_LDA(At, 1, 0); PG8_STAGE(PG8_SA(0, 1), a2 + hstepA, voffA);
;             PG8_WAIT_V(8); PG8_WAIT_L(0); PG8_BAR; PG8_MMA(0, 0, At, B0); PG8_MMA(0, 1, At, B1); PG8_BAR; PG8_SCHED;
;             PG8_LDA(At, 1, 1); PG8_STAGE(PG8_SB(1, 0), b3, voffB); PG8_STAGE(PG8_SB(1, 1), b3 + hstep, voffB); PG8_STAGE(PG8_SA(1, 0), a3, voffA);
;             PG8_WAIT_V(8); PG8_WAIT_L(0); PG8_BAR; PG8_MMA(1, 0, At, B0); PG8_MMA(1, 1, At, B1); PG8_BAR; PG8_SCHED;
.Lpg8skip14:
	s_waitcnt lgkmcnt(0)
	s_barrier
	s_waitcnt lgkmcnt(0)
	v_mfma_scale_f32_16x16x128_f8f6f4 v[160:163], v[28:35], v[174:181], v[160:163], v245, v245 op_sel_hi:[0,0,0]
	v_mfma_scale_f32_16x16x128_f8f6f4 v[156:159], v[20:27], v[174:181], v[156:159], v245, v245 op_sel_hi:[0,0,0]
	v_mfma_scale_f32_16x16x128_f8f6f4 v[144:147], v[28:35], v[186:193], v[144:147], v245, v245 op_sel_hi:[0,0,0]
	v_mfma_scale_f32_16x16x128_f8f6f4 v[140:143], v[20:27], v[186:193], v[140:143], v245, v245 op_sel_hi:[0,0,0]
	v_mfma_scale_f32_16x16x128_f8f6f4 v[128:131], v[28:35], v[208:215], v[128:131], v245, v245 op_sel_hi:[0,0,0]
	v_mfma_scale_f32_16x16x128_f8f6f4 v[124:127], v[20:27], v[208:215], v[124:127], v245, v245 op_sel_hi:[0,0,0]
	v_mfma_scale_f32_16x16x128_f8f6f4 v[112:115], v[28:35], v[216:223], v[112:115], v245, v245 op_sel_hi:[0,0,0]
	v_mfma_scale_f32_16x16x128_f8f6f4 v[108:111], v[20:27], v[216:223], v[108:111], v245, v245 op_sel_hi:[0,0,0]
	v_mfma_scale_f32_16x16x128_f8f6f4 v[152:155], v[12:19], v[174:181], v[152:155], v245, v245 op_sel_hi:[0,0,0]
	v_mfma_scale_f32_16x16x128_f8f6f4 v[148:151], v[4:11], v[174:181], v[148:151], v245, v245 op_sel_hi:[0,0,0]
	v_mfma_scale_f32_16x16x128_f8f6f4 v[136:139], v[12:19], v[186:193], v[136:139], v245, v245 op_sel_hi:[0,0,0]
	v_mfma_scale_f32_16x16x128_f8f6f4 v[132:135], v[4:11], v[186:193], v[132:135], v245, v245 op_sel_hi:[0,0,0]
	v_mfma_scale_f32_16x16x128_f8f6f4 v[120:123], v[12:19], v[208:215], v[120:123], v245, v245 op_sel_hi:[0,0,0]
	v_mfma_scale_f32_16x16x128_f8f6f4 v[116:119], v[4:11], v[208:215], v[116:119], v245, v245 op_sel_hi:[0,0,0]
	v_mfma_scale_f32_16x16x128_f8f6f4 v[104:107], v[12:19], v[216:223], v[104:107], v245, v245 op_sel_hi:[0,0,0]
	v_mfma_scale_f32_16x16x128_f8f6f4 v[100:103], v[4:11], v[216:223], v[100:103], v245, v245 op_sel_hi:[0,0,0]
	s_barrier
	s_add_i32 s72, s72, s17
	v_lshl_add_u64 v[174:175], s[58:59], 0, v[2:3]
	s_mov_b32 m0, s72
	ds_read_b128 v[186:189], v184 offset:16384
	ds_read_b128 v[190:193], v184 offset:17408
	ds_read_b128 v[208:211], v184 offset:18432
	ds_read_b128 v[212:215], v184 offset:19456
	ds_read_b128 v[216:219], v184 offset:20480
	ds_read_b128 v[220:223], v184 offset:21504
	ds_read_b128 v[228:231], v184 offset:22528
	ds_read_b128 v[232:235], v184 offset:23552
	global_load_lds_dwordx4 v2, s[58:59]
	s_add_i32 m0, s72, 0x2000
	s_add_u32 s74, s58, 0x20000
	v_lshl_add_u64 v[176:177], s[58:59], 0, v[164:165]
	s_addc_u32 s75, s59, 0
	s_add_i32 s72, s73, s17
	global_load_lds_dwordx4 v164, s[58:59]
	s_mov_b32 m0, s72
	v_lshl_add_u64 v[180:181], s[60:61], 0, v[166:167]
	global_load_lds_dwordx4 v2, s[74:75]
	s_add_i32 m0, s72, 0x2000
	s_nop 0
	global_load_lds_dwordx4 v164, s[74:75]
	v_lshl_add_u64 v[178:179], s[60:61], 0, v[168:169]
	s_mov_b32 m0, s18
	s_nop 0
	global_load_lds_dwordx4 v168, s[60:61]
	s_mov_b32 m0, s19
	s_nop 0
	global_load_lds_dwordx4 v166, s[60:61]
	s_cmp_eq_u32 s71, 0
	s_cbranch_scc1 .Lpg8skip15
	s_waitcnt vmcnt(8)
.Lpg8skip15:
	s_waitcnt lgkmcnt(0)
	s_barrier
	s_waitcnt lgkmcnt(0)
	v_mfma_scale_f32_16x16x128_f8f6f4 v[96:99], v[28:35], v[186:193], v[96:99], v245, v245 op_sel_hi:[0,0,0]
	v_mfma_scale_f32_16x16x128_f8f6f4 v[92:95], v[20:27], v[186:193], v[92:95], v245, v245 op_sel_hi:[0,0,0]
	v_mfma_scale_f32_16x16x128_f8f6f4 v[80:83], v[28:35], v[208:215], v[80:83], v245, v245 op_sel_hi:[0,0,0]
	v_mfma_scale_f32_16x16x128_f8f6f4 v[76:79], v[20:27], v[208:215], v[76:79], v245, v245 op_sel_hi:[0,0,0]
	v_mfma_scale_f32_16x16x128_f8f6f4 v[64:67], v[28:35], v[216:223], v[64:67], v245, v245 op_sel_hi:[0,0,0]
	v_mfma_scale_f32_16x16x128_f8f6f4 v[60:63], v[20:27], v[216:223], v[60:63], v245, v245 op_sel_hi:[0,0,0]
	v_mfma_scale_f32_16x16x128_f8f6f4 v[48:51], v[28:35], v[228:235], v[48:51], v245, v245 op_sel_hi:[0,0,0]
	v_mfma_scale_f32_16x16x128_f8f6f4 v[44:47], v[20:27], v[228:235], v[44:47], v245, v245 op_sel_hi:[0,0,0]
	v_mfma_scale_f32_16x16x128_f8f6f4 v[88:91], v[12:19], v[186:193], v[88:91], v245, v245 op_sel_hi:[0,0,0]
	v_mfma_scale_f32_16x16x128_f8f6f4 v[84:87], v[4:11], v[186:193], v[84:87], v245, v245 op_sel_hi:[0,0,0]
	v_mfma_scale_f32_16x16x128_f8f6f4 v[72:75], v[12:19], v[208:215], v[72:75], v245, v245 op_sel_hi:[0,0,0]
	v_mfma_scale_f32_16x16x128_f8f6f4 v[68:71], v[4:11], v[208:215], v[68:71], v245, v245 op_sel_hi:[0,0,0]
	v_mfma_scale_f32_16x16x128_f8f6f4 v[56:59], v[12:19], v[216:223], v[56:59], v245, v245 op_sel_hi:[0,0,0]
	v_mfma_scale_f32_16x16x128_f8f6f4 v[52:55], v[4:11], v[216:223], v[52:55], v245, v245 op_sel_hi:[0,0,0]
	v_mfma_scale_f32_16x16x128_f8f6f4 v[40:43], v[12:19], v[228:235], v[40:43], v245, v245 op_sel_hi:[0,0,0]
	v_mfma_scale_f32_16x16x128_f8f6f4 v[36:39], v[4:11], v[228:235], v[36:39], v245, v245 op_sel_hi:[0,0,0]
	s_barrier
	s_add_i32 s72, 0, 0x18000
	s_add_i32 s73, 0, 0x1c000
	v_add_u32_e32 v16, s72, v183
	v_add_u32_e32 v32, s73, v183
	ds_read_b128 v[4:7], v16
	ds_read_b128 v[8:11], v16 offset:1024
	ds_read_b128 v[12:15], v16 offset:2048
	ds_read_b128 v[16:19], v16 offset:3072
	ds_read_b128 v[20:23], v32
	ds_read_b128 v[24:27], v32 offset:1024
	ds_read_b128 v[28:31], v32 offset:2048
	ds_read_b128 v[32:35], v32 offset:3072
	s_add_u32 s60, s60, 0x20000
	s_addc_u32 s61, s61, 0
	s_mov_b32 m0, s20
	ds_read_b128 v[186:189], v184 offset:32768
	ds_read_b128 v[190:193], v184 offset:33792
	ds_read_b128 v[208:211], v184 offset:34816
	ds_read_b128 v[212:215], v184 offset:35840
	ds_read_b128 v[216:219], v184 offset:36864
	ds_read_b128 v[220:223], v184 offset:37888
	ds_read_b128 v[228:231], v184 offset:38912
	ds_read_b128 v[232:235], v184 offset:39936
	global_load_lds_dwordx4 v168, s[60:61]
	s_mov_b32 m0, s21
	s_nop 0
	global_load_lds_dwordx4 v166, s[60:61]
	s_waitcnt vmcnt(8)
	s_waitcnt lgkmcnt(0)
	s_barrier
; #define PG8_BAR __builtin_amdgcn_s_barrier()
; template <class Epi, class Sched, bool ALIGN_EPI = false, bool SP2 = false, bool FP8 = false, bool ABLK = false>
; __device__ __forceinline__ void gemm_phase(PG8_LAS unsigned char* lds, const Gemm g, const Sched& S, const Epi& E) {
;     ...
;             PG8_LDB(B0, 0, 0); PG8_LDB(B1, 0, 1); PG8_SCHED; PG8_LDA(At, 0, 0); PG8_STAGE(PG8_SA(1, 1), a1 + hstepA, voffA);
;             PG8_WAIT_V8_UNLESS_FIRST(t); PG8_WAIT_L(0); PG8_BAR; PG8_MMA(0, 0, At, B0); PG8_MMA(0, 1, At, B1); PG8_BAR; PG8_SCHED;
;             PG8_LDA(At, 0, 1); PG8_STAGE(PG8_SB(0, 0), b2, voffB); PG8_STAGE(PG8_SB(0, 1), b2 + hstep, voffB); PG8_STAGE(PG8_SA(0, 0), a2, voffA);
;             PG8_WAIT_V8_UNLESS_FIRST(t); PG8_WAIT_L(0); PG8_BAR; PG8_MMA(1, 0, At, B0); PG8_MMA(1, 1, At, B1); PG8_BAR; PG8_SCHED;
;             PG8_LDB(B0, 1, 0); PG8_LDB(B1, 1, 1); PG8_SCHED; PG8_LDA(At, 1, 0); PG8_STAGE(PG8_SA(0, 1), a2 + hstepA, voffA);
;             PG8_WAIT_V(8); PG8_WAIT_L(0); PG8_BAR; PG8_MMA(0, 0, At, B0); PG8_MMA(0, 1, At, B1); PG8_BAR; PG8_SCHED;
;             PG8_LDA(At, 1, 1); PG8_STAGE(PG8_SB(1, 0), b3, voffB); PG8_STAGE(PG8_SB(1, 1), b3 + hstep, voffB); PG8_STAGE(PG8_SA(1, 0), a3, voffA);
;             PG8_WAIT_V(8); PG8_WAIT_L(0); PG8_BAR; PG8_MMA(1, 0, At, B0); PG8_MMA(1, 1, At, B1); PG8_BAR; PG8_SCHED;
;             } else {
;             PG8_LDB(B0, 0, 0); PG8_SCHED; PG8_LDA(At, 0, 0); PG8_STAGE(PG8_SA(1, 1), a1 + hstepA, voffA);
;             PG8_WAIT_L(8); PG8_BAR; PG8_WAIT_L(0); PG8_MMA(0, 0, At, B0); PG8_BAR; PG8_SCHED;
;             PG8_LDB(B1, 0, 1); PG8_STAGE(PG8_SB(0, 0), b2, voffB);
;             PG8_BAR; PG8_WAIT_L(0); PG8_MMA(0, 1, At, B1); PG8_BAR;
;             PG8_LDA(At, 0, 1); PG8_STAGE(PG8_SA(0, 0), a2, voffA);
;             PG8_BAR; PG8_WAIT_L(0); PG8_MMA(1, 0, At, B0); PG8_BAR; PG8_SCHED;
;             PG8_STAGE(PG8_SB(0, 1), b2 + hstep, voffB);
;             PG8_WAIT_V(6); PG8_BAR; PG8_MMA(1, 1, At, B1); PG8_BAR;
;             PG8_LDB(B0, 1, 0); PG8_SCHED; PG8_LDA(At, 1, 0); PG8_STAGE(PG8_SA(0, 1), a2 + hstepA, voffA);
;             PG8_WAIT_L(8); PG8_BAR; PG8_WAIT_L(0); PG8_MMA(0, 0, At, B0); PG8_BAR; PG8_SCHED;
;             PG8_LDB(B1, 1, 1); PG8_STAGE(PG8_SB(1, 0), b3, voffB);
;             PG8_BAR; PG8_WAIT_L(0); PG8_MMA(0, 1, At, B1); PG8_BAR;
;             PG8_LDA(At, 1, 1); PG8_STAGE(PG8_SA(1, 0), a3, voffA);
	s_waitcnt lgkmcnt(0)
	v_mfma_scale_f32_16x16x128_f8f6f4 v[160:163], v[4:11], v[186:193], v[160:163], v245, v245 op_sel_hi:[0,0,0]
	v_mfma_scale_f32_16x16x128_f8f6f4 v[156:159], v[12:19], v[186:193], v[156:159], v245, v245 op_sel_hi:[0,0,0]
	v_mfma_scale_f32_16x16x128_f8f6f4 v[144:147], v[4:11], v[208:215], v[144:147], v245, v245 op_sel_hi:[0,0,0]
	v_mfma_scale_f32_16x16x128_f8f6f4 v[140:143], v[12:19], v[208:215], v[140:143], v245, v245 op_sel_hi:[0,0,0]
	v_mfma_scale_f32_16x16x128_f8f6f4 v[128:131], v[4:11], v[216:223], v[128:131], v245, v245 op_sel_hi:[0,0,0]
	v_mfma_scale_f32_16x16x128_f8f6f4 v[124:127], v[12:19], v[216:223], v[124:127], v245, v245 op_sel_hi:[0,0,0]
	v_mfma_scale_f32_16x16x128_f8f6f4 v[112:115], v[4:11], v[228:235], v[112:115], v245, v245 op_sel_hi:[0,0,0]
	v_mfma_scale_f32_16x16x128_f8f6f4 v[108:111], v[12:19], v[228:235], v[108:111], v245, v245 op_sel_hi:[0,0,0]
	v_mfma_scale_f32_16x16x128_f8f6f4 v[152:155], v[20:27], v[186:193], v[152:155], v245, v245 op_sel_hi:[0,0,0]
	v_mfma_scale_f32_16x16x128_f8f6f4 v[148:151], v[28:35], v[186:193], v[148:151], v245, v245 op_sel_hi:[0,0,0]
	v_mfma_scale_f32_16x16x128_f8f6f4 v[136:139], v[20:27], v[208:215], v[136:139], v245, v245 op_sel_hi:[0,0,0]
	v_mfma_scale_f32_16x16x128_f8f6f4 v[132:135], v[28:35], v[208:215], v[132:135], v245, v245 op_sel_hi:[0,0,0]
	v_mfma_scale_f32_16x16x128_f8f6f4 v[120:123], v[20:27], v[216:223], v[120:123], v245, v245 op_sel_hi:[0,0,0]
	v_mfma_scale_f32_16x16x128_f8f6f4 v[116:119], v[28:35], v[216:223], v[116:119], v245, v245 op_sel_hi:[0,0,0]
	v_mfma_scale_f32_16x16x128_f8f6f4 v[104:107], v[20:27], v[228:235], v[104:107], v245, v245 op_sel_hi:[0,0,0]
	v_mfma_scale_f32_16x16x128_f8f6f4 v[100:103], v[28:35], v[228:235], v[100:103], v245, v245 op_sel_hi:[0,0,0]
	s_barrier
	s_add_i32 s60, s72, s17
	v_lshl_add_u64 v[174:175], v[174:175], 0, s[34:35]
	s_mov_b32 m0, s60
	ds_read_b128 v[186:189], v184 offset:49152
	ds_read_b128 v[190:193], v184 offset:50176
	ds_read_b128 v[208:211], v184 offset:51200
	ds_read_b128 v[212:215], v184 offset:52224
	ds_read_b128 v[216:219], v184 offset:53248
	ds_read_b128 v[220:223], v184 offset:54272
	ds_read_b128 v[228:231], v184 offset:55296
	ds_read_b128 v[232:235], v184 offset:56320
	global_load_lds_dwordx4 v[174:175], off
	s_add_i32 m0, s60, 0x2000
	s_add_u32 s58, s58, 0x20080
	v_lshl_add_u64 v[174:175], v[176:177], 0, s[34:35]
	s_addc_u32 s59, s59, 0
	s_add_i32 s60, s73, s17
	global_load_lds_dwordx4 v[174:175], off
	s_mov_b32 m0, s60
	s_nop 0
	global_load_lds_dwordx4 v2, s[58:59]
	s_add_i32 m0, s60, 0x2000
	s_nop 0
	global_load_lds_dwordx4 v164, s[58:59]
	v_lshl_add_u64 v[174:175], v[178:179], 0, s[34:35]
	s_mov_b32 m0, s63
	s_nop 0
	global_load_lds_dwordx4 v[174:175], off
	v_lshl_add_u64 v[174:175], v[180:181], 0, s[34:35]
	s_mov_b32 m0, s64
	s_nop 0
	global_load_lds_dwordx4 v[174:175], off
	s_waitcnt vmcnt(8)
	s_waitcnt lgkmcnt(0)
	s_barrier
	s_waitcnt lgkmcnt(0)
	v_mfma_scale_f32_16x16x128_f8f6f4 v[96:99], v[4:11], v[186:193], v[96:99], v245, v245 op_sel_hi:[0,0,0]
	v_mfma_scale_f32_16x16x128_f8f6f4 v[92:95], v[12:19], v[186:193], v[92:95], v245, v245 op_sel_hi:[0,0,0]
	v_mfma_scale_f32_16x16x128_f8f6f4 v[80:83], v[4:11], v[208:215], v[80:83], v245, v245 op_sel_hi:[0,0,0]
	v_mfma_scale_f32_16x16x128_f8f6f4 v[76:79], v[12:19], v[208:215], v[76:79], v245, v245 op_sel_hi:[0,0,0]
	v_mfma_scale_f32_16x16x128_f8f6f4 v[64:67], v[4:11], v[216:223], v[64:67], v245, v245 op_sel_hi:[0,0,0]
	v_mfma_scale_f32_16x16x128_f8f6f4 v[60:63], v[12:19], v[216:223], v[60:63], v245, v245 op_sel_hi:[0,0,0]
	v_mfma_scale_f32_16x16x128_f8f6f4 v[48:51], v[4:11], v[228:235], v[48:51], v245, v245 op_sel_hi:[0,0,0]
	v_mfma_scale_f32_16x16x128_f8f6f4 v[44:47], v[12:19], v[228:235], v[44:47], v245, v245 op_sel_hi:[0,0,0]
	v_mfma_scale_f32_16x16x128_f8f6f4 v[88:91], v[20:27], v[186:193], v[88:91], v245, v245 op_sel_hi:[0,0,0]
	v_mfma_scale_f32_16x16x128_f8f6f4 v[84:87], v[28:35], v[186:193], v[84:87], v245, v245 op_sel_hi:[0,0,0]
	v_mfma_scale_f32_16x16x128_f8f6f4 v[72:75], v[20:27], v[208:215], v[72:75], v245, v245 op_sel_hi:[0,0,0]
	v_mfma_scale_f32_16x16x128_f8f6f4 v[68:71], v[28:35], v[208:215], v[68:71], v245, v245 op_sel_hi:[0,0,0]
	v_mfma_scale_f32_16x16x128_f8f6f4 v[56:59], v[20:27], v[216:223], v[56:59], v245, v245 op_sel_hi:[0,0,0]
	v_mfma_scale_f32_16x16x128_f8f6f4 v[52:55], v[28:35], v[216:223], v[52:55], v245, v245 op_sel_hi:[0,0,0]
	v_mfma_scale_f32_16x16x128_f8f6f4 v[40:43], v[20:27], v[228:235], v[40:43], v245, v245 op_sel_hi:[0,0,0]
	v_mfma_scale_f32_16x16x128_f8f6f4 v[36:39], v[28:35], v[228:235], v[36:39], v245, v245 op_sel_hi:[0,0,0]
	s_barrier
	s_add_u32 s56, s56, 0x100
	s_addc_u32 s57, s57, 0
	s_add_u32 s69, s69, 0x100
	s_addc_u32 s70, s70, 0
	s_cmp_gt_u32 s71, 5
	s_mov_b32 s58, s71
	s_cbranch_scc0 .LBB0_1689
	s_waitcnt vmcnt(0)
	s_nop 15
	s_nop 15
	s_and_b64 vcc, exec, s[46:47]
	s_cbranch_vccz .LBB0_1692
	s_barrier

; #define PG8_STAGE(bufoff, gbase, voff) do { _Pragma("unroll") for (int _i = 0; _i < 2; ++_i) \
;         __builtin_amdgcn_global_load_lds((const unsigned*)((const char*)(gbase) + (voff)[_i]), (PG8_LAS unsigned*)(lds + (bufoff) + ldsw + _i * 8192), 16, 0, 0); } while (0)
; #define PG8_LDA(dst, b, h) do { _Pragma("unroll") for (int m = 0; m < 4; ++m) _Pragma("unroll") for (int k = 0; k < 2; ++k) dst[m][k] = *(const PG8_LAS bf16x8*)(lds + PG8_SA(b, h) + aoff + m * 2048 + k * 1024); } while (0)
; #define PG8_WAIT_V8_UNLESS_FIRST(t) asm volatile("s_cmp_eq_u32 %0, 0\n\ts_cbranch_scc1 .Lpg8skip%=\n\ts_waitcnt vmcnt(8)\n.Lpg8skip%=:" :: "s"(t) : "scc", "memory")
; #define PG8_WAIT_L(n) asm volatile("s_waitcnt lgkmcnt(" #n ")" ::: "memory")
; #define PG8_BAR __builtin_amdgcn_s_barrier()
; #define PG8_SCHED __builtin_amdgcn_sched_barrier(0)
; template <class Epi, class Sched, bool ALIGN_EPI = false, bool SP2 = false, bool FP8 = false, bool ABLK = false>
; __device__ __forceinline__ void gemm_phase(PG8_LAS unsigned char* lds, const Gemm g, const Sched& S, const Epi& E) {
;     ...
;             PG8_WAIT_V8_UNLESS_FIRST(t); PG8_WAIT_L(0); PG8_BAR; PG8_MMA(0, 0, At, B0); PG8_MMA(0, 1, At, B1); PG8_BAR; PG8_SCHED;
;             PG8_LDA(At, 0, 1); PG8_STAGE(PG8_SB(0, 0), b2, voffB); PG8_STAGE(PG8_SB(0, 1), b2 + hstep, voffB); PG8_STAGE(PG8_SA(0, 0), a2, voffA);
;             PG8_WAIT_V8_UNLESS_FIRST(t); PG8_WAIT_L(0); PG8_BAR; PG8_MMA(1, 0, At, B0); PG8_MMA(1, 1, At, B1); PG8_BAR; PG8_SCHED;
.Lpg8skip16:
	s_waitcnt lgkmcnt(0)
	s_barrier
	s_waitcnt lgkmcnt(0)
	v_mfma_f32_16x16x32_bf16 v[132:135], v[124:127], v[180:183], v[132:135]
	v_mfma_f32_16x16x32_bf16 v[128:131], v[140:143], v[180:183], v[128:131]
	v_mfma_f32_16x16x32_bf16 v[112:115], v[124:127], v[188:191], v[112:115]
	v_mfma_f32_16x16x32_bf16 v[104:107], v[140:143], v[188:191], v[104:107]
	v_mfma_f32_16x16x32_bf16 v[96:99], v[124:127], v[208:211], v[96:99]
	v_mfma_f32_16x16x32_bf16 v[88:91], v[140:143], v[208:211], v[88:91]
	v_mfma_f32_16x16x32_bf16 v[80:83], v[124:127], v[216:219], v[80:83]
	v_mfma_f32_16x16x32_bf16 v[72:75], v[140:143], v[216:219], v[72:75]
	v_mfma_f32_16x16x32_bf16 v[132:135], v[136:139], v[184:187], v[132:135]
	v_mfma_f32_16x16x32_bf16 v[128:131], v[144:147], v[184:187], v[128:131]
	v_mfma_f32_16x16x32_bf16 v[112:115], v[136:139], v[192:195], v[112:115]
	v_mfma_f32_16x16x32_bf16 v[104:107], v[144:147], v[192:195], v[104:107]
	v_mfma_f32_16x16x32_bf16 v[96:99], v[136:139], v[212:215], v[96:99]
	v_mfma_f32_16x16x32_bf16 v[88:91], v[144:147], v[212:215], v[88:91]
	v_mfma_f32_16x16x32_bf16 v[80:83], v[136:139], v[220:223], v[80:83]
	v_mfma_f32_16x16x32_bf16 v[72:75], v[144:147], v[220:223], v[72:75]
	v_mfma_f32_16x16x32_bf16 v[120:123], v[148:151], v[180:183], v[120:123]
	v_mfma_f32_16x16x32_bf16 v[116:119], v[172:175], v[180:183], v[116:119]
	v_mfma_f32_16x16x32_bf16 v[108:111], v[148:151], v[188:191], v[108:111]
	v_mfma_f32_16x16x32_bf16 v[100:103], v[172:175], v[188:191], v[100:103]
	v_mfma_f32_16x16x32_bf16 v[92:95], v[148:151], v[208:211], v[92:95]
	v_mfma_f32_16x16x32_bf16 v[84:87], v[172:175], v[208:211], v[84:87]
	v_mfma_f32_16x16x32_bf16 v[76:79], v[148:151], v[216:219], v[76:79]
	v_mfma_f32_16x16x32_bf16 v[68:71], v[172:175], v[216:219], v[68:71]
	v_mfma_f32_16x16x32_bf16 v[120:123], v[152:155], v[184:187], v[120:123]
	v_mfma_f32_16x16x32_bf16 v[116:119], v[176:179], v[184:187], v[116:119]
	v_mfma_f32_16x16x32_bf16 v[108:111], v[152:155], v[192:195], v[108:111]
	v_mfma_f32_16x16x32_bf16 v[100:103], v[176:179], v[192:195], v[100:103]
	v_mfma_f32_16x16x32_bf16 v[92:95], v[152:155], v[212:215], v[92:95]
	v_mfma_f32_16x16x32_bf16 v[84:87], v[176:179], v[212:215], v[84:87]
	v_mfma_f32_16x16x32_bf16 v[76:79], v[152:155], v[220:223], v[76:79]
	v_mfma_f32_16x16x32_bf16 v[68:71], v[176:179], v[220:223], v[68:71]
	s_barrier
	s_add_i32 s74, s74, s19
	v_lshl_add_u64 v[166:167], s[60:61], 0, v[2:3]
	s_mov_b32 m0, s74
	ds_read_b128 v[180:183], v170 offset:16384
	ds_read_b128 v[184:187], v170 offset:17408
	ds_read_b128 v[188:191], v170 offset:18432
	ds_read_b128 v[192:195], v170 offset:19456
	ds_read_b128 v[208:211], v170 offset:20480
	ds_read_b128 v[212:215], v170 offset:21504
	ds_read_b128 v[216:219], v170 offset:22528
	ds_read_b128 v[220:223], v170 offset:23552
	global_load_lds_dwordx4 v2, s[60:61]
	s_add_i32 m0, s74, 0x2000
	s_add_u32 s74, s60, 0x40000
	v_lshl_add_u64 v[204:205], s[60:61], 0, v[156:157]
	s_addc_u32 s75, s61, 0
	s_add_i32 s76, s76, s19
	global_load_lds_dwordx4 v156, s[60:61]
	s_mov_b32 m0, s76
	v_lshl_add_u64 v[224:225], s[62:63], 0, v[158:159]
	global_load_lds_dwordx4 v2, s[74:75]
	s_add_i32 m0, s76, 0x2000
	s_nop 0
	global_load_lds_dwordx4 v156, s[74:75]
	v_lshl_add_u64 v[206:207], s[62:63], 0, v[160:161]
	s_mov_b32 m0, s20
	s_nop 0
	global_load_lds_dwordx4 v160, s[62:63]
	s_mov_b32 m0, s21
	s_nop 0
	global_load_lds_dwordx4 v158, s[62:63]
	s_cmp_eq_u32 s73, 0
	s_cbranch_scc1 .Lpg8skip17
	s_waitcnt vmcnt(8)
.Lpg8skip17:
	s_waitcnt lgkmcnt(0)
	s_barrier
	s_waitcnt lgkmcnt(0)
	v_mfma_f32_16x16x32_bf16 v[64:67], v[124:127], v[180:183], v[64:67]
	v_mfma_f32_16x16x32_bf16 v[56:59], v[140:143], v[180:183], v[56:59]
	v_mfma_f32_16x16x32_bf16 v[48:51], v[124:127], v[188:191], v[48:51]
	v_mfma_f32_16x16x32_bf16 v[40:43], v[140:143], v[188:191], v[40:43]
	v_mfma_f32_16x16x32_bf16 v[32:35], v[124:127], v[208:211], v[32:35]
	v_mfma_f32_16x16x32_bf16 v[24:27], v[140:143], v[208:211], v[24:27]
	v_mfma_f32_16x16x32_bf16 v[16:19], v[124:127], v[216:219], v[16:19]
	v_mfma_f32_16x16x32_bf16 v[8:11], v[140:143], v[216:219], v[8:11]
	v_mfma_f32_16x16x32_bf16 v[64:67], v[136:139], v[184:187], v[64:67]
	v_mfma_f32_16x16x32_bf16 v[56:59], v[144:147], v[184:187], v[56:59]
	v_mfma_f32_16x16x32_bf16 v[48:51], v[136:139], v[192:195], v[48:51]
	v_mfma_f32_16x16x32_bf16 v[40:43], v[144:147], v[192:195], v[40:43]
	v_mfma_f32_16x16x32_bf16 v[32:35], v[136:139], v[212:215], v[32:35]
	v_mfma_f32_16x16x32_bf16 v[24:27], v[144:147], v[212:215], v[24:27]
	v_mfma_f32_16x16x32_bf16 v[16:19], v[136:139], v[220:223], v[16:19]
	v_mfma_f32_16x16x32_bf16 v[8:11], v[144:147], v[220:223], v[8:11]
	v_mfma_f32_16x16x32_bf16 v[60:63], v[148:151], v[180:183], v[60:63]
	v_mfma_f32_16x16x32_bf16 v[52:55], v[172:175], v[180:183], v[52:55]
	v_mfma_f32_16x16x32_bf16 v[44:47], v[148:151], v[188:191], v[44:47]
	v_mfma_f32_16x16x32_bf16 v[36:39], v[172:175], v[188:191], v[36:39]
	v_mfma_f32_16x16x32_bf16 v[28:31], v[148:151], v[208:211], v[28:31]
	v_mfma_f32_16x16x32_bf16 v[20:23], v[172:175], v[208:211], v[20:23]
	v_mfma_f32_16x16x32_bf16 v[12:15], v[148:151], v[216:219], v[12:15]
	v_mfma_f32_16x16x32_bf16 v[4:7], v[172:175], v[216:219], v[4:7]
	v_mfma_f32_16x16x32_bf16 v[60:63], v[152:155], v[184:187], v[60:63]
	v_mfma_f32_16x16x32_bf16 v[52:55], v[176:179], v[184:187], v[52:55]
	v_mfma_f32_16x16x32_bf16 v[44:47], v[152:155], v[192:195], v[44:47]
	v_mfma_f32_16x16x32_bf16 v[36:39], v[176:179], v[192:195], v[36:39]
	v_mfma_f32_16x16x32_bf16 v[28:31], v[152:155], v[212:215], v[28:31]
	v_mfma_f32_16x16x32_bf16 v[20:23], v[176:179], v[212:215], v[20:23]
	v_mfma_f32_16x16x32_bf16 v[12:15], v[152:155], v[220:223], v[12:15]
	v_mfma_f32_16x16x32_bf16 v[4:7], v[176:179], v[220:223], v[4:7]
	s_barrier
; #define PG8_STAGE(bufoff, gbase, voff) do { _Pragma("unroll") for (int _i = 0; _i < 2; ++_i) \
;         __builtin_amdgcn_global_load_lds((const unsigned*)((const char*)(gbase) + (voff)[_i]), (PG8_LAS unsigned*)(lds + (bufoff) + ldsw + _i * 8192), 16, 0, 0); } while (0)
; #define PG8_LDA(dst, b, h) do { _Pragma("unroll") for (int m = 0; m < 4; ++m) _Pragma("unroll") for (int k = 0; k < 2; ++k) dst[m][k] = *(const PG8_LAS bf16x8*)(lds + PG8_SA(b, h) + aoff + m * 2048 + k * 1024); } while (0)
; #define PG8_LDB(dst, b, h) do { _Pragma("unroll") for (int n = 0; n < 2; ++n) _Pragma("unroll") for (int k = 0; k < 2; ++k) dst[n][k] = *(const PG8_LAS bf16x8*)(lds + PG8_SB(b, h) + boff + n * 2048 + k * 1024); } while (0)
; #define PG8_WAIT_V(n) asm volatile("s_waitcnt vmcnt(" #n ")" ::: "memory")
; #define PG8_WAIT_L(n) asm volatile("s_waitcnt lgkmcnt(" #n ")" ::: "memory")
; #define PG8_BAR __builtin_amdgcn_s_barrier()
; #define PG8_SCHED __builtin_amdgcn_sched_barrier(0)
; template <class Epi, class Sched, bool ALIGN_EPI = false, bool SP2 = false, bool FP8 = false, bool ABLK = false>
; __device__ __forceinline__ void gemm_phase(PG8_LAS unsigned char* lds, const Gemm g, const Sched& S, const Epi& E) {
;     ...
;             PG8_LDB(B0, 1, 0); PG8_LDB(B1, 1, 1); PG8_SCHED; PG8_LDA(At, 1, 0); PG8_STAGE(PG8_SA(0, 1), a2 + hstepA, voffA);
;             PG8_WAIT_V(8); PG8_WAIT_L(0); PG8_BAR; PG8_MMA(0, 0, At, B0); PG8_MMA(0, 1, At, B1); PG8_BAR; PG8_SCHED;
;             PG8_LDA(At, 1, 1); PG8_STAGE(PG8_SB(1, 0), b3, voffB); PG8_STAGE(PG8_SB(1, 1), b3 + hstep, voffB); PG8_STAGE(PG8_SA(1, 0), a3, voffA);
;             PG8_WAIT_V(8); PG8_WAIT_L(0); PG8_BAR; PG8_MMA(1, 0, At, B0); PG8_MMA(1, 1, At, B1); PG8_BAR; PG8_SCHED;
;     ...
;         if constexpr (SP2) PG8_WAIT_V(0);
;         if constexpr (FP8) asm volatile("s_nop 15\n\ts_nop 15" ::: "memory");
;         if constexpr (ALIGN_EPI) { if (wr == 0) PG8_BAR; }
	s_add_i32 s74, 0, 0x18000
	s_add_i32 s75, 0, 0x1c000
	v_add_u32_e32 v144, s74, v169
	v_add_u32_e32 v171, s75, v169
	ds_read_b128 v[124:127], v144
	ds_read_b128 v[136:139], v144 offset:1024
	ds_read_b128 v[140:143], v144 offset:2048
	ds_read_b128 v[144:147], v144 offset:3072
	ds_read_b128 v[148:151], v171
	ds_read_b128 v[152:155], v171 offset:1024
	ds_read_b128 v[172:175], v171 offset:2048
	ds_read_b128 v[176:179], v171 offset:3072
	s_add_u32 s62, s62, 0x40000
	s_addc_u32 s63, s63, 0
	s_mov_b32 m0, s22
	ds_read_b128 v[180:183], v170 offset:32768
	ds_read_b128 v[184:187], v170 offset:33792
	ds_read_b128 v[188:191], v170 offset:34816
	ds_read_b128 v[192:195], v170 offset:35840
	ds_read_b128 v[208:211], v170 offset:36864
	ds_read_b128 v[212:215], v170 offset:37888
	ds_read_b128 v[216:219], v170 offset:38912
	ds_read_b128 v[220:223], v170 offset:39936
	global_load_lds_dwordx4 v160, s[62:63]
	s_mov_b32 m0, s23
	s_nop 0
	global_load_lds_dwordx4 v158, s[62:63]
	s_waitcnt vmcnt(8)
	s_waitcnt lgkmcnt(0)
	s_barrier
	s_waitcnt lgkmcnt(0)
	v_mfma_f32_16x16x32_bf16 v[132:135], v[124:127], v[180:183], v[132:135]
	v_mfma_f32_16x16x32_bf16 v[128:131], v[140:143], v[180:183], v[128:131]
	v_mfma_f32_16x16x32_bf16 v[112:115], v[124:127], v[188:191], v[112:115]
	v_mfma_f32_16x16x32_bf16 v[104:107], v[140:143], v[188:191], v[104:107]
	v_mfma_f32_16x16x32_bf16 v[96:99], v[124:127], v[208:211], v[96:99]
	v_mfma_f32_16x16x32_bf16 v[88:91], v[140:143], v[208:211], v[88:91]
	v_mfma_f32_16x16x32_bf16 v[80:83], v[124:127], v[216:219], v[80:83]
	v_mfma_f32_16x16x32_bf16 v[72:75], v[140:143], v[216:219], v[72:75]
	v_mfma_f32_16x16x32_bf16 v[132:135], v[136:139], v[184:187], v[132:135]
	v_mfma_f32_16x16x32_bf16 v[128:131], v[144:147], v[184:187], v[128:131]
	v_mfma_f32_16x16x32_bf16 v[112:115], v[136:139], v[192:195], v[112:115]
	v_mfma_f32_16x16x32_bf16 v[104:107], v[144:147], v[192:195], v[104:107]
	v_mfma_f32_16x16x32_bf16 v[96:99], v[136:139], v[212:215], v[96:99]
	v_mfma_f32_16x16x32_bf16 v[88:91], v[144:147], v[212:215], v[88:91]
	v_mfma_f32_16x16x32_bf16 v[80:83], v[136:139], v[220:223], v[80:83]
	v_mfma_f32_16x16x32_bf16 v[72:75], v[144:147], v[220:223], v[72:75]
	v_mfma_f32_16x16x32_bf16 v[120:123], v[148:151], v[180:183], v[120:123]
	v_mfma_f32_16x16x32_bf16 v[116:119], v[172:175], v[180:183], v[116:119]
	v_mfma_f32_16x16x32_bf16 v[108:111], v[148:151], v[188:191], v[108:111]
	v_mfma_f32_16x16x32_bf16 v[100:103], v[172:175], v[188:191], v[100:103]
	v_mfma_f32_16x16x32_bf16 v[92:95], v[148:151], v[208:211], v[92:95]
	v_mfma_f32_16x16x32_bf16 v[84:87], v[172:175], v[208:211], v[84:87]
	v_mfma_f32_16x16x32_bf16 v[76:79], v[148:151], v[216:219], v[76:79]
	v_mfma_f32_16x16x32_bf16 v[68:71], v[172:175], v[216:219], v[68:71]
	v_mfma_f32_16x16x32_bf16 v[120:123], v[152:155], v[184:187], v[120:123]
	v_mfma_f32_16x16x32_bf16 v[116:119], v[176:179], v[184:187], v[116:119]
	v_mfma_f32_16x16x32_bf16 v[108:111], v[152:155], v[192:195], v[108:111]
	v_mfma_f32_16x16x32_bf16 v[100:103], v[176:179], v[192:195], v[100:103]
	v_mfma_f32_16x16x32_bf16 v[92:95], v[152:155], v[212:215], v[92:95]
	v_mfma_f32_16x16x32_bf16 v[84:87], v[176:179], v[212:215], v[84:87]
	v_mfma_f32_16x16x32_bf16 v[76:79], v[152:155], v[220:223], v[76:79]
	v_mfma_f32_16x16x32_bf16 v[68:71], v[176:179], v[220:223], v[68:71]
	s_barrier
	s_add_i32 s62, s74, s19
	v_lshl_add_u64 v[166:167], v[166:167], 0, s[34:35]
	s_mov_b32 m0, s62
	ds_read_b128 v[180:183], v170 offset:49152
	ds_read_b128 v[184:187], v170 offset:50176
	ds_read_b128 v[188:191], v170 offset:51200
	ds_read_b128 v[192:195], v170 offset:52224
	ds_read_b128 v[208:211], v170 offset:53248
	ds_read_b128 v[212:215], v170 offset:54272
	ds_read_b128 v[216:219], v170 offset:55296
	ds_read_b128 v[220:223], v170 offset:56320
	global_load_lds_dwordx4 v[166:167], off
	s_add_i32 m0, s62, 0x2000
	s_add_u32 s60, s60, 0x40080
	v_lshl_add_u64 v[166:167], v[204:205], 0, s[34:35]
	s_addc_u32 s61, s61, 0
	s_add_i32 s62, s75, s19
	global_load_lds_dwordx4 v[166:167], off
	s_mov_b32 m0, s62
	s_nop 0
	global_load_lds_dwordx4 v2, s[60:61]
	s_add_i32 m0, s62, 0x2000
	s_nop 0
	global_load_lds_dwordx4 v156, s[60:61]
	v_lshl_add_u64 v[166:167], v[206:207], 0, s[34:35]
	s_mov_b32 m0, s65
	s_nop 0
	global_load_lds_dwordx4 v[166:167], off
	v_lshl_add_u64 v[166:167], v[224:225], 0, s[34:35]
	s_mov_b32 m0, s66
	s_nop 0
	global_load_lds_dwordx4 v[166:167], off
	s_waitcnt vmcnt(8)
	s_waitcnt lgkmcnt(0)
	s_barrier
	s_waitcnt lgkmcnt(0)
	v_mfma_f32_16x16x32_bf16 v[64:67], v[124:127], v[180:183], v[64:67]
	v_mfma_f32_16x16x32_bf16 v[56:59], v[140:143], v[180:183], v[56:59]
	v_mfma_f32_16x16x32_bf16 v[48:51], v[124:127], v[188:191], v[48:51]
	v_mfma_f32_16x16x32_bf16 v[40:43], v[140:143], v[188:191], v[40:43]
	v_mfma_f32_16x16x32_bf16 v[32:35], v[124:127], v[208:211], v[32:35]
	v_mfma_f32_16x16x32_bf16 v[24:27], v[140:143], v[208:211], v[24:27]
	v_mfma_f32_16x16x32_bf16 v[16:19], v[124:127], v[216:219], v[16:19]
	v_mfma_f32_16x16x32_bf16 v[8:11], v[140:143], v[216:219], v[8:11]
	v_mfma_f32_16x16x32_bf16 v[64:67], v[136:139], v[184:187], v[64:67]
	v_mfma_f32_16x16x32_bf16 v[56:59], v[144:147], v[184:187], v[56:59]
	v_mfma_f32_16x16x32_bf16 v[48:51], v[136:139], v[192:195], v[48:51]
	v_mfma_f32_16x16x32_bf16 v[40:43], v[144:147], v[192:195], v[40:43]
	v_mfma_f32_16x16x32_bf16 v[32:35], v[136:139], v[212:215], v[32:35]
	v_mfma_f32_16x16x32_bf16 v[24:27], v[144:147], v[212:215], v[24:27]
	v_mfma_f32_16x16x32_bf16 v[16:19], v[136:139], v[220:223], v[16:19]
	v_mfma_f32_16x16x32_bf16 v[8:11], v[144:147], v[220:223], v[8:11]
	v_mfma_f32_16x16x32_bf16 v[60:63], v[148:151], v[180:183], v[60:63]
	v_mfma_f32_16x16x32_bf16 v[52:55], v[172:175], v[180:183], v[52:55]
	v_mfma_f32_16x16x32_bf16 v[44:47], v[148:151], v[188:191], v[44:47]
	v_mfma_f32_16x16x32_bf16 v[36:39], v[172:175], v[188:191], v[36:39]
	v_mfma_f32_16x16x32_bf16 v[28:31], v[148:151], v[208:211], v[28:31]
	v_mfma_f32_16x16x32_bf16 v[20:23], v[172:175], v[208:211], v[20:23]
	v_mfma_f32_16x16x32_bf16 v[12:15], v[148:151], v[216:219], v[12:15]
	v_mfma_f32_16x16x32_bf16 v[4:7], v[172:175], v[216:219], v[4:7]
	v_mfma_f32_16x16x32_bf16 v[60:63], v[152:155], v[184:187], v[60:63]
	v_mfma_f32_16x16x32_bf16 v[52:55], v[176:179], v[184:187], v[52:55]
	v_mfma_f32_16x16x32_bf16 v[44:47], v[152:155], v[192:195], v[44:47]
	v_mfma_f32_16x16x32_bf16 v[36:39], v[176:179], v[192:195], v[36:39]
	v_mfma_f32_16x16x32_bf16 v[28:31], v[152:155], v[212:215], v[28:31]
	v_mfma_f32_16x16x32_bf16 v[20:23], v[176:179], v[212:215], v[20:23]
	v_mfma_f32_16x16x32_bf16 v[12:15], v[152:155], v[220:223], v[12:15]
	v_mfma_f32_16x16x32_bf16 v[4:7], v[176:179], v[220:223], v[4:7]
	s_barrier
	s_add_u32 s58, s58, 0x100
	s_addc_u32 s59, s59, 0
	s_add_u32 s71, s71, 0x100
	s_addc_u32 s72, s72, 0
	s_cmp_gt_u32 s73, 13
	s_mov_b32 s60, s73
	s_cbranch_scc0 .LBB0_1709
	s_waitcnt vmcnt(0)
	s_and_b64 vcc, exec, s[48:49]
	s_cbranch_vccz .LBB0_1712
	s_barrier

; #define PG8_STAGE(bufoff, gbase, voff) do { _Pragma("unroll") for (int _i = 0; _i < 2; ++_i) \
;         __builtin_amdgcn_global_load_lds((const unsigned*)((const char*)(gbase) + (voff)[_i]), (PG8_LAS unsigned*)(lds + (bufoff) + ldsw + _i * 8192), 16, 0, 0); } while (0)
; #define PG8_LDA(dst, b, h) do { _Pragma("unroll") for (int m = 0; m < 4; ++m) _Pragma("unroll") for (int k = 0; k < 2; ++k) dst[m][k] = *(const PG8_LAS bf16x8*)(lds + PG8_SA(b, h) + aoff + m * 2048 + k * 1024); } while (0)
; #define PG8_LDB(dst, b, h) do { _Pragma("unroll") for (int n = 0; n < 2; ++n) _Pragma("unroll") for (int k = 0; k < 2; ++k) dst[n][k] = *(const PG8_LAS bf16x8*)(lds + PG8_SB(b, h) + boff + n * 2048 + k * 1024); } while (0)
; #define PG8_WAIT_V(n) asm volatile("s_waitcnt vmcnt(" #n ")" ::: "memory")
; #define PG8_WAIT_V8_UNLESS_FIRST(t) asm volatile("s_cmp_eq_u32 %0, 0\n\ts_cbranch_scc1 .Lpg8skip%=\n\ts_waitcnt vmcnt(8)\n.Lpg8skip%=:" :: "s"(t) : "scc", "memory")
; #define PG8_WAIT_L(n) asm volatile("s_waitcnt lgkmcnt(" #n ")" ::: "memory")
; #define PG8_BAR __builtin_amdgcn_s_barrier()
; #define PG8_SCHED __builtin_amdgcn_sched_barrier(0)
; template <class Epi, class Sched, bool ALIGN_EPI = false, bool SP2 = false, bool FP8 = false, bool ABLK = false>
; __device__ __forceinline__ void gemm_phase(PG8_LAS unsigned char* lds, const Gemm g, const Sched& S, const Epi& E) {
;     ...
;             PG8_WAIT_V8_UNLESS_FIRST(t); PG8_WAIT_L(0); PG8_BAR; PG8_MMA(0, 0, At, B0); PG8_MMA(0, 1, At, B1); PG8_BAR; PG8_SCHED;
;             PG8_LDA(At, 0, 1); PG8_STAGE(PG8_SB(0, 0), b2, voffB); PG8_STAGE(PG8_SB(0, 1), b2 + hstep, voffB); PG8_STAGE(PG8_SA(0, 0), a2, voffA);
;             PG8_WAIT_V8_UNLESS_FIRST(t); PG8_WAIT_L(0); PG8_BAR; PG8_MMA(1, 0, At, B0); PG8_MMA(1, 1, At, B1); PG8_BAR; PG8_SCHED;
;             PG8_LDB(B0, 1, 0); PG8_LDB(B1, 1, 1); PG8_SCHED; PG8_LDA(At, 1, 0); PG8_STAGE(PG8_SA(0, 1), a2 + hstepA, voffA);
;             PG8_WAIT_V(8); PG8_WAIT_L(0); PG8_BAR; PG8_MMA(0, 0, At, B0); PG8_MMA(0, 1, At, B1); PG8_BAR; PG8_SCHED;
.Lpg8skip18:
	s_waitcnt lgkmcnt(0)
	s_barrier
	s_waitcnt lgkmcnt(0)
	v_mfma_scale_f32_16x16x128_f8f6f4 v[160:163], v[28:35], v[186:193], v[160:163], v245, v245 op_sel_hi:[0,0,0]
	v_mfma_scale_f32_16x16x128_f8f6f4 v[156:159], v[20:27], v[186:193], v[156:159], v245, v245 op_sel_hi:[0,0,0]
	v_mfma_scale_f32_16x16x128_f8f6f4 v[144:147], v[28:35], v[208:215], v[144:147], v245, v245 op_sel_hi:[0,0,0]
	v_mfma_scale_f32_16x16x128_f8f6f4 v[140:143], v[20:27], v[208:215], v[140:143], v245, v245 op_sel_hi:[0,0,0]
	v_mfma_scale_f32_16x16x128_f8f6f4 v[128:131], v[28:35], v[216:223], v[128:131], v245, v245 op_sel_hi:[0,0,0]
	v_mfma_scale_f32_16x16x128_f8f6f4 v[124:127], v[20:27], v[216:223], v[124:127], v245, v245 op_sel_hi:[0,0,0]
	v_mfma_scale_f32_16x16x128_f8f6f4 v[112:115], v[28:35], v[228:235], v[112:115], v245, v245 op_sel_hi:[0,0,0]
	v_mfma_scale_f32_16x16x128_f8f6f4 v[108:111], v[20:27], v[228:235], v[108:111], v245, v245 op_sel_hi:[0,0,0]
	v_mfma_scale_f32_16x16x128_f8f6f4 v[152:155], v[12:19], v[186:193], v[152:155], v245, v245 op_sel_hi:[0,0,0]
	v_mfma_scale_f32_16x16x128_f8f6f4 v[148:151], v[4:11], v[186:193], v[148:151], v245, v245 op_sel_hi:[0,0,0]
	v_mfma_scale_f32_16x16x128_f8f6f4 v[136:139], v[12:19], v[208:215], v[136:139], v245, v245 op_sel_hi:[0,0,0]
	v_mfma_scale_f32_16x16x128_f8f6f4 v[132:135], v[4:11], v[208:215], v[132:135], v245, v245 op_sel_hi:[0,0,0]
	v_mfma_scale_f32_16x16x128_f8f6f4 v[120:123], v[12:19], v[216:223], v[120:123], v245, v245 op_sel_hi:[0,0,0]
	v_mfma_scale_f32_16x16x128_f8f6f4 v[116:119], v[4:11], v[216:223], v[116:119], v245, v245 op_sel_hi:[0,0,0]
	v_mfma_scale_f32_16x16x128_f8f6f4 v[104:107], v[12:19], v[228:235], v[104:107], v245, v245 op_sel_hi:[0,0,0]
	v_mfma_scale_f32_16x16x128_f8f6f4 v[100:103], v[4:11], v[228:235], v[100:103], v245, v245 op_sel_hi:[0,0,0]
	s_barrier
	s_add_i32 s72, s72, s17
	v_lshl_add_u64 v[178:179], s[58:59], 0, v[2:3]
	s_mov_b32 m0, s72
	ds_read_b128 v[186:189], v184 offset:16384
	ds_read_b128 v[190:193], v184 offset:17408
	ds_read_b128 v[208:211], v184 offset:18432
	ds_read_b128 v[212:215], v184 offset:19456
	ds_read_b128 v[216:219], v184 offset:20480
	ds_read_b128 v[220:223], v184 offset:21504
	ds_read_b128 v[228:231], v184 offset:22528
	ds_read_b128 v[232:235], v184 offset:23552
	global_load_lds_dwordx4 v2, s[58:59]
	s_add_i32 m0, s72, 0x2000
	s_add_u32 s72, s58, 0x58000
	v_lshl_add_u64 v[180:181], s[58:59], 0, v[164:165]
	s_addc_u32 s73, s59, 0
	s_add_i32 s71, s71, s17
	global_load_lds_dwordx4 v164, s[58:59]
	s_mov_b32 m0, s71
	v_lshl_add_u64 v[204:205], s[60:61], 0, v[166:167]
	global_load_lds_dwordx4 v2, s[72:73]
	s_add_i32 m0, s71, 0x2000
	s_nop 0
	global_load_lds_dwordx4 v164, s[72:73]
	v_lshl_add_u64 v[194:195], s[60:61], 0, v[168:169]
	s_mov_b32 m0, s18
	s_nop 0
	global_load_lds_dwordx4 v168, s[60:61]
	s_mov_b32 m0, s19
	s_nop 0
	global_load_lds_dwordx4 v166, s[60:61]
	s_cmp_eq_u32 s70, 0
	s_cbranch_scc1 .Lpg8skip19
	s_waitcnt vmcnt(8)
.Lpg8skip19:
	s_waitcnt lgkmcnt(0)
	s_barrier
	s_waitcnt lgkmcnt(0)
	v_mfma_scale_f32_16x16x128_f8f6f4 v[96:99], v[28:35], v[186:193], v[96:99], v245, v245 op_sel_hi:[0,0,0]
	v_mfma_scale_f32_16x16x128_f8f6f4 v[92:95], v[20:27], v[186:193], v[92:95], v245, v245 op_sel_hi:[0,0,0]
	v_mfma_scale_f32_16x16x128_f8f6f4 v[80:83], v[28:35], v[208:215], v[80:83], v245, v245 op_sel_hi:[0,0,0]
	v_mfma_scale_f32_16x16x128_f8f6f4 v[76:79], v[20:27], v[208:215], v[76:79], v245, v245 op_sel_hi:[0,0,0]
	v_mfma_scale_f32_16x16x128_f8f6f4 v[64:67], v[28:35], v[216:223], v[64:67], v245, v245 op_sel_hi:[0,0,0]
	v_mfma_scale_f32_16x16x128_f8f6f4 v[60:63], v[20:27], v[216:223], v[60:63], v245, v245 op_sel_hi:[0,0,0]
	v_mfma_scale_f32_16x16x128_f8f6f4 v[48:51], v[28:35], v[228:235], v[48:51], v245, v245 op_sel_hi:[0,0,0]
	v_mfma_scale_f32_16x16x128_f8f6f4 v[44:47], v[20:27], v[228:235], v[44:47], v245, v245 op_sel_hi:[0,0,0]
	v_mfma_scale_f32_16x16x128_f8f6f4 v[88:91], v[12:19], v[186:193], v[88:91], v245, v245 op_sel_hi:[0,0,0]
	v_mfma_scale_f32_16x16x128_f8f6f4 v[84:87], v[4:11], v[186:193], v[84:87], v245, v245 op_sel_hi:[0,0,0]
	v_mfma_scale_f32_16x16x128_f8f6f4 v[72:75], v[12:19], v[208:215], v[72:75], v245, v245 op_sel_hi:[0,0,0]
	v_mfma_scale_f32_16x16x128_f8f6f4 v[68:71], v[4:11], v[208:215], v[68:71], v245, v245 op_sel_hi:[0,0,0]
	v_mfma_scale_f32_16x16x128_f8f6f4 v[56:59], v[12:19], v[216:223], v[56:59], v245, v245 op_sel_hi:[0,0,0]
	v_mfma_scale_f32_16x16x128_f8f6f4 v[52:55], v[4:11], v[216:223], v[52:55], v245, v245 op_sel_hi:[0,0,0]
	v_mfma_scale_f32_16x16x128_f8f6f4 v[40:43], v[12:19], v[228:235], v[40:43], v245, v245 op_sel_hi:[0,0,0]
	v_mfma_scale_f32_16x16x128_f8f6f4 v[36:39], v[4:11], v[228:235], v[36:39], v245, v245 op_sel_hi:[0,0,0]
	s_barrier
	s_add_i32 s60, 0, 0x18000
	s_add_i32 s61, 0, 0x1c000
	v_add_u32_e32 v16, s60, v183
	v_add_u32_e32 v32, s61, v183
	ds_read_b128 v[4:7], v16
	ds_read_b128 v[8:11], v16 offset:1024
	ds_read_b128 v[12:15], v16 offset:2048
	ds_read_b128 v[16:19], v16 offset:3072
	ds_read_b128 v[20:23], v32
	ds_read_b128 v[24:27], v32 offset:1024
	ds_read_b128 v[28:31], v32 offset:2048
	ds_read_b128 v[32:35], v32 offset:3072
	s_mov_b32 m0, s20
	v_lshl_add_u64 v[194:195], v[194:195], 0, s[24:25]
	ds_read_b128 v[186:189], v184 offset:32768
	ds_read_b128 v[190:193], v184 offset:33792
	ds_read_b128 v[208:211], v184 offset:34816
	ds_read_b128 v[212:215], v184 offset:35840
	ds_read_b128 v[216:219], v184 offset:36864
	ds_read_b128 v[220:223], v184 offset:37888
	ds_read_b128 v[228:231], v184 offset:38912
	ds_read_b128 v[232:235], v184 offset:39936
	global_load_lds_dwordx4 v[194:195], off
	v_lshl_add_u64 v[194:195], v[204:205], 0, s[24:25]
	s_mov_b32 m0, s21
	s_nop 0
	global_load_lds_dwordx4 v[194:195], off
	s_waitcnt vmcnt(8)
	s_waitcnt lgkmcnt(0)
	s_barrier
; #define PG8_STAGE(bufoff, gbase, voff) do { _Pragma("unroll") for (int _i = 0; _i < 2; ++_i) \
;         __builtin_amdgcn_global_load_lds((const unsigned*)((const char*)(gbase) + (voff)[_i]), (PG8_LAS unsigned*)(lds + (bufoff) + ldsw + _i * 8192), 16, 0, 0); } while (0)
; #define PG8_LDA(dst, b, h) do { _Pragma("unroll") for (int m = 0; m < 4; ++m) _Pragma("unroll") for (int k = 0; k < 2; ++k) dst[m][k] = *(const PG8_LAS bf16x8*)(lds + PG8_SA(b, h) + aoff + m * 2048 + k * 1024); } while (0)
; #define PG8_WAIT_V(n) asm volatile("s_waitcnt vmcnt(" #n ")" ::: "memory")
; #define PG8_WAIT_L(n) asm volatile("s_waitcnt lgkmcnt(" #n ")" ::: "memory")
; #define PG8_BAR __builtin_amdgcn_s_barrier()
; #define PG8_SCHED __builtin_amdgcn_sched_barrier(0)
; template <class Epi, class Sched, bool ALIGN_EPI = false, bool SP2 = false, bool FP8 = false, bool ABLK = false>
; __device__ __forceinline__ void gemm_phase(PG8_LAS unsigned char* lds, const Gemm g, const Sched& S, const Epi& E) {
;     ...
;             PG8_WAIT_V(8); PG8_WAIT_L(0); PG8_BAR; PG8_MMA(0, 0, At, B0); PG8_MMA(0, 1, At, B1); PG8_BAR; PG8_SCHED;
;             PG8_LDA(At, 1, 1); PG8_STAGE(PG8_SB(1, 0), b3, voffB); PG8_STAGE(PG8_SB(1, 1), b3 + hstep, voffB); PG8_STAGE(PG8_SA(1, 0), a3, voffA);
;             PG8_WAIT_V(8); PG8_WAIT_L(0); PG8_BAR; PG8_MMA(1, 0, At, B0); PG8_MMA(1, 1, At, B1); PG8_BAR; PG8_SCHED;
;     ...
;         if constexpr (SP2) PG8_WAIT_V(0);
;         if constexpr (FP8) asm volatile("s_nop 15\n\ts_nop 15" ::: "memory");
;         if constexpr (ALIGN_EPI) { if (wr == 0) PG8_BAR; }
	s_waitcnt lgkmcnt(0)
	v_mfma_scale_f32_16x16x128_f8f6f4 v[160:163], v[4:11], v[186:193], v[160:163], v245, v245 op_sel_hi:[0,0,0]
	v_mfma_scale_f32_16x16x128_f8f6f4 v[156:159], v[12:19], v[186:193], v[156:159], v245, v245 op_sel_hi:[0,0,0]
	v_mfma_scale_f32_16x16x128_f8f6f4 v[144:147], v[4:11], v[208:215], v[144:147], v245, v245 op_sel_hi:[0,0,0]
	v_mfma_scale_f32_16x16x128_f8f6f4 v[140:143], v[12:19], v[208:215], v[140:143], v245, v245 op_sel_hi:[0,0,0]
	v_mfma_scale_f32_16x16x128_f8f6f4 v[128:131], v[4:11], v[216:223], v[128:131], v245, v245 op_sel_hi:[0,0,0]
	v_mfma_scale_f32_16x16x128_f8f6f4 v[124:127], v[12:19], v[216:223], v[124:127], v245, v245 op_sel_hi:[0,0,0]
	v_mfma_scale_f32_16x16x128_f8f6f4 v[112:115], v[4:11], v[228:235], v[112:115], v245, v245 op_sel_hi:[0,0,0]
	v_mfma_scale_f32_16x16x128_f8f6f4 v[108:111], v[12:19], v[228:235], v[108:111], v245, v245 op_sel_hi:[0,0,0]
	v_mfma_scale_f32_16x16x128_f8f6f4 v[152:155], v[20:27], v[186:193], v[152:155], v245, v245 op_sel_hi:[0,0,0]
	v_mfma_scale_f32_16x16x128_f8f6f4 v[148:151], v[28:35], v[186:193], v[148:151], v245, v245 op_sel_hi:[0,0,0]
	v_mfma_scale_f32_16x16x128_f8f6f4 v[136:139], v[20:27], v[208:215], v[136:139], v245, v245 op_sel_hi:[0,0,0]
	v_mfma_scale_f32_16x16x128_f8f6f4 v[132:135], v[28:35], v[208:215], v[132:135], v245, v245 op_sel_hi:[0,0,0]
	v_mfma_scale_f32_16x16x128_f8f6f4 v[120:123], v[20:27], v[216:223], v[120:123], v245, v245 op_sel_hi:[0,0,0]
	v_mfma_scale_f32_16x16x128_f8f6f4 v[116:119], v[28:35], v[216:223], v[116:119], v245, v245 op_sel_hi:[0,0,0]
	v_mfma_scale_f32_16x16x128_f8f6f4 v[104:107], v[20:27], v[228:235], v[104:107], v245, v245 op_sel_hi:[0,0,0]
	v_mfma_scale_f32_16x16x128_f8f6f4 v[100:103], v[28:35], v[228:235], v[100:103], v245, v245 op_sel_hi:[0,0,0]
	s_barrier
	s_add_i32 s60, s60, s17
	v_lshl_add_u64 v[178:179], v[178:179], 0, s[34:35]
	s_mov_b32 m0, s60
	ds_read_b128 v[186:189], v184 offset:49152
	ds_read_b128 v[190:193], v184 offset:50176
	ds_read_b128 v[208:211], v184 offset:51200
	ds_read_b128 v[212:215], v184 offset:52224
	ds_read_b128 v[216:219], v184 offset:53248
	ds_read_b128 v[220:223], v184 offset:54272
	ds_read_b128 v[228:231], v184 offset:55296
	ds_read_b128 v[232:235], v184 offset:56320
	global_load_lds_dwordx4 v[178:179], off
	s_add_i32 m0, s60, 0x2000
	s_add_u32 s58, s58, 0x58080
	v_lshl_add_u64 v[178:179], v[180:181], 0, s[34:35]
	s_addc_u32 s59, s59, 0
	s_add_i32 s60, s61, s17
	global_load_lds_dwordx4 v[178:179], off
	s_mov_b32 m0, s60
	s_nop 0
	global_load_lds_dwordx4 v2, s[58:59]
	s_add_i32 m0, s60, 0x2000
	s_nop 0
	global_load_lds_dwordx4 v164, s[58:59]
	s_mov_b32 m0, s63
	s_nop 0
	global_load_lds_dwordx4 v168, s[56:57]
	s_mov_b32 m0, s64
	s_nop 0
	global_load_lds_dwordx4 v166, s[56:57]
	s_waitcnt vmcnt(8)
	s_waitcnt lgkmcnt(0)
	s_barrier
	s_waitcnt lgkmcnt(0)
	v_mfma_scale_f32_16x16x128_f8f6f4 v[96:99], v[4:11], v[186:193], v[96:99], v245, v245 op_sel_hi:[0,0,0]
	v_mfma_scale_f32_16x16x128_f8f6f4 v[92:95], v[12:19], v[186:193], v[92:95], v245, v245 op_sel_hi:[0,0,0]
	v_mfma_scale_f32_16x16x128_f8f6f4 v[80:83], v[4:11], v[208:215], v[80:83], v245, v245 op_sel_hi:[0,0,0]
	v_mfma_scale_f32_16x16x128_f8f6f4 v[76:79], v[12:19], v[208:215], v[76:79], v245, v245 op_sel_hi:[0,0,0]
	v_mfma_scale_f32_16x16x128_f8f6f4 v[64:67], v[4:11], v[216:223], v[64:67], v245, v245 op_sel_hi:[0,0,0]
	v_mfma_scale_f32_16x16x128_f8f6f4 v[60:63], v[12:19], v[216:223], v[60:63], v245, v245 op_sel_hi:[0,0,0]
	v_mfma_scale_f32_16x16x128_f8f6f4 v[48:51], v[4:11], v[228:235], v[48:51], v245, v245 op_sel_hi:[0,0,0]
	v_mfma_scale_f32_16x16x128_f8f6f4 v[44:47], v[12:19], v[228:235], v[44:47], v245, v245 op_sel_hi:[0,0,0]
	v_mfma_scale_f32_16x16x128_f8f6f4 v[88:91], v[20:27], v[186:193], v[88:91], v245, v245 op_sel_hi:[0,0,0]
	v_mfma_scale_f32_16x16x128_f8f6f4 v[84:87], v[28:35], v[186:193], v[84:87], v245, v245 op_sel_hi:[0,0,0]
	v_mfma_scale_f32_16x16x128_f8f6f4 v[72:75], v[20:27], v[208:215], v[72:75], v245, v245 op_sel_hi:[0,0,0]
	v_mfma_scale_f32_16x16x128_f8f6f4 v[68:71], v[28:35], v[208:215], v[68:71], v245, v245 op_sel_hi:[0,0,0]
	v_mfma_scale_f32_16x16x128_f8f6f4 v[56:59], v[20:27], v[216:223], v[56:59], v245, v245 op_sel_hi:[0,0,0]
	v_mfma_scale_f32_16x16x128_f8f6f4 v[52:55], v[28:35], v[216:223], v[52:55], v245, v245 op_sel_hi:[0,0,0]
	v_mfma_scale_f32_16x16x128_f8f6f4 v[40:43], v[20:27], v[228:235], v[40:43], v245, v245 op_sel_hi:[0,0,0]
	v_mfma_scale_f32_16x16x128_f8f6f4 v[36:39], v[28:35], v[228:235], v[36:39], v245, v245 op_sel_hi:[0,0,0]
	s_barrier
	s_add_u32 s4, s4, 0x100
	s_addc_u32 s5, s5, 0
	s_add_u32 s54, s54, 0x10000
	s_addc_u32 s55, s55, 0
	s_cmp_gt_u32 s70, 19
	s_cbranch_scc0 .LBB0_1831
	s_waitcnt vmcnt(0)
	s_nop 15
	s_nop 15
	s_and_b64 vcc, exec, s[48:49]
	s_cbranch_vccz .LBB0_1834
	s_barrier
